# NSA QK^T K-fragment ds_reads software-pipelined through 10 free VGPR quads (counted lgkmcnt), bit-identical math
# speedup vs baseline: 1.0052x; 1.0052x over previous
.LBB0_1651:
	ds_read_b128 v[212:215], v39 offset:32768
	ds_read_b128 v[216:219], v40 offset:32768
	ds_read_b128 v[220:223], v39 offset:40960
	ds_read_b128 v[224:227], v40 offset:40960
	ds_read_b128 v[228:231], v41 offset:32768
	ds_read_b128 v[232:235], v41 offset:40960
	ds_read_b128 v[236:239], v42 offset:32768
	ds_read_b128 v[240:243], v42 offset:40960
	ds_read_b128 v[244:247], v39 offset:32896
	ds_read_b128 v[248:251], v39 offset:41088
	v_cmp_lt_i32_e32 vcc, 63, v43
	s_cmp_eq_u64 vcc, exec
	s_waitcnt lgkmcnt(9)
	v_mfma_f32_32x32x16_bf16 v[20:35], v[212:215], v[136:139], 0
	ds_read_b128 v[212:215], v40 offset:32896
	s_waitcnt lgkmcnt(9)
	v_mfma_f32_32x32x16_bf16 v[20:35], v[216:219], v[112:115], v[20:35]
	ds_read_b128 v[216:219], v40 offset:41088
	s_waitcnt lgkmcnt(9)
	v_mfma_f32_32x32x16_bf16 v[4:19], v[220:223], v[136:139], 0
	ds_read_b128 v[220:223], v41 offset:32896
	s_waitcnt lgkmcnt(9)
	v_mfma_f32_32x32x16_bf16 v[4:19], v[224:227], v[112:115], v[4:19]
	ds_read_b128 v[224:227], v41 offset:41088
	s_waitcnt lgkmcnt(9)
	v_mfma_f32_32x32x16_bf16 v[20:35], v[228:231], v[116:119], v[20:35]
	ds_read_b128 v[228:231], v42 offset:32896
	s_waitcnt lgkmcnt(9)
	v_mfma_f32_32x32x16_bf16 v[4:19], v[232:235], v[116:119], v[4:19]
	ds_read_b128 v[232:235], v42 offset:41088
	s_waitcnt lgkmcnt(9)
	v_mfma_f32_32x32x16_bf16 v[20:35], v[236:239], v[124:127], v[20:35]
	s_waitcnt lgkmcnt(8)
	v_mfma_f32_32x32x16_bf16 v[4:19], v[240:243], v[124:127], v[4:19]
	s_waitcnt lgkmcnt(7)
	v_mfma_f32_32x32x16_bf16 v[20:35], v[244:247], v[140:143], v[20:35]
	s_waitcnt lgkmcnt(6)
	v_mfma_f32_32x32x16_bf16 v[4:19], v[248:251], v[140:143], v[4:19]
	s_waitcnt lgkmcnt(5)
	v_mfma_f32_32x32x16_bf16 v[20:35], v[212:215], v[132:135], v[20:35]
	s_waitcnt lgkmcnt(4)
	v_mfma_f32_32x32x16_bf16 v[4:19], v[216:219], v[132:135], v[4:19]
	s_waitcnt lgkmcnt(3)
	v_mfma_f32_32x32x16_bf16 v[20:35], v[220:223], v[120:123], v[20:35]
	s_waitcnt lgkmcnt(2)
	v_mfma_f32_32x32x16_bf16 v[4:19], v[224:227], v[120:123], v[4:19]
	s_waitcnt lgkmcnt(1)
	v_mfma_f32_32x32x16_bf16 v[20:35], v[228:231], v[128:131], v[20:35]
	s_waitcnt lgkmcnt(0)
	s_nop 0
	v_mfma_f32_32x32x16_bf16 v[4:19], v[232:235], v[128:131], v[4:19]
	s_cbranch_scc1 .LBB0_1653
	v_add_u32_e32 v2, v38, v43
	v_cmp_lt_i32_e32 vcc, 0, v2
	s_nop 5
	v_cndmask_b32_e32 v20, v168, v20, vcc
	v_cmp_lt_i32_e32 vcc, 32, v2
	s_nop 1
	v_cndmask_b32_e32 v4, v168, v4, vcc
	v_cmp_lt_i32_e32 vcc, 1, v2
	s_nop 1
	v_cndmask_b32_e32 v21, v168, v21, vcc
	v_cmp_lt_i32_e32 vcc, 33, v2
	s_nop 1
	v_cndmask_b32_e32 v5, v168, v5, vcc
	v_cmp_lt_i32_e32 vcc, 2, v2
	s_nop 1
	v_cndmask_b32_e32 v22, v168, v22, vcc
	v_cmp_lt_i32_e32 vcc, 34, v2
	s_nop 1
	v_cndmask_b32_e32 v6, v168, v6, vcc
	v_cmp_lt_i32_e32 vcc, 3, v2
	s_nop 1
	v_cndmask_b32_e32 v23, v168, v23, vcc
	v_cmp_lt_i32_e32 vcc, 35, v2
	s_nop 1
	v_cndmask_b32_e32 v7, v168, v7, vcc
	v_cmp_lt_i32_e32 vcc, 8, v2
	s_nop 1
	v_cndmask_b32_e32 v24, v168, v24, vcc
	v_cmp_lt_i32_e32 vcc, 40, v2
	s_nop 1
	v_cndmask_b32_e32 v8, v168, v8, vcc
	v_cmp_lt_i32_e32 vcc, 9, v2
	s_nop 1
	v_cndmask_b32_e32 v25, v168, v25, vcc
	v_cmp_lt_i32_e32 vcc, 41, v2
	s_nop 1
	v_cndmask_b32_e32 v9, v168, v9, vcc
	v_cmp_lt_i32_e32 vcc, 10, v2
	s_nop 1
	v_cndmask_b32_e32 v26, v168, v26, vcc
	v_cmp_lt_i32_e32 vcc, 42, v2
	s_nop 1
	v_cndmask_b32_e32 v10, v168, v10, vcc
	v_cmp_lt_i32_e32 vcc, 11, v2
	s_nop 1
	v_cndmask_b32_e32 v27, v168, v27, vcc
	v_cmp_lt_i32_e32 vcc, 43, v2
	s_nop 1
	v_cndmask_b32_e32 v11, v168, v11, vcc
	v_cmp_lt_i32_e32 vcc, 16, v2
	s_nop 1
	v_cndmask_b32_e32 v28, v168, v28, vcc
	v_cmp_lt_i32_e32 vcc, 48, v2
	s_nop 1
	v_cndmask_b32_e32 v12, v168, v12, vcc
	v_cmp_lt_i32_e32 vcc, 17, v2
	s_nop 1
	v_cndmask_b32_e32 v29, v168, v29, vcc
	v_cmp_lt_i32_e32 vcc, 49, v2
	s_nop 1
	v_cndmask_b32_e32 v13, v168, v13, vcc
	v_cmp_lt_i32_e32 vcc, 18, v2
	s_nop 1
	v_cndmask_b32_e32 v30, v168, v30, vcc
	v_cmp_lt_i32_e32 vcc, 50, v2
	s_nop 1
	v_cndmask_b32_e32 v14, v168, v14, vcc
	v_cmp_lt_i32_e32 vcc, 19, v2
	s_nop 1
	v_cndmask_b32_e32 v31, v168, v31, vcc
	v_cmp_lt_i32_e32 vcc, 51, v2
	s_nop 1
	v_cndmask_b32_e32 v15, v168, v15, vcc
	v_cmp_lt_i32_e32 vcc, 24, v2
	s_nop 1
	v_cndmask_b32_e32 v32, v168, v32, vcc
	v_cmp_lt_i32_e32 vcc, 56, v2
	s_nop 1
	v_cndmask_b32_e32 v16, v168, v16, vcc
	v_cmp_lt_i32_e32 vcc, 25, v2
	s_nop 1
	v_cndmask_b32_e32 v33, v168, v33, vcc
	v_cmp_lt_i32_e32 vcc, 57, v2
	s_nop 1
	v_cndmask_b32_e32 v17, v168, v17, vcc
	v_cmp_lt_i32_e32 vcc, 26, v2
	s_nop 1
	v_cndmask_b32_e32 v34, v168, v34, vcc
	v_cmp_lt_i32_e32 vcc, 58, v2
	s_nop 1
	v_cndmask_b32_e32 v18, v168, v18, vcc
	v_cmp_lt_i32_e32 vcc, 27, v2
	s_nop 1
	v_cndmask_b32_e32 v35, v168, v35, vcc
	v_cmp_lt_i32_e32 vcc, 59, v2
	s_nop 1
	v_cndmask_b32_e32 v19, v168, v19, vcc

.LBB0_1656:
	ds_read_b128 v[212:215], v39 offset:49152
	ds_read_b128 v[216:219], v40 offset:49152
	ds_read_b128 v[220:223], v39 offset:57344
	ds_read_b128 v[224:227], v40 offset:57344
	ds_read_b128 v[228:231], v41 offset:49152
	ds_read_b128 v[232:235], v41 offset:57344
	ds_read_b128 v[236:239], v42 offset:49152
	ds_read_b128 v[240:243], v42 offset:57344
	ds_read_b128 v[244:247], v39 offset:49280
	ds_read_b128 v[248:251], v39 offset:57472
	v_subrev_u32_e32 v2, 64, v43
	v_cmp_lt_i32_e32 vcc, 63, v2
	s_cmp_eq_u64 vcc, exec
	s_waitcnt lgkmcnt(9)
	v_mfma_f32_32x32x16_bf16 v[20:35], v[212:215], v[136:139], 0
	ds_read_b128 v[212:215], v40 offset:49280
	s_waitcnt lgkmcnt(9)
	v_mfma_f32_32x32x16_bf16 v[20:35], v[216:219], v[112:115], v[20:35]
	ds_read_b128 v[216:219], v40 offset:57472
	s_waitcnt lgkmcnt(9)
	v_mfma_f32_32x32x16_bf16 v[4:19], v[220:223], v[136:139], 0
	ds_read_b128 v[220:223], v41 offset:49280
	s_waitcnt lgkmcnt(9)
	v_mfma_f32_32x32x16_bf16 v[4:19], v[224:227], v[112:115], v[4:19]
	ds_read_b128 v[224:227], v41 offset:57472
	s_waitcnt lgkmcnt(9)
	v_mfma_f32_32x32x16_bf16 v[20:35], v[228:231], v[116:119], v[20:35]
	ds_read_b128 v[228:231], v42 offset:49280
	s_waitcnt lgkmcnt(9)
	v_mfma_f32_32x32x16_bf16 v[4:19], v[232:235], v[116:119], v[4:19]
	ds_read_b128 v[232:235], v42 offset:57472
	s_waitcnt lgkmcnt(9)
	v_mfma_f32_32x32x16_bf16 v[20:35], v[236:239], v[124:127], v[20:35]
	s_waitcnt lgkmcnt(8)
	v_mfma_f32_32x32x16_bf16 v[4:19], v[240:243], v[124:127], v[4:19]
	s_waitcnt lgkmcnt(7)
	v_mfma_f32_32x32x16_bf16 v[20:35], v[244:247], v[140:143], v[20:35]
	s_waitcnt lgkmcnt(6)
	v_mfma_f32_32x32x16_bf16 v[4:19], v[248:251], v[140:143], v[4:19]
	s_waitcnt lgkmcnt(5)
	v_mfma_f32_32x32x16_bf16 v[20:35], v[212:215], v[132:135], v[20:35]
	s_waitcnt lgkmcnt(4)
	v_mfma_f32_32x32x16_bf16 v[4:19], v[216:219], v[132:135], v[4:19]
	s_waitcnt lgkmcnt(3)
	v_mfma_f32_32x32x16_bf16 v[20:35], v[220:223], v[120:123], v[20:35]
	s_waitcnt lgkmcnt(2)
	v_mfma_f32_32x32x16_bf16 v[4:19], v[224:227], v[120:123], v[4:19]
	s_waitcnt lgkmcnt(1)
	v_mfma_f32_32x32x16_bf16 v[20:35], v[228:231], v[128:131], v[20:35]
	s_waitcnt lgkmcnt(0)
	s_nop 0
	v_mfma_f32_32x32x16_bf16 v[4:19], v[232:235], v[128:131], v[4:19]
	s_cbranch_scc1 .LBB0_1658
	v_add3_u32 v2, v38, v43, s38
	v_cmp_lt_i32_e32 vcc, 0, v2
	s_nop 5
	v_cndmask_b32_e32 v20, v168, v20, vcc
	v_cmp_lt_i32_e32 vcc, 32, v2
	s_nop 1
	v_cndmask_b32_e32 v4, v168, v4, vcc
	v_cmp_lt_i32_e32 vcc, 1, v2
	s_nop 1
	v_cndmask_b32_e32 v21, v168, v21, vcc
	v_cmp_lt_i32_e32 vcc, 33, v2
	s_nop 1
	v_cndmask_b32_e32 v5, v168, v5, vcc
	v_cmp_lt_i32_e32 vcc, 2, v2
	s_nop 1
	v_cndmask_b32_e32 v22, v168, v22, vcc
	v_cmp_lt_i32_e32 vcc, 34, v2
	s_nop 1
	v_cndmask_b32_e32 v6, v168, v6, vcc
	v_cmp_lt_i32_e32 vcc, 3, v2
	s_nop 1
	v_cndmask_b32_e32 v23, v168, v23, vcc
	v_cmp_lt_i32_e32 vcc, 35, v2
	s_nop 1
	v_cndmask_b32_e32 v7, v168, v7, vcc
	v_cmp_lt_i32_e32 vcc, 8, v2
	s_nop 1
	v_cndmask_b32_e32 v24, v168, v24, vcc
	v_cmp_lt_i32_e32 vcc, 40, v2
	s_nop 1
	v_cndmask_b32_e32 v8, v168, v8, vcc
	v_cmp_lt_i32_e32 vcc, 9, v2
	s_nop 1
	v_cndmask_b32_e32 v25, v168, v25, vcc
	v_cmp_lt_i32_e32 vcc, 41, v2
	s_nop 1
	v_cndmask_b32_e32 v9, v168, v9, vcc
	v_cmp_lt_i32_e32 vcc, 10, v2
	s_nop 1
	v_cndmask_b32_e32 v26, v168, v26, vcc
	v_cmp_lt_i32_e32 vcc, 42, v2
	s_nop 1
	v_cndmask_b32_e32 v10, v168, v10, vcc
	v_cmp_lt_i32_e32 vcc, 11, v2
	s_nop 1
	v_cndmask_b32_e32 v27, v168, v27, vcc
	v_cmp_lt_i32_e32 vcc, 43, v2
	s_nop 1
	v_cndmask_b32_e32 v11, v168, v11, vcc
	v_cmp_lt_i32_e32 vcc, 16, v2
	s_nop 1
	v_cndmask_b32_e32 v28, v168, v28, vcc
	v_cmp_lt_i32_e32 vcc, 48, v2
	s_nop 1
	v_cndmask_b32_e32 v12, v168, v12, vcc
	v_cmp_lt_i32_e32 vcc, 17, v2
	s_nop 1
	v_cndmask_b32_e32 v29, v168, v29, vcc
	v_cmp_lt_i32_e32 vcc, 49, v2
	s_nop 1
	v_cndmask_b32_e32 v13, v168, v13, vcc
	v_cmp_lt_i32_e32 vcc, 18, v2
	s_nop 1
	v_cndmask_b32_e32 v30, v168, v30, vcc
	v_cmp_lt_i32_e32 vcc, 50, v2
	s_nop 1
	v_cndmask_b32_e32 v14, v168, v14, vcc
	v_cmp_lt_i32_e32 vcc, 19, v2
	s_nop 1
	v_cndmask_b32_e32 v31, v168, v31, vcc
	v_cmp_lt_i32_e32 vcc, 51, v2
	s_nop 1
	v_cndmask_b32_e32 v15, v168, v15, vcc
	v_cmp_lt_i32_e32 vcc, 24, v2
	s_nop 1
	v_cndmask_b32_e32 v32, v168, v32, vcc
	v_cmp_lt_i32_e32 vcc, 56, v2
	s_nop 1
	v_cndmask_b32_e32 v16, v168, v16, vcc
	v_cmp_lt_i32_e32 vcc, 25, v2
	s_nop 1
	v_cndmask_b32_e32 v33, v168, v33, vcc
	v_cmp_lt_i32_e32 vcc, 57, v2
	s_nop 1
	v_cndmask_b32_e32 v17, v168, v17, vcc
	v_cmp_lt_i32_e32 vcc, 26, v2
	s_nop 1
	v_cndmask_b32_e32 v34, v168, v34, vcc
	v_cmp_lt_i32_e32 vcc, 58, v2
	s_nop 1
	v_cndmask_b32_e32 v18, v168, v18, vcc
	v_cmp_lt_i32_e32 vcc, 27, v2
	s_nop 1
	v_cndmask_b32_e32 v35, v168, v35, vcc
	v_cmp_lt_i32_e32 vcc, 59, v2
	s_nop 1
	v_cndmask_b32_e32 v19, v168, v19, vcc

.LBB0_1666:
	ds_read_b128 v[212:215], v181 offset:32768
	ds_read_b128 v[216:219], v181 offset:40960
	ds_read_b128 v[220:223], v182 offset:32768
	ds_read_b128 v[224:227], v182 offset:40960
	ds_read_b128 v[228:231], v183 offset:32768
	ds_read_b128 v[232:235], v183 offset:40960
	ds_read_b128 v[236:239], v184 offset:32768
	ds_read_b128 v[240:243], v184 offset:40960
	ds_read_b128 v[244:247], v181 offset:32896
	ds_read_b128 v[248:251], v181 offset:41088
	v_cmp_lt_i32_e32 vcc, 63, v170
	s_cmp_eq_u64 vcc, exec
	s_waitcnt lgkmcnt(9)
	v_mfma_f32_32x32x16_bf16 v[96:111], v[212:215], v[136:139], 0
	ds_read_b128 v[212:215], v182 offset:32896
	s_waitcnt lgkmcnt(9)
	v_mfma_f32_32x32x16_bf16 v[80:95], v[216:219], v[136:139], 0
	ds_read_b128 v[216:219], v182 offset:41088
	s_waitcnt lgkmcnt(9)
	v_mfma_f32_32x32x16_bf16 v[96:111], v[220:223], v[112:115], v[96:111]
	ds_read_b128 v[220:223], v183 offset:32896
	s_waitcnt lgkmcnt(9)
	v_mfma_f32_32x32x16_bf16 v[80:95], v[224:227], v[112:115], v[80:95]
	ds_read_b128 v[224:227], v183 offset:41088
	s_waitcnt lgkmcnt(9)
	v_mfma_f32_32x32x16_bf16 v[96:111], v[228:231], v[116:119], v[96:111]
	ds_read_b128 v[228:231], v184 offset:32896
	s_waitcnt lgkmcnt(9)
	v_mfma_f32_32x32x16_bf16 v[80:95], v[232:235], v[116:119], v[80:95]
	ds_read_b128 v[232:235], v184 offset:41088
	s_waitcnt lgkmcnt(9)
	v_mfma_f32_32x32x16_bf16 v[96:111], v[236:239], v[124:127], v[96:111]
	s_waitcnt lgkmcnt(8)
	v_mfma_f32_32x32x16_bf16 v[80:95], v[240:243], v[124:127], v[80:95]
	s_waitcnt lgkmcnt(7)
	v_mfma_f32_32x32x16_bf16 v[96:111], v[244:247], v[140:143], v[96:111]
	s_waitcnt lgkmcnt(6)
	v_mfma_f32_32x32x16_bf16 v[80:95], v[248:251], v[140:143], v[80:95]
	s_waitcnt lgkmcnt(5)
	v_mfma_f32_32x32x16_bf16 v[96:111], v[212:215], v[132:135], v[96:111]
	s_waitcnt lgkmcnt(4)
	v_mfma_f32_32x32x16_bf16 v[80:95], v[216:219], v[132:135], v[80:95]
	s_waitcnt lgkmcnt(3)
	v_mfma_f32_32x32x16_bf16 v[96:111], v[220:223], v[120:123], v[96:111]
	s_waitcnt lgkmcnt(2)
	v_mfma_f32_32x32x16_bf16 v[80:95], v[224:227], v[120:123], v[80:95]
	s_waitcnt lgkmcnt(1)
	v_mfma_f32_32x32x16_bf16 v[96:111], v[228:231], v[128:131], v[96:111]
	s_waitcnt lgkmcnt(0)
	s_nop 0
	v_mfma_f32_32x32x16_bf16 v[80:95], v[232:235], v[128:131], v[80:95]
	s_cbranch_scc1 .LBB0_1668
	v_add_u32_e32 v0, v180, v170
	v_cmp_lt_i32_e32 vcc, 0, v0
	s_nop 5
	v_cndmask_b32_e32 v96, v168, v96, vcc
	v_cmp_lt_i32_e32 vcc, 32, v0
	s_nop 1
	v_cndmask_b32_e32 v80, v168, v80, vcc
	v_cmp_lt_i32_e32 vcc, 1, v0
	s_nop 1
	v_cndmask_b32_e32 v97, v168, v97, vcc
	v_cmp_lt_i32_e32 vcc, 33, v0
	s_nop 1
	v_cndmask_b32_e32 v81, v168, v81, vcc
	v_cmp_lt_i32_e32 vcc, 2, v0
	s_nop 1
	v_cndmask_b32_e32 v98, v168, v98, vcc
	v_cmp_lt_i32_e32 vcc, 34, v0
	s_nop 1
	v_cndmask_b32_e32 v82, v168, v82, vcc
	v_cmp_lt_i32_e32 vcc, 3, v0
	s_nop 1
	v_cndmask_b32_e32 v99, v168, v99, vcc
	v_cmp_lt_i32_e32 vcc, 35, v0
	s_nop 1
	v_cndmask_b32_e32 v83, v168, v83, vcc
	v_cmp_lt_i32_e32 vcc, 8, v0
	s_nop 1
	v_cndmask_b32_e32 v100, v168, v100, vcc
	v_cmp_lt_i32_e32 vcc, 40, v0
	s_nop 1
	v_cndmask_b32_e32 v84, v168, v84, vcc
	v_cmp_lt_i32_e32 vcc, 9, v0
	s_nop 1
	v_cndmask_b32_e32 v101, v168, v101, vcc
	v_cmp_lt_i32_e32 vcc, 41, v0
	s_nop 1
	v_cndmask_b32_e32 v85, v168, v85, vcc
	v_cmp_lt_i32_e32 vcc, 10, v0
	s_nop 1
	v_cndmask_b32_e32 v102, v168, v102, vcc
	v_cmp_lt_i32_e32 vcc, 42, v0
	s_nop 1
	v_cndmask_b32_e32 v86, v168, v86, vcc
	v_cmp_lt_i32_e32 vcc, 11, v0
	s_nop 1
	v_cndmask_b32_e32 v103, v168, v103, vcc
	v_cmp_lt_i32_e32 vcc, 43, v0
	s_nop 1
	v_cndmask_b32_e32 v87, v168, v87, vcc
	v_cmp_lt_i32_e32 vcc, 16, v0
	s_nop 1
	v_cndmask_b32_e32 v104, v168, v104, vcc
	v_cmp_lt_i32_e32 vcc, 48, v0
	s_nop 1
	v_cndmask_b32_e32 v88, v168, v88, vcc
	v_cmp_lt_i32_e32 vcc, 17, v0
	s_nop 1
	v_cndmask_b32_e32 v105, v168, v105, vcc
	v_cmp_lt_i32_e32 vcc, 49, v0
	s_nop 1
	v_cndmask_b32_e32 v89, v168, v89, vcc
	v_cmp_lt_i32_e32 vcc, 18, v0
	s_nop 1
	v_cndmask_b32_e32 v106, v168, v106, vcc
	v_cmp_lt_i32_e32 vcc, 50, v0
	s_nop 1
	v_cndmask_b32_e32 v90, v168, v90, vcc
	v_cmp_lt_i32_e32 vcc, 19, v0
	s_nop 1
	v_cndmask_b32_e32 v107, v168, v107, vcc
	v_cmp_lt_i32_e32 vcc, 51, v0
	s_nop 1
	v_cndmask_b32_e32 v91, v168, v91, vcc
	v_cmp_lt_i32_e32 vcc, 24, v0
	s_nop 1
	v_cndmask_b32_e32 v108, v168, v108, vcc
	v_cmp_lt_i32_e32 vcc, 56, v0
	s_nop 1
	v_cndmask_b32_e32 v92, v168, v92, vcc
	v_cmp_lt_i32_e32 vcc, 25, v0
	s_nop 1
	v_cndmask_b32_e32 v109, v168, v109, vcc
	v_cmp_lt_i32_e32 vcc, 57, v0
	s_nop 1
	v_cndmask_b32_e32 v93, v168, v93, vcc
	v_cmp_lt_i32_e32 vcc, 26, v0
	s_nop 1
	v_cndmask_b32_e32 v110, v168, v110, vcc
	v_cmp_lt_i32_e32 vcc, 58, v0
	s_nop 1
	v_cndmask_b32_e32 v94, v168, v94, vcc
	v_cmp_lt_i32_e32 vcc, 27, v0
	s_nop 1
	v_cndmask_b32_e32 v111, v168, v111, vcc
	v_cmp_lt_i32_e32 vcc, 59, v0
	s_nop 1
	v_cndmask_b32_e32 v95, v168, v95, vcc

.LBB0_1679:
	ds_read_b128 v[212:215], v181 offset:49152
	ds_read_b128 v[216:219], v181 offset:57344
	ds_read_b128 v[220:223], v182 offset:49152
	ds_read_b128 v[224:227], v182 offset:57344
	ds_read_b128 v[228:231], v183 offset:49152
	ds_read_b128 v[232:235], v183 offset:57344
	ds_read_b128 v[236:239], v184 offset:49152
	ds_read_b128 v[240:243], v184 offset:57344
	ds_read_b128 v[244:247], v181 offset:49280
	ds_read_b128 v[248:251], v181 offset:57472
	v_subrev_u32_e32 v0, 64, v170
	v_cmp_lt_i32_e32 vcc, 63, v0
	s_cmp_eq_u64 vcc, exec
	s_waitcnt lgkmcnt(9)
	v_mfma_f32_32x32x16_bf16 v[96:111], v[212:215], v[136:139], 0
	ds_read_b128 v[212:215], v182 offset:49280
	s_waitcnt lgkmcnt(9)
	v_mfma_f32_32x32x16_bf16 v[80:95], v[216:219], v[136:139], 0
	ds_read_b128 v[216:219], v182 offset:57472
	s_waitcnt lgkmcnt(9)
	v_mfma_f32_32x32x16_bf16 v[96:111], v[220:223], v[112:115], v[96:111]
	ds_read_b128 v[220:223], v183 offset:49280
	s_waitcnt lgkmcnt(9)
	v_mfma_f32_32x32x16_bf16 v[80:95], v[224:227], v[112:115], v[80:95]
	ds_read_b128 v[224:227], v183 offset:57472
	s_waitcnt lgkmcnt(9)
	v_mfma_f32_32x32x16_bf16 v[96:111], v[228:231], v[116:119], v[96:111]
	ds_read_b128 v[228:231], v184 offset:49280
	s_waitcnt lgkmcnt(9)
	v_mfma_f32_32x32x16_bf16 v[80:95], v[232:235], v[116:119], v[80:95]
	ds_read_b128 v[232:235], v184 offset:57472
	s_waitcnt lgkmcnt(9)
	v_mfma_f32_32x32x16_bf16 v[96:111], v[236:239], v[124:127], v[96:111]
	s_waitcnt lgkmcnt(8)
	v_mfma_f32_32x32x16_bf16 v[80:95], v[240:243], v[124:127], v[80:95]
	s_waitcnt lgkmcnt(7)
	v_mfma_f32_32x32x16_bf16 v[96:111], v[244:247], v[140:143], v[96:111]
	s_waitcnt lgkmcnt(6)
	v_mfma_f32_32x32x16_bf16 v[80:95], v[248:251], v[140:143], v[80:95]
	s_waitcnt lgkmcnt(5)
	v_mfma_f32_32x32x16_bf16 v[96:111], v[212:215], v[132:135], v[96:111]
	s_waitcnt lgkmcnt(4)
	v_mfma_f32_32x32x16_bf16 v[80:95], v[216:219], v[132:135], v[80:95]
	s_waitcnt lgkmcnt(3)
	v_mfma_f32_32x32x16_bf16 v[96:111], v[220:223], v[120:123], v[96:111]
	s_waitcnt lgkmcnt(2)
	v_mfma_f32_32x32x16_bf16 v[80:95], v[224:227], v[120:123], v[80:95]
	s_waitcnt lgkmcnt(1)
	v_mfma_f32_32x32x16_bf16 v[96:111], v[228:231], v[128:131], v[96:111]
	s_waitcnt lgkmcnt(0)
	s_nop 0
	v_mfma_f32_32x32x16_bf16 v[80:95], v[232:235], v[128:131], v[80:95]
	s_cbranch_scc1 .LBB0_1681
	v_add3_u32 v0, v180, v170, s38
	v_cmp_lt_i32_e32 vcc, 0, v0
	s_nop 5
	v_cndmask_b32_e32 v96, v168, v96, vcc
	v_cmp_lt_i32_e32 vcc, 32, v0
	s_nop 1
	v_cndmask_b32_e32 v80, v168, v80, vcc
	v_cmp_lt_i32_e32 vcc, 1, v0
	s_nop 1
	v_cndmask_b32_e32 v97, v168, v97, vcc
	v_cmp_lt_i32_e32 vcc, 33, v0
	s_nop 1
	v_cndmask_b32_e32 v81, v168, v81, vcc
	v_cmp_lt_i32_e32 vcc, 2, v0
	s_nop 1
	v_cndmask_b32_e32 v98, v168, v98, vcc
	v_cmp_lt_i32_e32 vcc, 34, v0
	s_nop 1
	v_cndmask_b32_e32 v82, v168, v82, vcc
	v_cmp_lt_i32_e32 vcc, 3, v0
	s_nop 1
	v_cndmask_b32_e32 v99, v168, v99, vcc
	v_cmp_lt_i32_e32 vcc, 35, v0
	s_nop 1
	v_cndmask_b32_e32 v83, v168, v83, vcc
	v_cmp_lt_i32_e32 vcc, 8, v0
	s_nop 1
	v_cndmask_b32_e32 v100, v168, v100, vcc
	v_cmp_lt_i32_e32 vcc, 40, v0
	s_nop 1
	v_cndmask_b32_e32 v84, v168, v84, vcc
	v_cmp_lt_i32_e32 vcc, 9, v0
	s_nop 1
	v_cndmask_b32_e32 v101, v168, v101, vcc
	v_cmp_lt_i32_e32 vcc, 41, v0
	s_nop 1
	v_cndmask_b32_e32 v85, v168, v85, vcc
	v_cmp_lt_i32_e32 vcc, 10, v0
	s_nop 1
	v_cndmask_b32_e32 v102, v168, v102, vcc
	v_cmp_lt_i32_e32 vcc, 42, v0
	s_nop 1
	v_cndmask_b32_e32 v86, v168, v86, vcc
	v_cmp_lt_i32_e32 vcc, 11, v0
	s_nop 1
	v_cndmask_b32_e32 v103, v168, v103, vcc
	v_cmp_lt_i32_e32 vcc, 43, v0
	s_nop 1
	v_cndmask_b32_e32 v87, v168, v87, vcc
	v_cmp_lt_i32_e32 vcc, 16, v0
	s_nop 1
	v_cndmask_b32_e32 v104, v168, v104, vcc
	v_cmp_lt_i32_e32 vcc, 48, v0
	s_nop 1
	v_cndmask_b32_e32 v88, v168, v88, vcc
	v_cmp_lt_i32_e32 vcc, 17, v0
	s_nop 1
	v_cndmask_b32_e32 v105, v168, v105, vcc
	v_cmp_lt_i32_e32 vcc, 49, v0
	s_nop 1
	v_cndmask_b32_e32 v89, v168, v89, vcc
	v_cmp_lt_i32_e32 vcc, 18, v0
	s_nop 1
	v_cndmask_b32_e32 v106, v168, v106, vcc
	v_cmp_lt_i32_e32 vcc, 50, v0
	s_nop 1
	v_cndmask_b32_e32 v90, v168, v90, vcc
	v_cmp_lt_i32_e32 vcc, 19, v0
	s_nop 1
	v_cndmask_b32_e32 v107, v168, v107, vcc
	v_cmp_lt_i32_e32 vcc, 51, v0
	s_nop 1
	v_cndmask_b32_e32 v91, v168, v91, vcc
	v_cmp_lt_i32_e32 vcc, 24, v0
	s_nop 1
	v_cndmask_b32_e32 v108, v168, v108, vcc
	v_cmp_lt_i32_e32 vcc, 56, v0
	s_nop 1
	v_cndmask_b32_e32 v92, v168, v92, vcc
	v_cmp_lt_i32_e32 vcc, 25, v0
	s_nop 1
	v_cndmask_b32_e32 v109, v168, v109, vcc
	v_cmp_lt_i32_e32 vcc, 57, v0
	s_nop 1
	v_cndmask_b32_e32 v93, v168, v93, vcc
	v_cmp_lt_i32_e32 vcc, 26, v0
	s_nop 1
	v_cndmask_b32_e32 v110, v168, v110, vcc
	v_cmp_lt_i32_e32 vcc, 58, v0
	s_nop 1
	v_cndmask_b32_e32 v94, v168, v94, vcc
	v_cmp_lt_i32_e32 vcc, 27, v0
	s_nop 1
	v_cndmask_b32_e32 v111, v168, v111, vcc
	v_cmp_lt_i32_e32 vcc, 59, v0
	s_nop 1
	v_cndmask_b32_e32 v95, v168, v95, vcc

.LBB0_1707:
	s_or_b64 exec, exec, s[4:5]
	s_waitcnt lgkmcnt(0)
	s_waitcnt lgkmcnt(0)
	v_lshlrev_b32_e32 v1, 2, v2
	v_lshl_add_u32 v2, v2, 4, s45
	ds_read_b128 v[4:7], v2
	s_add_i32 s72, 0, 0x10000
	v_lshl_add_u32 v0, v0, 1, s72
	v_or_b32_e32 v8, s48, v1
	v_mad_u64_u32 v[8:9], s[4:5], v8, s71, v[0:1]
	s_waitcnt lgkmcnt(0)
	v_mul_f32_e32 v9, v64, v4
	v_bfe_u32 v10, v9, 16, 1
	v_add3_u32 v9, v9, v10, s96
	ds_write_b16_d16_hi v8, v9
	v_mul_f32_e32 v9, v48, v4
	v_bfe_u32 v10, v9, 16, 1
	v_add3_u32 v9, v9, v10, s96
	ds_write_b16_d16_hi v8, v9 offset:64
	v_mul_f32_e32 v9, v32, v4
	v_bfe_u32 v10, v9, 16, 1
	v_add3_u32 v9, v9, v10, s96
	v_mul_f32_e32 v4, v16, v4
	ds_write_b16_d16_hi v8, v9 offset:128
	v_bfe_u32 v9, v4, 16, 1
	v_add3_u32 v4, v4, v9, s96
	ds_write_b16_d16_hi v8, v4 offset:192
	v_or_b32_e32 v4, s49, v1
	v_mad_u64_u32 v[8:9], s[4:5], v4, s71, v[0:1]
	v_mul_f32_e32 v4, v65, v5
	v_bfe_u32 v9, v4, 16, 1
	v_add3_u32 v4, v4, v9, s96
	ds_write_b16_d16_hi v8, v4
	v_mul_f32_e32 v4, v49, v5
	v_bfe_u32 v9, v4, 16, 1
	v_add3_u32 v4, v4, v9, s96
	ds_write_b16_d16_hi v8, v4 offset:64
	v_mul_f32_e32 v4, v33, v5
	v_bfe_u32 v9, v4, 16, 1
	v_add3_u32 v4, v4, v9, s96
	ds_write_b16_d16_hi v8, v4 offset:128
	v_mul_f32_e32 v4, v17, v5
	v_bfe_u32 v5, v4, 16, 1
	v_add3_u32 v4, v4, v5, s96
	ds_write_b16_d16_hi v8, v4 offset:192
	v_or_b32_e32 v4, s56, v1
	v_mad_u64_u32 v[4:5], s[4:5], v4, s71, v[0:1]
	v_mul_f32_e32 v5, v66, v6
	v_bfe_u32 v8, v5, 16, 1
	v_add3_u32 v5, v5, v8, s96
	ds_write_b16_d16_hi v4, v5
	v_mul_f32_e32 v5, v50, v6
	v_bfe_u32 v8, v5, 16, 1
	v_add3_u32 v5, v5, v8, s96
	ds_write_b16_d16_hi v4, v5 offset:64
	v_mul_f32_e32 v5, v34, v6
	v_bfe_u32 v8, v5, 16, 1
	v_add3_u32 v5, v5, v8, s96
	ds_write_b16_d16_hi v4, v5 offset:128
	v_mul_f32_e32 v5, v18, v6
	v_bfe_u32 v6, v5, 16, 1
	v_add3_u32 v5, v5, v6, s96
	ds_write_b16_d16_hi v4, v5 offset:192
	v_or_b32_e32 v4, s57, v1
	v_mad_u64_u32 v[4:5], s[4:5], v4, s71, v[0:1]
	v_mul_f32_e32 v5, v67, v7
	v_bfe_u32 v6, v5, 16, 1
	v_add3_u32 v5, v5, v6, s96
	ds_write_b16_d16_hi v4, v5
	v_mul_f32_e32 v5, v51, v7
	v_bfe_u32 v6, v5, 16, 1
	v_add3_u32 v5, v5, v6, s96
	ds_write_b16_d16_hi v4, v5 offset:64
	v_mul_f32_e32 v5, v35, v7
	v_bfe_u32 v6, v5, 16, 1
	v_add3_u32 v5, v5, v6, s96
	ds_write_b16_d16_hi v4, v5 offset:128
	v_mul_f32_e32 v5, v19, v7
	v_bfe_u32 v6, v5, 16, 1
	v_add3_u32 v5, v5, v6, s96
	ds_write_b16_d16_hi v4, v5 offset:192
	ds_read_b128 v[4:7], v2 offset:32
	v_or_b32_e32 v8, s58, v1
	v_mad_u64_u32 v[8:9], s[4:5], v8, s71, v[0:1]
	s_mov_b32 s1, 0x100000
	s_waitcnt lgkmcnt(0)
	v_mul_f32_e32 v9, v68, v4
	v_bfe_u32 v10, v9, 16, 1
	v_add3_u32 v9, v9, v10, s96
	ds_write_b16_d16_hi v8, v9
	v_mul_f32_e32 v9, v52, v4
	v_bfe_u32 v10, v9, 16, 1
	v_add3_u32 v9, v9, v10, s96
	ds_write_b16_d16_hi v8, v9 offset:64
	v_mul_f32_e32 v9, v36, v4
	v_bfe_u32 v10, v9, 16, 1
	v_add3_u32 v9, v9, v10, s96
	v_mul_f32_e32 v4, v20, v4
	ds_write_b16_d16_hi v8, v9 offset:128
	v_bfe_u32 v9, v4, 16, 1
	v_add3_u32 v4, v4, v9, s96
	ds_write_b16_d16_hi v8, v4 offset:192
	v_or_b32_e32 v4, s59, v1
	v_mad_u64_u32 v[8:9], s[4:5], v4, s71, v[0:1]
	v_mul_f32_e32 v4, v69, v5
	v_bfe_u32 v9, v4, 16, 1
	v_add3_u32 v4, v4, v9, s96
	ds_write_b16_d16_hi v8, v4
	v_mul_f32_e32 v4, v53, v5
	v_bfe_u32 v9, v4, 16, 1
	v_add3_u32 v4, v4, v9, s96
	ds_write_b16_d16_hi v8, v4 offset:64
	v_mul_f32_e32 v4, v37, v5
	v_bfe_u32 v9, v4, 16, 1
	v_add3_u32 v4, v4, v9, s96
	ds_write_b16_d16_hi v8, v4 offset:128
	v_mul_f32_e32 v4, v21, v5
	v_bfe_u32 v5, v4, 16, 1
	v_add3_u32 v4, v4, v5, s96
	ds_write_b16_d16_hi v8, v4 offset:192
	v_or_b32_e32 v4, s60, v1
	v_mad_u64_u32 v[4:5], s[4:5], v4, s71, v[0:1]
	v_mul_f32_e32 v5, v70, v6
	v_bfe_u32 v8, v5, 16, 1
	v_add3_u32 v5, v5, v8, s96
	ds_write_b16_d16_hi v4, v5
	v_mul_f32_e32 v5, v54, v6
	v_bfe_u32 v8, v5, 16, 1
	v_add3_u32 v5, v5, v8, s96
	ds_write_b16_d16_hi v4, v5 offset:64
	v_mul_f32_e32 v5, v38, v6
	v_bfe_u32 v8, v5, 16, 1
	v_add3_u32 v5, v5, v8, s96
	ds_write_b16_d16_hi v4, v5 offset:128
	v_mul_f32_e32 v5, v22, v6
	v_bfe_u32 v6, v5, 16, 1
	v_add3_u32 v5, v5, v6, s96
	ds_write_b16_d16_hi v4, v5 offset:192
	v_or_b32_e32 v4, s61, v1
	v_mad_u64_u32 v[4:5], s[4:5], v4, s71, v[0:1]
	v_mul_f32_e32 v5, v71, v7
	v_bfe_u32 v6, v5, 16, 1
	v_add3_u32 v5, v5, v6, s96
	ds_write_b16_d16_hi v4, v5
	v_mul_f32_e32 v5, v55, v7
	v_bfe_u32 v6, v5, 16, 1
	v_add3_u32 v5, v5, v6, s96
	ds_write_b16_d16_hi v4, v5 offset:64
	v_mul_f32_e32 v5, v39, v7
	v_bfe_u32 v6, v5, 16, 1
	v_add3_u32 v5, v5, v6, s96
	ds_write_b16_d16_hi v4, v5 offset:128
	v_mul_f32_e32 v5, v23, v7
	v_bfe_u32 v6, v5, 16, 1
	v_add3_u32 v5, v5, v6, s96
	ds_write_b16_d16_hi v4, v5 offset:192
	ds_read_b128 v[4:7], v2 offset:64
	v_or_b32_e32 v8, s62, v1
	v_mad_u64_u32 v[8:9], s[4:5], v8, s71, v[0:1]
	v_lshlrev_b32_e32 v23, 16, v136
	s_waitcnt lgkmcnt(0)
	v_mul_f32_e32 v9, v72, v4
	v_bfe_u32 v10, v9, 16, 1
	v_add3_u32 v9, v9, v10, s96
	ds_write_b16_d16_hi v8, v9
	v_mul_f32_e32 v9, v56, v4
	v_bfe_u32 v10, v9, 16, 1
	v_add3_u32 v9, v9, v10, s96
	ds_write_b16_d16_hi v8, v9 offset:64
	v_mul_f32_e32 v9, v40, v4
	v_bfe_u32 v10, v9, 16, 1
	v_add3_u32 v9, v9, v10, s96
	v_mul_f32_e32 v4, v24, v4
	ds_write_b16_d16_hi v8, v9 offset:128
	v_bfe_u32 v9, v4, 16, 1
	v_add3_u32 v4, v4, v9, s96
	ds_write_b16_d16_hi v8, v4 offset:192
	v_or_b32_e32 v4, s63, v1
	v_mad_u64_u32 v[8:9], s[4:5], v4, s71, v[0:1]
	v_mul_f32_e32 v4, v73, v5
	v_bfe_u32 v9, v4, 16, 1
	v_add3_u32 v4, v4, v9, s96
	ds_write_b16_d16_hi v8, v4
	v_mul_f32_e32 v4, v57, v5
	v_bfe_u32 v9, v4, 16, 1
	v_add3_u32 v4, v4, v9, s96
	ds_write_b16_d16_hi v8, v4 offset:64
	v_mul_f32_e32 v4, v41, v5
	v_bfe_u32 v9, v4, 16, 1
	v_add3_u32 v4, v4, v9, s96
	ds_write_b16_d16_hi v8, v4 offset:128
	v_mul_f32_e32 v4, v25, v5
	v_bfe_u32 v5, v4, 16, 1
	v_add3_u32 v4, v4, v5, s96
	ds_write_b16_d16_hi v8, v4 offset:192
	v_or_b32_e32 v4, s64, v1
	v_mad_u64_u32 v[4:5], s[4:5], v4, s71, v[0:1]
	v_mul_f32_e32 v5, v74, v6
	v_bfe_u32 v8, v5, 16, 1
	v_add3_u32 v5, v5, v8, s96
	ds_write_b16_d16_hi v4, v5
	v_mul_f32_e32 v5, v58, v6
	v_bfe_u32 v8, v5, 16, 1
	v_add3_u32 v5, v5, v8, s96
	ds_write_b16_d16_hi v4, v5 offset:64
	v_mul_f32_e32 v5, v42, v6
	v_bfe_u32 v8, v5, 16, 1
	v_add3_u32 v5, v5, v8, s96
	ds_write_b16_d16_hi v4, v5 offset:128
	v_mul_f32_e32 v5, v26, v6
	v_bfe_u32 v6, v5, 16, 1
	v_add3_u32 v5, v5, v6, s96
	ds_write_b16_d16_hi v4, v5 offset:192
	v_or_b32_e32 v4, s65, v1
	v_mad_u64_u32 v[4:5], s[4:5], v4, s71, v[0:1]
	v_mul_f32_e32 v5, v75, v7
	v_bfe_u32 v6, v5, 16, 1
	v_add3_u32 v5, v5, v6, s96
	ds_write_b16_d16_hi v4, v5
	v_mul_f32_e32 v5, v59, v7
	v_bfe_u32 v6, v5, 16, 1
	v_add3_u32 v5, v5, v6, s96
	ds_write_b16_d16_hi v4, v5 offset:64
	v_mul_f32_e32 v5, v43, v7
	v_bfe_u32 v6, v5, 16, 1
	v_add3_u32 v5, v5, v6, s96
	ds_write_b16_d16_hi v4, v5 offset:128
	v_mul_f32_e32 v5, v27, v7
	v_bfe_u32 v6, v5, 16, 1
	v_add3_u32 v5, v5, v6, s96
	ds_write_b16_d16_hi v4, v5 offset:192
	ds_read_b128 v[4:7], v2 offset:96
	v_or_b32_e32 v2, s66, v1
	v_mad_u64_u32 v[8:9], s[4:5], v2, s71, v[0:1]
	v_lshlrev_b32_e32 v22, 16, v140
	s_waitcnt lgkmcnt(0)
	v_mul_f32_e32 v2, v76, v4
	v_bfe_u32 v9, v2, 16, 1
	v_add3_u32 v2, v2, v9, s96
	ds_write_b16_d16_hi v8, v2
	v_mul_f32_e32 v2, v60, v4
	v_bfe_u32 v9, v2, 16, 1
	v_add3_u32 v2, v2, v9, s96
	ds_write_b16_d16_hi v8, v2 offset:64
	v_mul_f32_e32 v2, v44, v4
	v_bfe_u32 v9, v2, 16, 1
	v_add3_u32 v2, v2, v9, s96
	ds_write_b16_d16_hi v8, v2 offset:128
	v_mul_f32_e32 v2, v28, v4
	v_bfe_u32 v4, v2, 16, 1
	v_add3_u32 v2, v2, v4, s96
	ds_write_b16_d16_hi v8, v2 offset:192
	v_or_b32_e32 v2, s67, v1
	v_mad_u64_u32 v[8:9], s[4:5], v2, s71, v[0:1]
	v_mul_f32_e32 v2, v77, v5
	v_bfe_u32 v4, v2, 16, 1
	v_add3_u32 v2, v2, v4, s96
	ds_write_b16_d16_hi v8, v2
	v_mul_f32_e32 v2, v61, v5
	v_bfe_u32 v4, v2, 16, 1
	v_add3_u32 v2, v2, v4, s96
	ds_write_b16_d16_hi v8, v2 offset:64
	v_mul_f32_e32 v2, v45, v5
	v_bfe_u32 v4, v2, 16, 1
	v_add3_u32 v2, v2, v4, s96
	ds_write_b16_d16_hi v8, v2 offset:128
	v_mul_f32_e32 v2, v29, v5
	v_bfe_u32 v4, v2, 16, 1
	v_add3_u32 v2, v2, v4, s96
	ds_write_b16_d16_hi v8, v2 offset:192
	v_or_b32_e32 v2, s68, v1
	v_mad_u64_u32 v[4:5], s[4:5], v2, s71, v[0:1]
	v_mul_f32_e32 v2, v78, v6
	v_bfe_u32 v5, v2, 16, 1
	v_add3_u32 v2, v2, v5, s96
	ds_write_b16_d16_hi v4, v2
	v_mul_f32_e32 v2, v62, v6
	v_bfe_u32 v5, v2, 16, 1
	v_add3_u32 v2, v2, v5, s96
	ds_write_b16_d16_hi v4, v2 offset:64
	v_mul_f32_e32 v2, v46, v6
	v_bfe_u32 v5, v2, 16, 1
	v_add3_u32 v2, v2, v5, s96
	ds_write_b16_d16_hi v4, v2 offset:128
	v_mul_f32_e32 v2, v30, v6
	v_or_b32_e32 v1, s69, v1
	v_bfe_u32 v5, v2, 16, 1
	v_mad_u64_u32 v[0:1], s[4:5], v1, s71, v[0:1]
	v_add3_u32 v2, v2, v5, s96
	v_mul_f32_e32 v1, v79, v7
	ds_write_b16_d16_hi v4, v2 offset:192
	v_bfe_u32 v2, v1, 16, 1
	v_add3_u32 v1, v1, v2, s96
	ds_write_b16_d16_hi v0, v1
	v_mul_f32_e32 v1, v63, v7
	v_bfe_u32 v2, v1, 16, 1
	v_add3_u32 v1, v1, v2, s96
	ds_write_b16_d16_hi v0, v1 offset:64
	v_mul_f32_e32 v1, v47, v7
	v_bfe_u32 v2, v1, 16, 1
	v_add3_u32 v1, v1, v2, s96
	ds_write_b16_d16_hi v0, v1 offset:128
	v_mul_f32_e32 v1, v31, v7
	v_bfe_u32 v2, v1, 16, 1
	v_add3_u32 v1, v1, v2, s96
	v_readlane_b32 s4, v254, 28
	ds_write_b16_d16_hi v0, v1 offset:192
	v_lshlrev_b64 v[0:1], 8, v[152:153]
	v_readlane_b32 s5, v254, 29
	s_waitcnt lgkmcnt(0)
	ds_read_b64 v[150:151], v167
	s_mov_b64 s[12:13], -1
	v_lshl_add_u64 v[0:1], s[4:5], 0, v[0:1]
	v_lshl_add_u64 v[4:5], v[144:145], 2, v[0:1]
	v_add_co_u32_e32 v14, vcc, s1, v4
	global_load_dwordx4 v[6:9], v[4:5], off offset:16
	global_load_dwordx4 v[10:13], v[4:5], off
	s_mov_b64 s[4:5], 0x100000
	v_addc_co_u32_e32 v15, vcc, 0, v5, vcc
	v_lshl_add_u64 v[0:1], v[4:5], 0, s[4:5]
	global_load_dwordx4 v[14:17], v[14:15], off
	s_nop 0
	global_load_dwordx4 v[18:21], v[0:1], off offset:16
	s_waitcnt lgkmcnt(0)
	v_and_b32_e32 v155, 1, v150
	s_and_b64 vcc, exec, s[50:51]
	v_cmp_ne_u32_e64 s[10:11], 0, v155
	s_waitcnt vmcnt(2)
	v_mov_b32_e32 v25, v10
	s_waitcnt vmcnt(1)
	v_mov_b32_e32 v24, v14
	v_pk_mul_f32 v[24:25], v[24:25], v[22:23]
	s_nop 0
	v_sub_f32_e32 v2, v25, v24
	v_mov_b32_e32 v24, v10
	v_mov_b32_e32 v25, v14
	v_pk_mul_f32 v[22:23], v[24:25], v[22:23]
	v_mov_b32_e32 v10, v15
	v_add_f32_e32 v26, v22, v23
	v_and_b32_e32 v23, 0xffff0000, v136
	v_and_b32_e32 v22, 0xffff0000, v140
	v_pk_mul_f32 v[24:25], v[10:11], v[22:23]
	v_mov_b32_e32 v14, v11
	v_sub_f32_e32 v10, v25, v24
	v_cvt_pk_bf16_f32 v100, v2, v10
	v_pk_mul_f32 v[10:11], v[14:15], v[22:23]
	v_mov_b32_e32 v14, v16
	v_add_f32_e32 v2, v10, v11
	v_lshlrev_b32_e32 v11, 16, v137
	v_lshlrev_b32_e32 v10, 16, v141
	v_mov_b32_e32 v15, v12
	v_pk_mul_f32 v[14:15], v[14:15], v[10:11]
	v_cvt_pk_bf16_f32 v104, v26, v2
	v_lshlrev_b32_e32 v23, 16, v112
	v_sub_f32_e32 v2, v15, v14
	v_mov_b32_e32 v14, v12
	v_mov_b32_e32 v15, v16
	v_pk_mul_f32 v[10:11], v[14:15], v[10:11]
	v_mov_b32_e32 v12, v17
	v_add_f32_e32 v22, v10, v11
	v_and_b32_e32 v11, 0xffff0000, v137
	v_and_b32_e32 v10, 0xffff0000, v141
	v_pk_mul_f32 v[14:15], v[12:13], v[10:11]
	v_mov_b32_e32 v16, v13
	v_sub_f32_e32 v12, v15, v14
	v_pk_mul_f32 v[10:11], v[16:17], v[10:11]
	v_cvt_pk_bf16_f32 v101, v2, v12
	s_waitcnt vmcnt(0)
	v_mov_b32_e32 v12, v18
	v_add_f32_e32 v2, v10, v11
	v_lshlrev_b32_e32 v11, 16, v138
	v_lshlrev_b32_e32 v10, 16, v142
	v_mov_b32_e32 v13, v6
	v_pk_mul_f32 v[12:13], v[12:13], v[10:11]
	v_cvt_pk_bf16_f32 v105, v22, v2
	v_lshlrev_b32_e32 v22, 16, v132
	v_sub_f32_e32 v2, v13, v12
	v_mov_b32_e32 v12, v6
	v_mov_b32_e32 v13, v18
	v_pk_mul_f32 v[10:11], v[12:13], v[10:11]
	v_mov_b32_e32 v6, v19
	v_add_f32_e32 v14, v10, v11
	v_and_b32_e32 v11, 0xffff0000, v138
	v_and_b32_e32 v10, 0xffff0000, v142
	v_pk_mul_f32 v[12:13], v[6:7], v[10:11]
	v_mov_b32_e32 v18, v7
	v_sub_f32_e32 v6, v13, v12
	v_cvt_pk_bf16_f32 v102, v2, v6
	v_pk_mul_f32 v[6:7], v[18:19], v[10:11]
	v_mov_b32_e32 v10, v20
	v_add_f32_e32 v2, v6, v7
	v_lshlrev_b32_e32 v7, 16, v139
	v_lshlrev_b32_e32 v6, 16, v143
	v_mov_b32_e32 v11, v8
	v_pk_mul_f32 v[10:11], v[10:11], v[6:7]
	v_cvt_pk_bf16_f32 v106, v14, v2
	s_nop 0
	v_sub_f32_e32 v2, v11, v10
	v_mov_b32_e32 v10, v8
	v_mov_b32_e32 v11, v20
	v_pk_mul_f32 v[6:7], v[10:11], v[6:7]
	v_mov_b32_e32 v8, v21
	v_add_f32_e32 v12, v6, v7
	v_and_b32_e32 v7, 0xffff0000, v139
	v_and_b32_e32 v6, 0xffff0000, v143
	v_pk_mul_f32 v[10:11], v[8:9], v[6:7]
	v_mov_b32_e32 v20, v9
	v_sub_f32_e32 v8, v11, v10
	v_pk_mul_f32 v[6:7], v[20:21], v[6:7]
	v_cvt_pk_bf16_f32 v103, v2, v8
	s_nop 0
	v_add_f32_e32 v2, v6, v7
	v_cvt_pk_bf16_f32 v107, v12, v2
	global_load_dwordx4 v[6:9], v[4:5], off offset:80
	global_load_dwordx4 v[10:13], v[4:5], off offset:64
	global_load_dwordx4 v[14:17], v[0:1], off offset:80
	global_load_dwordx4 v[18:21], v[0:1], off offset:64
	s_waitcnt vmcnt(2)
	v_mov_b32_e32 v25, v10
	s_waitcnt vmcnt(0)
	v_mov_b32_e32 v24, v18
	v_pk_mul_f32 v[24:25], v[24:25], v[22:23]
	s_nop 0
	v_sub_f32_e32 v2, v25, v24
	v_mov_b32_e32 v24, v10
	v_mov_b32_e32 v25, v18
	v_pk_mul_f32 v[22:23], v[24:25], v[22:23]
	v_mov_b32_e32 v10, v19
	v_add_f32_e32 v26, v22, v23
	v_and_b32_e32 v23, 0xffff0000, v112
	v_and_b32_e32 v22, 0xffff0000, v132
	v_pk_mul_f32 v[24:25], v[10:11], v[22:23]
	v_mov_b32_e32 v18, v11
	v_sub_f32_e32 v10, v25, v24
	v_cvt_pk_bf16_f32 v108, v2, v10
	v_pk_mul_f32 v[10:11], v[18:19], v[22:23]
	v_mov_b32_e32 v18, v20
	v_add_f32_e32 v2, v10, v11
	v_lshlrev_b32_e32 v11, 16, v113
	v_lshlrev_b32_e32 v10, 16, v133
	v_mov_b32_e32 v19, v12
	v_pk_mul_f32 v[18:19], v[18:19], v[10:11]
	v_cvt_pk_bf16_f32 v112, v26, v2
	v_lshlrev_b32_e32 v23, 16, v116
	v_sub_f32_e32 v2, v19, v18
	v_mov_b32_e32 v18, v12
	v_mov_b32_e32 v19, v20
	v_pk_mul_f32 v[10:11], v[18:19], v[10:11]
	v_mov_b32_e32 v12, v21
	v_add_f32_e32 v22, v10, v11
	v_and_b32_e32 v11, 0xffff0000, v113
	v_and_b32_e32 v10, 0xffff0000, v133
	v_pk_mul_f32 v[18:19], v[12:13], v[10:11]
	v_mov_b32_e32 v20, v13
	v_sub_f32_e32 v12, v19, v18
	v_pk_mul_f32 v[10:11], v[20:21], v[10:11]
	v_cvt_pk_bf16_f32 v109, v2, v12
	v_mov_b32_e32 v12, v14
	v_add_f32_e32 v2, v10, v11
	v_lshlrev_b32_e32 v11, 16, v114
	v_lshlrev_b32_e32 v10, 16, v134
	v_mov_b32_e32 v13, v6
	v_pk_mul_f32 v[12:13], v[12:13], v[10:11]
	v_cvt_pk_bf16_f32 v113, v22, v2
	v_lshlrev_b32_e32 v22, 16, v120
	v_sub_f32_e32 v2, v13, v12
	v_mov_b32_e32 v12, v6
	v_mov_b32_e32 v13, v14
	v_pk_mul_f32 v[10:11], v[12:13], v[10:11]
	v_mov_b32_e32 v6, v15
	v_add_f32_e32 v18, v10, v11
	v_and_b32_e32 v11, 0xffff0000, v114
	v_and_b32_e32 v10, 0xffff0000, v134
	v_pk_mul_f32 v[12:13], v[6:7], v[10:11]
	v_mov_b32_e32 v14, v7
	v_sub_f32_e32 v6, v13, v12
	v_cvt_pk_bf16_f32 v110, v2, v6
	v_pk_mul_f32 v[6:7], v[14:15], v[10:11]
	v_mov_b32_e32 v10, v16
	v_add_f32_e32 v2, v6, v7
	v_lshlrev_b32_e32 v7, 16, v115
	v_lshlrev_b32_e32 v6, 16, v135
	v_mov_b32_e32 v11, v8
	v_pk_mul_f32 v[10:11], v[10:11], v[6:7]
	v_cvt_pk_bf16_f32 v114, v18, v2
	s_nop 0
	v_sub_f32_e32 v2, v11, v10
	v_mov_b32_e32 v10, v8
	v_mov_b32_e32 v11, v16
	v_pk_mul_f32 v[6:7], v[10:11], v[6:7]
	v_mov_b32_e32 v8, v17
	v_add_f32_e32 v12, v6, v7
	v_and_b32_e32 v7, 0xffff0000, v115
	v_and_b32_e32 v6, 0xffff0000, v135
	v_pk_mul_f32 v[10:11], v[8:9], v[6:7]
	v_mov_b32_e32 v16, v9
	v_sub_f32_e32 v8, v11, v10
	v_pk_mul_f32 v[6:7], v[16:17], v[6:7]
	v_cvt_pk_bf16_f32 v111, v2, v8
	s_nop 0
	v_add_f32_e32 v2, v6, v7
	v_cvt_pk_bf16_f32 v115, v12, v2
	global_load_dwordx4 v[6:9], v[4:5], off offset:144
	global_load_dwordx4 v[10:13], v[4:5], off offset:128
	global_load_dwordx4 v[14:17], v[0:1], off offset:144
	global_load_dwordx4 v[18:21], v[0:1], off offset:128
	s_waitcnt vmcnt(2)
	v_mov_b32_e32 v25, v10
	s_waitcnt vmcnt(0)
	v_mov_b32_e32 v24, v18
	v_pk_mul_f32 v[24:25], v[24:25], v[22:23]
	s_nop 0
	v_sub_f32_e32 v2, v25, v24
	v_mov_b32_e32 v24, v10
	v_mov_b32_e32 v25, v18
	v_pk_mul_f32 v[22:23], v[24:25], v[22:23]
	v_mov_b32_e32 v10, v19
	v_add_f32_e32 v26, v22, v23
	v_and_b32_e32 v23, 0xffff0000, v116
	v_and_b32_e32 v22, 0xffff0000, v120
	v_pk_mul_f32 v[24:25], v[10:11], v[22:23]
	v_mov_b32_e32 v18, v11
	v_sub_f32_e32 v10, v25, v24
	v_cvt_pk_bf16_f32 v116, v2, v10
	v_pk_mul_f32 v[10:11], v[18:19], v[22:23]
	v_mov_b32_e32 v18, v20
	v_add_f32_e32 v2, v10, v11
	v_lshlrev_b32_e32 v11, 16, v117
	v_lshlrev_b32_e32 v10, 16, v121
	v_mov_b32_e32 v19, v12
	v_pk_mul_f32 v[18:19], v[18:19], v[10:11]
	v_cvt_pk_bf16_f32 v120, v26, v2
	s_nop 0
	v_sub_f32_e32 v2, v19, v18
	v_mov_b32_e32 v18, v12
	v_mov_b32_e32 v19, v20
	v_pk_mul_f32 v[10:11], v[18:19], v[10:11]
	v_mov_b32_e32 v12, v21
	v_add_f32_e32 v22, v10, v11
	v_and_b32_e32 v11, 0xffff0000, v117
	v_and_b32_e32 v10, 0xffff0000, v121
	v_pk_mul_f32 v[18:19], v[12:13], v[10:11]
	v_mov_b32_e32 v20, v13
	v_sub_f32_e32 v12, v19, v18
	v_pk_mul_f32 v[10:11], v[20:21], v[10:11]
	v_cvt_pk_bf16_f32 v117, v2, v12
	v_mov_b32_e32 v12, v14
	v_add_f32_e32 v2, v10, v11
	v_lshlrev_b32_e32 v11, 16, v118
	v_lshlrev_b32_e32 v10, 16, v122
	v_mov_b32_e32 v13, v6
	v_pk_mul_f32 v[12:13], v[12:13], v[10:11]
	v_cvt_pk_bf16_f32 v121, v22, v2
	s_nop 0
	v_sub_f32_e32 v2, v13, v12
	v_mov_b32_e32 v12, v6
	v_mov_b32_e32 v13, v14
	v_pk_mul_f32 v[10:11], v[12:13], v[10:11]
	v_mov_b32_e32 v6, v15
	v_add_f32_e32 v18, v10, v11
	v_and_b32_e32 v11, 0xffff0000, v118
	v_and_b32_e32 v10, 0xffff0000, v122
	v_pk_mul_f32 v[12:13], v[6:7], v[10:11]
	v_mov_b32_e32 v14, v7
	v_sub_f32_e32 v6, v13, v12
	v_cvt_pk_bf16_f32 v118, v2, v6
	v_pk_mul_f32 v[6:7], v[14:15], v[10:11]
	v_mov_b32_e32 v10, v16
	v_add_f32_e32 v2, v6, v7
	v_lshlrev_b32_e32 v7, 16, v119
	v_lshlrev_b32_e32 v6, 16, v123
	v_mov_b32_e32 v11, v8
	v_pk_mul_f32 v[10:11], v[10:11], v[6:7]
	v_cvt_pk_bf16_f32 v122, v18, v2
	s_nop 0
	v_sub_f32_e32 v2, v11, v10
	v_mov_b32_e32 v10, v8
	v_mov_b32_e32 v11, v16
	v_pk_mul_f32 v[6:7], v[10:11], v[6:7]
	v_mov_b32_e32 v8, v17
	v_add_f32_e32 v12, v6, v7
	v_and_b32_e32 v7, 0xffff0000, v119
	v_and_b32_e32 v6, 0xffff0000, v123
	v_pk_mul_f32 v[10:11], v[8:9], v[6:7]
	v_mov_b32_e32 v16, v9
	v_sub_f32_e32 v8, v11, v10
	v_pk_mul_f32 v[6:7], v[16:17], v[6:7]
	v_cvt_pk_bf16_f32 v119, v2, v8
	s_nop 0
	v_add_f32_e32 v2, v6, v7
	v_cvt_pk_bf16_f32 v123, v12, v2
	global_load_dwordx4 v[6:9], v[4:5], off offset:208
	global_load_dwordx4 v[10:13], v[4:5], off offset:192
	global_load_dwordx4 v[14:17], v[0:1], off offset:208
	global_load_dwordx4 v[18:21], v[0:1], off offset:192
	v_lshlrev_b32_e32 v1, 16, v124
	v_lshlrev_b32_e32 v0, 16, v128
	s_waitcnt vmcnt(2)
	v_mov_b32_e32 v5, v10
	s_waitcnt vmcnt(0)
	v_mov_b32_e32 v4, v18
	v_pk_mul_f32 v[4:5], v[4:5], v[0:1]
	s_nop 0
	v_sub_f32_e32 v2, v5, v4
	v_mov_b32_e32 v4, v10
	v_mov_b32_e32 v5, v18
	v_pk_mul_f32 v[0:1], v[4:5], v[0:1]
	v_mov_b32_e32 v10, v19
	v_add_f32_e32 v22, v0, v1
	v_and_b32_e32 v1, 0xffff0000, v124
	v_and_b32_e32 v0, 0xffff0000, v128
	v_mov_b32_e32 v18, v11
	v_pk_mul_f32 v[4:5], v[10:11], v[0:1]
	v_pk_mul_f32 v[0:1], v[18:19], v[0:1]
	v_sub_f32_e32 v4, v5, v4
	v_add_f32_e32 v0, v0, v1
	v_cvt_pk_bf16_f32 v124, v2, v4
	v_cvt_pk_bf16_f32 v128, v22, v0
	v_lshlrev_b32_e32 v1, 16, v125
	v_lshlrev_b32_e32 v0, 16, v129
	v_mov_b32_e32 v4, v20
	v_mov_b32_e32 v5, v12
	v_pk_mul_f32 v[4:5], v[4:5], v[0:1]
	s_nop 0
	v_sub_f32_e32 v2, v5, v4
	v_mov_b32_e32 v4, v12
	v_mov_b32_e32 v5, v20
	v_pk_mul_f32 v[0:1], v[4:5], v[0:1]
	v_mov_b32_e32 v12, v21
	v_add_f32_e32 v10, v0, v1
	v_and_b32_e32 v1, 0xffff0000, v125
	v_and_b32_e32 v0, 0xffff0000, v129
	v_mov_b32_e32 v20, v13
	v_pk_mul_f32 v[4:5], v[12:13], v[0:1]
	v_pk_mul_f32 v[0:1], v[20:21], v[0:1]
	v_sub_f32_e32 v4, v5, v4
	v_add_f32_e32 v0, v0, v1
	v_cvt_pk_bf16_f32 v125, v2, v4
	v_cvt_pk_bf16_f32 v129, v10, v0
	v_lshlrev_b32_e32 v1, 16, v126
	v_lshlrev_b32_e32 v0, 16, v130
	v_mov_b32_e32 v4, v14
	v_mov_b32_e32 v5, v6
	v_pk_mul_f32 v[4:5], v[4:5], v[0:1]
	s_nop 0
	v_sub_f32_e32 v2, v5, v4
	v_mov_b32_e32 v4, v6
	v_mov_b32_e32 v5, v14
	v_pk_mul_f32 v[0:1], v[4:5], v[0:1]
	v_mov_b32_e32 v6, v15
	v_add_f32_e32 v10, v0, v1
	v_and_b32_e32 v1, 0xffff0000, v126
	v_and_b32_e32 v0, 0xffff0000, v130
	v_mov_b32_e32 v14, v7
	v_pk_mul_f32 v[4:5], v[6:7], v[0:1]
	v_pk_mul_f32 v[0:1], v[14:15], v[0:1]
	v_sub_f32_e32 v4, v5, v4
	v_add_f32_e32 v0, v0, v1
	v_cvt_pk_bf16_f32 v126, v2, v4
	v_cvt_pk_bf16_f32 v130, v10, v0
	v_lshlrev_b32_e32 v1, 16, v127
	v_lshlrev_b32_e32 v0, 16, v131
	v_mov_b32_e32 v4, v16
	v_mov_b32_e32 v5, v8
	v_pk_mul_f32 v[4:5], v[4:5], v[0:1]
	s_nop 0
	v_sub_f32_e32 v2, v5, v4
	v_mov_b32_e32 v4, v8
	v_mov_b32_e32 v5, v16
	v_pk_mul_f32 v[0:1], v[4:5], v[0:1]
	v_mov_b32_e32 v8, v17
	v_add_f32_e32 v6, v0, v1
	v_and_b32_e32 v1, 0xffff0000, v127
	v_and_b32_e32 v0, 0xffff0000, v131
	v_mov_b32_e32 v16, v9
	v_pk_mul_f32 v[4:5], v[8:9], v[0:1]
	v_pk_mul_f32 v[0:1], v[16:17], v[0:1]
	v_sub_f32_e32 v4, v5, v4
	v_add_f32_e32 v0, v0, v1
	v_cvt_pk_bf16_f32 v127, v2, v4
	v_cvt_pk_bf16_f32 v131, v6, v0
	v_mbcnt_lo_u32_b32 v0, -1, 0
	v_mbcnt_hi_u32_b32 v0, -1, v0
	s_waitcnt vmcnt(0) lgkmcnt(0)
	s_barrier
	v_lshlrev_b32_e32 v4, 4, v0
	v_lshlrev_b32_e32 v2, 3, v0
	v_and_b32_e32 v5, 0xc0, v4
	v_lshlrev_b32_e32 v6, 1, v0
	v_and_or_b32 v5, v2, 24, v5
	v_and_b32_e32 v7, 32, v6
	v_and_b32_e32 v2, 0x100, v2
	v_or3_b32 v139, v5, v7, v2
	v_add_u32_e32 v2, s40, v4
	v_bfe_u32 v7, v0, 2, 2
	v_lshrrev_b32_e32 v8, 1, v0
	v_and_b32_e32 v5, 15, v0
	v_and_or_b32 v7, v8, 8, v7
	v_ashrrev_i32_e32 v8, 8, v2
	v_bitop3_b32 v9, v8, v5, 7 bitop3:0x6c
	v_lshlrev_b32_e32 v10, 10, v8
	v_lshl_or_b32 v132, v9, 4, v10
	v_and_b32_e32 v9, 0xfffff0, v8
	v_lshrrev_b32_e32 v8, 1, v8
	v_and_b32_e32 v8, 4, v8
	v_or3_b32 v8, v9, v8, v7
	v_and_b32_e32 v4, 48, v4
	v_and_b32_e32 v6, 0xc0, v6
	v_mul_i32_i24_e32 v8, 0x6a00, v8
	v_add_u32_e32 v2, 0x400, v2
	v_or3_b32 v133, v8, v6, v4
	v_ashrrev_i32_e32 v6, 8, v2
	v_bitop3_b32 v5, v6, v5, 7 bitop3:0x6c
	v_lshlrev_b32_e32 v8, 10, v6
	v_lshl_or_b32 v134, v5, 4, v8
	v_and_b32_e32 v5, 0xfffff0, v6
	v_lshrrev_b32_e32 v6, 1, v6
	v_and_b32_e32 v6, 4, v6
	v_lshrrev_b32_e32 v1, 5, v0
	v_or3_b32 v5, v5, v6, v7
	v_lshrrev_b32_e32 v2, 3, v2
	v_and_b32_e32 v141, 31, v0
	v_bfe_u32 v140, v0, 5, 1
	v_and_b32_e32 v2, 0xc0, v2
	v_mul_i32_i24_e32 v5, 0x6a00, v5
	v_xor_b32_e32 v0, v1, v0
	v_lshlrev_b32_e32 v1, 4, v141
	v_or3_b32 v135, v5, v2, v4
	v_add_u32_e32 v136, 0, v139
	v_lshlrev_b32_e32 v142, 8, v141
	v_lshlrev_b32_e32 v137, 2, v140
	v_lshlrev_b32_e32 v170, 4, v0
	v_and_b32_e32 v143, 0x60, v1
	v_bitop3_b32 v152, v1, 32, v166 bitop3:0x6c
	v_bitop3_b32 v153, v1, 64, v166 bitop3:0x6c
	v_bitop3_b32 v154, v1, s70, v1 bitop3:0xc
	s_cbranch_vccz .LBB0_1808
	s_waitcnt vmcnt(0) lgkmcnt(0)
	s_barrier
	v_and_b32_e32 v0, 16, v170
	v_add3_u32 v0, 0, v142, v0
	s_cmp_lg_u64 s[10:11], 0
	s_cselect_b64 s[12:13], -1, 0
	v_add_u32_e32 v171, v0, v143
	v_add_u32_e32 v172, v0, v152
	v_add_u32_e32 v173, v0, v153
	v_add_u32_e32 v174, v0, v154
	s_mov_b64 vcc, s[10:11]
	s_cbranch_vccz .LBB0_1714
	ds_read_b128 v[212:215], v171 offset:32768
	ds_read_b128 v[216:219], v172 offset:32768
	ds_read_b128 v[220:223], v171 offset:40960
	ds_read_b128 v[224:227], v172 offset:40960
	ds_read_b128 v[228:231], v173 offset:32768
	ds_read_b128 v[232:235], v173 offset:40960
	ds_read_b128 v[236:239], v174 offset:32768
	ds_read_b128 v[240:243], v174 offset:40960
	ds_read_b128 v[244:247], v171 offset:32896
	ds_read_b128 v[248:251], v171 offset:41088
	v_cndmask_b32_e64 v0, 64, v163, s[8:9]
	v_cndmask_b32_e64 v0, 0, v0, s[10:11]
	v_cmp_lt_u32_e32 vcc, 63, v0
	s_cmp_eq_u64 vcc, exec
	s_waitcnt lgkmcnt(9)
	v_mfma_f32_32x32x16_bf16 v[20:35], v[212:215], v[100:103], 0
	ds_read_b128 v[212:215], v172 offset:32896
	s_waitcnt lgkmcnt(9)
	v_mfma_f32_32x32x16_bf16 v[20:35], v[216:219], v[108:111], v[20:35]
	ds_read_b128 v[216:219], v172 offset:41088
	s_waitcnt lgkmcnt(9)
	v_mfma_f32_32x32x16_bf16 v[4:19], v[220:223], v[100:103], 0
	ds_read_b128 v[220:223], v173 offset:32896
	s_waitcnt lgkmcnt(9)
	v_mfma_f32_32x32x16_bf16 v[4:19], v[224:227], v[108:111], v[4:19]
	ds_read_b128 v[224:227], v173 offset:41088
	s_waitcnt lgkmcnt(9)
	v_mfma_f32_32x32x16_bf16 v[20:35], v[228:231], v[116:119], v[20:35]
	ds_read_b128 v[228:231], v174 offset:32896
	s_waitcnt lgkmcnt(9)
	v_mfma_f32_32x32x16_bf16 v[4:19], v[232:235], v[116:119], v[4:19]
	ds_read_b128 v[232:235], v174 offset:41088
	s_waitcnt lgkmcnt(9)
	v_mfma_f32_32x32x16_bf16 v[20:35], v[236:239], v[124:127], v[20:35]
	s_waitcnt lgkmcnt(8)
	v_mfma_f32_32x32x16_bf16 v[4:19], v[240:243], v[124:127], v[4:19]
	s_waitcnt lgkmcnt(7)
	v_mfma_f32_32x32x16_bf16 v[20:35], v[244:247], v[104:107], v[20:35]
	s_waitcnt lgkmcnt(6)
	v_mfma_f32_32x32x16_bf16 v[4:19], v[248:251], v[104:107], v[4:19]
	s_waitcnt lgkmcnt(5)
	v_mfma_f32_32x32x16_bf16 v[20:35], v[212:215], v[112:115], v[20:35]
	s_waitcnt lgkmcnt(4)
	v_mfma_f32_32x32x16_bf16 v[4:19], v[216:219], v[112:115], v[4:19]
	s_waitcnt lgkmcnt(3)
	v_mfma_f32_32x32x16_bf16 v[20:35], v[220:223], v[120:123], v[20:35]
	s_waitcnt lgkmcnt(2)
	v_mfma_f32_32x32x16_bf16 v[4:19], v[224:227], v[120:123], v[4:19]
	s_waitcnt lgkmcnt(1)
	v_mfma_f32_32x32x16_bf16 v[20:35], v[228:231], v[128:131], v[20:35]
	s_waitcnt lgkmcnt(0)
	s_nop 0
	v_mfma_f32_32x32x16_bf16 v[4:19], v[232:235], v[128:131], v[4:19]
	s_cbranch_scc1 .LBB0_1711
	v_sub_u32_e32 v0, v0, v137
	v_cmp_lt_i32_e32 vcc, 0, v0
	s_nop 5
	v_cndmask_b32_e32 v20, v168, v20, vcc
	v_cmp_lt_i32_e32 vcc, 32, v0
	s_nop 1
	v_cndmask_b32_e32 v4, v168, v4, vcc
	v_cmp_lt_i32_e32 vcc, 1, v0
	s_nop 1
	v_cndmask_b32_e32 v21, v168, v21, vcc
	v_cmp_lt_i32_e32 vcc, 33, v0
	s_nop 1
	v_cndmask_b32_e32 v5, v168, v5, vcc
	v_cmp_lt_i32_e32 vcc, 2, v0
	s_nop 1
	v_cndmask_b32_e32 v22, v168, v22, vcc
	v_cmp_lt_i32_e32 vcc, 34, v0
	s_nop 1
	v_cndmask_b32_e32 v6, v168, v6, vcc
	v_cmp_lt_i32_e32 vcc, 3, v0
	s_nop 1
	v_cndmask_b32_e32 v23, v168, v23, vcc
	v_cmp_lt_i32_e32 vcc, 35, v0
	s_nop 1
	v_cndmask_b32_e32 v7, v168, v7, vcc
	v_cmp_lt_i32_e32 vcc, 8, v0
	s_nop 1
	v_cndmask_b32_e32 v24, v168, v24, vcc
	v_cmp_lt_i32_e32 vcc, 40, v0
	s_nop 1
	v_cndmask_b32_e32 v8, v168, v8, vcc
	v_cmp_lt_i32_e32 vcc, 9, v0
	s_nop 1
	v_cndmask_b32_e32 v25, v168, v25, vcc
	v_cmp_lt_i32_e32 vcc, 41, v0
	s_nop 1
	v_cndmask_b32_e32 v9, v168, v9, vcc
	v_cmp_lt_i32_e32 vcc, 10, v0
	s_nop 1
	v_cndmask_b32_e32 v26, v168, v26, vcc
	v_cmp_lt_i32_e32 vcc, 42, v0
	s_nop 1
	v_cndmask_b32_e32 v10, v168, v10, vcc
	v_cmp_lt_i32_e32 vcc, 11, v0
	s_nop 1
	v_cndmask_b32_e32 v27, v168, v27, vcc
	v_cmp_lt_i32_e32 vcc, 43, v0
	s_nop 1
	v_cndmask_b32_e32 v11, v168, v11, vcc
	v_cmp_lt_i32_e32 vcc, 16, v0
	s_nop 1
	v_cndmask_b32_e32 v28, v168, v28, vcc
	v_cmp_lt_i32_e32 vcc, 48, v0
	s_nop 1
	v_cndmask_b32_e32 v12, v168, v12, vcc
	v_cmp_lt_i32_e32 vcc, 17, v0
	s_nop 1
	v_cndmask_b32_e32 v29, v168, v29, vcc
	v_cmp_lt_i32_e32 vcc, 49, v0
	s_nop 1
	v_cndmask_b32_e32 v13, v168, v13, vcc
	v_cmp_lt_i32_e32 vcc, 18, v0
	s_nop 1
	v_cndmask_b32_e32 v30, v168, v30, vcc
	v_cmp_lt_i32_e32 vcc, 50, v0
	s_nop 1
	v_cndmask_b32_e32 v14, v168, v14, vcc
	v_cmp_lt_i32_e32 vcc, 19, v0
	s_nop 1
	v_cndmask_b32_e32 v31, v168, v31, vcc
	v_cmp_lt_i32_e32 vcc, 51, v0
	s_nop 1
	v_cndmask_b32_e32 v15, v168, v15, vcc
	v_cmp_lt_i32_e32 vcc, 24, v0
	s_nop 1
	v_cndmask_b32_e32 v32, v168, v32, vcc
	v_cmp_lt_i32_e32 vcc, 56, v0
	s_nop 1
	v_cndmask_b32_e32 v16, v168, v16, vcc
	v_cmp_lt_i32_e32 vcc, 25, v0
	s_nop 1
	v_cndmask_b32_e32 v33, v168, v33, vcc
	v_cmp_lt_i32_e32 vcc, 57, v0
	s_nop 1
	v_cndmask_b32_e32 v17, v168, v17, vcc
	v_cmp_lt_i32_e32 vcc, 26, v0
	s_nop 1
	v_cndmask_b32_e32 v34, v168, v34, vcc
	v_cmp_lt_i32_e32 vcc, 58, v0
	s_nop 1
	v_cndmask_b32_e32 v18, v168, v18, vcc
	v_cmp_lt_i32_e32 vcc, 27, v0
	s_nop 1
	v_cndmask_b32_e32 v35, v168, v35, vcc
	v_cmp_lt_i32_e32 vcc, 59, v0
	s_nop 1
	v_cndmask_b32_e32 v19, v168, v19, vcc

.LBB0_1732:
	v_bfe_u32 v1, v150, 1, 1
	v_cmp_ne_u32_e32 vcc, 0, v1
	s_cmp_lg_u64 vcc, 0
	s_cselect_b64 s[16:17], -1, 0
	s_cbranch_vccz .LBB0_1737
	ds_read_b128 v[212:215], v171 offset:49152
	ds_read_b128 v[216:219], v172 offset:49152
	ds_read_b128 v[220:223], v171 offset:57344
	ds_read_b128 v[224:227], v172 offset:57344
	ds_read_b128 v[228:231], v173 offset:49152
	ds_read_b128 v[232:235], v173 offset:57344
	ds_read_b128 v[236:239], v174 offset:49152
	ds_read_b128 v[240:243], v174 offset:57344
	ds_read_b128 v[244:247], v171 offset:49280
	ds_read_b128 v[248:251], v171 offset:57472
	s_cmp_eq_u32 s89, 1
	s_cselect_b64 s[14:15], -1, 0
	v_cndmask_b32_e64 v1, 64, v163, s[14:15]
	v_cndmask_b32_e32 v1, 0, v1, vcc
	v_cmp_lt_u32_e32 vcc, 63, v1
	s_cmp_eq_u64 vcc, exec
	s_waitcnt lgkmcnt(9)
	v_mfma_f32_32x32x16_bf16 v[68:83], v[212:215], v[100:103], 0
	ds_read_b128 v[212:215], v172 offset:49280
	s_waitcnt lgkmcnt(9)
	v_mfma_f32_32x32x16_bf16 v[68:83], v[216:219], v[108:111], v[68:83]
	ds_read_b128 v[216:219], v172 offset:57472
	s_waitcnt lgkmcnt(9)
	v_mfma_f32_32x32x16_bf16 v[84:99], v[220:223], v[100:103], 0
	ds_read_b128 v[220:223], v173 offset:49280
	s_waitcnt lgkmcnt(9)
	v_mfma_f32_32x32x16_bf16 v[84:99], v[224:227], v[108:111], v[84:99]
	ds_read_b128 v[224:227], v173 offset:57472
	s_waitcnt lgkmcnt(9)
	v_mfma_f32_32x32x16_bf16 v[68:83], v[228:231], v[116:119], v[68:83]
	ds_read_b128 v[228:231], v174 offset:49280
	s_waitcnt lgkmcnt(9)
	v_mfma_f32_32x32x16_bf16 v[84:99], v[232:235], v[116:119], v[84:99]
	ds_read_b128 v[232:235], v174 offset:57472
	s_waitcnt lgkmcnt(9)
	v_mfma_f32_32x32x16_bf16 v[68:83], v[236:239], v[124:127], v[68:83]
	s_waitcnt lgkmcnt(8)
	v_mfma_f32_32x32x16_bf16 v[84:99], v[240:243], v[124:127], v[84:99]
	s_waitcnt lgkmcnt(7)
	v_mfma_f32_32x32x16_bf16 v[68:83], v[244:247], v[104:107], v[68:83]
	s_waitcnt lgkmcnt(6)
	v_mfma_f32_32x32x16_bf16 v[84:99], v[248:251], v[104:107], v[84:99]
	s_waitcnt lgkmcnt(5)
	v_mfma_f32_32x32x16_bf16 v[68:83], v[212:215], v[112:115], v[68:83]
	s_waitcnt lgkmcnt(4)
	v_mfma_f32_32x32x16_bf16 v[84:99], v[216:219], v[112:115], v[84:99]
	s_waitcnt lgkmcnt(3)
	v_mfma_f32_32x32x16_bf16 v[68:83], v[220:223], v[120:123], v[68:83]
	s_waitcnt lgkmcnt(2)
	v_mfma_f32_32x32x16_bf16 v[84:99], v[224:227], v[120:123], v[84:99]
	s_waitcnt lgkmcnt(1)
	v_mfma_f32_32x32x16_bf16 v[68:83], v[228:231], v[128:131], v[68:83]
	s_waitcnt lgkmcnt(0)
	s_nop 0
	v_mfma_f32_32x32x16_bf16 v[84:99], v[232:235], v[128:131], v[84:99]
	s_cbranch_scc1 .LBB0_1735
	v_sub_u32_e32 v1, v1, v137
	v_cmp_lt_i32_e32 vcc, 0, v1
	s_nop 5
	v_cndmask_b32_e32 v68, v168, v68, vcc
	v_cmp_lt_i32_e32 vcc, 32, v1
	s_nop 1
	v_cndmask_b32_e32 v84, v168, v84, vcc
	v_cmp_lt_i32_e32 vcc, 1, v1
	s_nop 1
	v_cndmask_b32_e32 v69, v168, v69, vcc
	v_cmp_lt_i32_e32 vcc, 33, v1
	s_nop 1
	v_cndmask_b32_e32 v85, v168, v85, vcc
	v_cmp_lt_i32_e32 vcc, 2, v1
	s_nop 1
	v_cndmask_b32_e32 v70, v168, v70, vcc
	v_cmp_lt_i32_e32 vcc, 34, v1
	s_nop 1
	v_cndmask_b32_e32 v86, v168, v86, vcc
	v_cmp_lt_i32_e32 vcc, 3, v1
	s_nop 1
	v_cndmask_b32_e32 v71, v168, v71, vcc
	v_cmp_lt_i32_e32 vcc, 35, v1
	s_nop 1
	v_cndmask_b32_e32 v87, v168, v87, vcc
	v_cmp_lt_i32_e32 vcc, 8, v1
	s_nop 1
	v_cndmask_b32_e32 v72, v168, v72, vcc
	v_cmp_lt_i32_e32 vcc, 40, v1
	s_nop 1
	v_cndmask_b32_e32 v88, v168, v88, vcc
	v_cmp_lt_i32_e32 vcc, 9, v1
	s_nop 1
	v_cndmask_b32_e32 v73, v168, v73, vcc
	v_cmp_lt_i32_e32 vcc, 41, v1
	s_nop 1
	v_cndmask_b32_e32 v89, v168, v89, vcc
	v_cmp_lt_i32_e32 vcc, 10, v1
	s_nop 1
	v_cndmask_b32_e32 v74, v168, v74, vcc
	v_cmp_lt_i32_e32 vcc, 42, v1
	s_nop 1
	v_cndmask_b32_e32 v90, v168, v90, vcc
	v_cmp_lt_i32_e32 vcc, 11, v1
	s_nop 1
	v_cndmask_b32_e32 v75, v168, v75, vcc
	v_cmp_lt_i32_e32 vcc, 43, v1
	s_nop 1
	v_cndmask_b32_e32 v91, v168, v91, vcc
	v_cmp_lt_i32_e32 vcc, 16, v1
	s_nop 1
	v_cndmask_b32_e32 v76, v168, v76, vcc
	v_cmp_lt_i32_e32 vcc, 48, v1
	s_nop 1
	v_cndmask_b32_e32 v92, v168, v92, vcc
	v_cmp_lt_i32_e32 vcc, 17, v1
	s_nop 1
	v_cndmask_b32_e32 v77, v168, v77, vcc
	v_cmp_lt_i32_e32 vcc, 49, v1
	s_nop 1
	v_cndmask_b32_e32 v93, v168, v93, vcc
	v_cmp_lt_i32_e32 vcc, 18, v1
	s_nop 1
	v_cndmask_b32_e32 v78, v168, v78, vcc
	v_cmp_lt_i32_e32 vcc, 50, v1
	s_nop 1
	v_cndmask_b32_e32 v94, v168, v94, vcc
	v_cmp_lt_i32_e32 vcc, 19, v1
	s_nop 1
	v_cndmask_b32_e32 v79, v168, v79, vcc
	v_cmp_lt_i32_e32 vcc, 51, v1
	s_nop 1
	v_cndmask_b32_e32 v95, v168, v95, vcc
	v_cmp_lt_i32_e32 vcc, 24, v1
	s_nop 1
	v_cndmask_b32_e32 v80, v168, v80, vcc
	v_cmp_lt_i32_e32 vcc, 56, v1
	s_nop 1
	v_cndmask_b32_e32 v96, v168, v96, vcc
	v_cmp_lt_i32_e32 vcc, 25, v1
	s_nop 1
	v_cndmask_b32_e32 v81, v168, v81, vcc
	v_cmp_lt_i32_e32 vcc, 57, v1
	s_nop 1
	v_cndmask_b32_e32 v97, v168, v97, vcc
	v_cmp_lt_i32_e32 vcc, 26, v1
	s_nop 1
	v_cndmask_b32_e32 v82, v168, v82, vcc
	v_cmp_lt_i32_e32 vcc, 58, v1
	s_nop 1
	v_cndmask_b32_e32 v98, v168, v98, vcc
	v_cmp_lt_i32_e32 vcc, 27, v1
	s_nop 1
	v_cndmask_b32_e32 v83, v168, v83, vcc
	v_cmp_lt_i32_e32 vcc, 59, v1
	s_nop 1
	v_cndmask_b32_e32 v99, v168, v99, vcc

.LBB0_1760:
	s_add_i32 s6, s1, s30
	s_cmp_lt_u32 s3, 32
	v_lshrrev_b32_e32 v1, s3, v150
	s_cselect_b64 s[12:13], -1, 0
	s_sub_i32 s3, s30, 35
	v_lshrrev_b32_e32 v2, s3, v151
	v_cndmask_b32_e64 v1, v2, v1, s[12:13]
	v_and_b32_e32 v1, 1, v1
	v_cmp_ne_u32_e32 vcc, 0, v1
	s_cmp_lg_u64 vcc, 0
	s_cselect_b64 s[20:21], -1, 0
	s_cbranch_vccz .LBB0_1765
	ds_read_b128 v[212:215], v171 offset:32768
	ds_read_b128 v[216:219], v172 offset:32768
	ds_read_b128 v[220:223], v171 offset:40960
	ds_read_b128 v[224:227], v172 offset:40960
	ds_read_b128 v[228:231], v173 offset:32768
	ds_read_b128 v[232:235], v173 offset:40960
	ds_read_b128 v[236:239], v174 offset:32768
	ds_read_b128 v[240:243], v174 offset:40960
	ds_read_b128 v[244:247], v171 offset:32896
	ds_read_b128 v[248:251], v171 offset:41088
	s_cmp_eq_u32 s6, 3
	s_cselect_b64 s[14:15], -1, 0
	v_cndmask_b32_e64 v1, 64, v163, s[14:15]
	v_cndmask_b32_e32 v1, 0, v1, vcc
	v_cmp_lt_u32_e32 vcc, 63, v1
	s_cmp_eq_u64 vcc, exec
	s_waitcnt lgkmcnt(9)
	v_mfma_f32_32x32x16_bf16 v[68:83], v[212:215], v[100:103], 0
	ds_read_b128 v[212:215], v172 offset:32896
	s_waitcnt lgkmcnt(9)
	v_mfma_f32_32x32x16_bf16 v[68:83], v[216:219], v[108:111], v[68:83]
	ds_read_b128 v[216:219], v172 offset:41088
	s_waitcnt lgkmcnt(9)
	v_mfma_f32_32x32x16_bf16 v[84:99], v[220:223], v[100:103], 0
	ds_read_b128 v[220:223], v173 offset:32896
	s_waitcnt lgkmcnt(9)
	v_mfma_f32_32x32x16_bf16 v[84:99], v[224:227], v[108:111], v[84:99]
	ds_read_b128 v[224:227], v173 offset:41088
	s_waitcnt lgkmcnt(9)
	v_mfma_f32_32x32x16_bf16 v[68:83], v[228:231], v[116:119], v[68:83]
	ds_read_b128 v[228:231], v174 offset:32896
	s_waitcnt lgkmcnt(9)
	v_mfma_f32_32x32x16_bf16 v[84:99], v[232:235], v[116:119], v[84:99]
	ds_read_b128 v[232:235], v174 offset:41088
	s_waitcnt lgkmcnt(9)
	v_mfma_f32_32x32x16_bf16 v[68:83], v[236:239], v[124:127], v[68:83]
	s_waitcnt lgkmcnt(8)
	v_mfma_f32_32x32x16_bf16 v[84:99], v[240:243], v[124:127], v[84:99]
	s_waitcnt lgkmcnt(7)
	v_mfma_f32_32x32x16_bf16 v[68:83], v[244:247], v[104:107], v[68:83]
	s_waitcnt lgkmcnt(6)
	v_mfma_f32_32x32x16_bf16 v[84:99], v[248:251], v[104:107], v[84:99]
	s_waitcnt lgkmcnt(5)
	v_mfma_f32_32x32x16_bf16 v[68:83], v[212:215], v[112:115], v[68:83]
	s_waitcnt lgkmcnt(4)
	v_mfma_f32_32x32x16_bf16 v[84:99], v[216:219], v[112:115], v[84:99]
	s_waitcnt lgkmcnt(3)
	v_mfma_f32_32x32x16_bf16 v[68:83], v[220:223], v[120:123], v[68:83]
	s_waitcnt lgkmcnt(2)
	v_mfma_f32_32x32x16_bf16 v[84:99], v[224:227], v[120:123], v[84:99]
	s_waitcnt lgkmcnt(1)
	v_mfma_f32_32x32x16_bf16 v[68:83], v[228:231], v[128:131], v[68:83]
	s_waitcnt lgkmcnt(0)
	s_nop 0
	v_mfma_f32_32x32x16_bf16 v[84:99], v[232:235], v[128:131], v[84:99]
	s_cbranch_scc1 .LBB0_1763
	v_sub_u32_e32 v1, v1, v137
	v_cmp_lt_i32_e32 vcc, 0, v1
	s_nop 5
	v_cndmask_b32_e32 v68, v168, v68, vcc
	v_cmp_lt_i32_e32 vcc, 32, v1
	s_nop 1
	v_cndmask_b32_e32 v84, v168, v84, vcc
	v_cmp_lt_i32_e32 vcc, 1, v1
	s_nop 1
	v_cndmask_b32_e32 v69, v168, v69, vcc
	v_cmp_lt_i32_e32 vcc, 33, v1
	s_nop 1
	v_cndmask_b32_e32 v85, v168, v85, vcc
	v_cmp_lt_i32_e32 vcc, 2, v1
	s_nop 1
	v_cndmask_b32_e32 v70, v168, v70, vcc
	v_cmp_lt_i32_e32 vcc, 34, v1
	s_nop 1
	v_cndmask_b32_e32 v86, v168, v86, vcc
	v_cmp_lt_i32_e32 vcc, 3, v1
	s_nop 1
	v_cndmask_b32_e32 v71, v168, v71, vcc
	v_cmp_lt_i32_e32 vcc, 35, v1
	s_nop 1
	v_cndmask_b32_e32 v87, v168, v87, vcc
	v_cmp_lt_i32_e32 vcc, 8, v1
	s_nop 1
	v_cndmask_b32_e32 v72, v168, v72, vcc
	v_cmp_lt_i32_e32 vcc, 40, v1
	s_nop 1
	v_cndmask_b32_e32 v88, v168, v88, vcc
	v_cmp_lt_i32_e32 vcc, 9, v1
	s_nop 1
	v_cndmask_b32_e32 v73, v168, v73, vcc
	v_cmp_lt_i32_e32 vcc, 41, v1
	s_nop 1
	v_cndmask_b32_e32 v89, v168, v89, vcc
	v_cmp_lt_i32_e32 vcc, 10, v1
	s_nop 1
	v_cndmask_b32_e32 v74, v168, v74, vcc
	v_cmp_lt_i32_e32 vcc, 42, v1
	s_nop 1
	v_cndmask_b32_e32 v90, v168, v90, vcc
	v_cmp_lt_i32_e32 vcc, 11, v1
	s_nop 1
	v_cndmask_b32_e32 v75, v168, v75, vcc
	v_cmp_lt_i32_e32 vcc, 43, v1
	s_nop 1
	v_cndmask_b32_e32 v91, v168, v91, vcc
	v_cmp_lt_i32_e32 vcc, 16, v1
	s_nop 1
	v_cndmask_b32_e32 v76, v168, v76, vcc
	v_cmp_lt_i32_e32 vcc, 48, v1
	s_nop 1
	v_cndmask_b32_e32 v92, v168, v92, vcc
	v_cmp_lt_i32_e32 vcc, 17, v1
	s_nop 1
	v_cndmask_b32_e32 v77, v168, v77, vcc
	v_cmp_lt_i32_e32 vcc, 49, v1
	s_nop 1
	v_cndmask_b32_e32 v93, v168, v93, vcc
	v_cmp_lt_i32_e32 vcc, 18, v1
	s_nop 1
	v_cndmask_b32_e32 v78, v168, v78, vcc
	v_cmp_lt_i32_e32 vcc, 50, v1
	s_nop 1
	v_cndmask_b32_e32 v94, v168, v94, vcc
	v_cmp_lt_i32_e32 vcc, 19, v1
	s_nop 1
	v_cndmask_b32_e32 v79, v168, v79, vcc
	v_cmp_lt_i32_e32 vcc, 51, v1
	s_nop 1
	v_cndmask_b32_e32 v95, v168, v95, vcc
	v_cmp_lt_i32_e32 vcc, 24, v1
	s_nop 1
	v_cndmask_b32_e32 v80, v168, v80, vcc
	v_cmp_lt_i32_e32 vcc, 56, v1
	s_nop 1
	v_cndmask_b32_e32 v96, v168, v96, vcc
	v_cmp_lt_i32_e32 vcc, 25, v1
	s_nop 1
	v_cndmask_b32_e32 v81, v168, v81, vcc
	v_cmp_lt_i32_e32 vcc, 57, v1
	s_nop 1
	v_cndmask_b32_e32 v97, v168, v97, vcc
	v_cmp_lt_i32_e32 vcc, 26, v1
	s_nop 1
	v_cndmask_b32_e32 v82, v168, v82, vcc
	v_cmp_lt_i32_e32 vcc, 58, v1
	s_nop 1
	v_cndmask_b32_e32 v98, v168, v98, vcc
	v_cmp_lt_i32_e32 vcc, 27, v1
	s_nop 1
	v_cndmask_b32_e32 v83, v168, v83, vcc
	v_cmp_lt_i32_e32 vcc, 59, v1
	s_nop 1
	v_cndmask_b32_e32 v99, v168, v99, vcc

.LBB0_1784:
	s_add_i32 s4, s30, -2
	v_lshrrev_b32_e32 v1, s4, v150
	s_sub_i32 s4, s30, 34
	v_lshrrev_b32_e32 v2, s4, v151
	v_cndmask_b32_e64 v1, v2, v1, s[12:13]
	v_and_b32_e32 v1, 1, v1
	v_cmp_ne_u32_e32 vcc, 0, v1
	s_cmp_lg_u64 vcc, 0
	s_cselect_b64 s[16:17], -1, 0
	s_cbranch_vccz .LBB0_1789
	ds_read_b128 v[212:215], v171 offset:49152
	ds_read_b128 v[216:219], v172 offset:49152
	ds_read_b128 v[220:223], v171 offset:57344
	ds_read_b128 v[224:227], v172 offset:57344
	ds_read_b128 v[228:231], v173 offset:49152
	ds_read_b128 v[232:235], v173 offset:57344
	ds_read_b128 v[236:239], v174 offset:49152
	ds_read_b128 v[240:243], v174 offset:57344
	ds_read_b128 v[244:247], v171 offset:49280
	ds_read_b128 v[248:251], v171 offset:57472
	s_cmp_eq_u32 s6, 2
	s_cselect_b64 s[12:13], -1, 0
	v_cndmask_b32_e64 v1, 64, v163, s[12:13]
	v_cndmask_b32_e32 v1, 0, v1, vcc
	v_cmp_lt_u32_e32 vcc, 63, v1
	s_cmp_eq_u64 vcc, exec
	s_waitcnt lgkmcnt(9)
	v_mfma_f32_32x32x16_bf16 v[68:83], v[212:215], v[100:103], 0
	ds_read_b128 v[212:215], v172 offset:49280
	s_waitcnt lgkmcnt(9)
	v_mfma_f32_32x32x16_bf16 v[68:83], v[216:219], v[108:111], v[68:83]
	ds_read_b128 v[216:219], v172 offset:57472
	s_waitcnt lgkmcnt(9)
	v_mfma_f32_32x32x16_bf16 v[84:99], v[220:223], v[100:103], 0
	ds_read_b128 v[220:223], v173 offset:49280
	s_waitcnt lgkmcnt(9)
	v_mfma_f32_32x32x16_bf16 v[84:99], v[224:227], v[108:111], v[84:99]
	ds_read_b128 v[224:227], v173 offset:57472
	s_waitcnt lgkmcnt(9)
	v_mfma_f32_32x32x16_bf16 v[68:83], v[228:231], v[116:119], v[68:83]
	ds_read_b128 v[228:231], v174 offset:49280
	s_waitcnt lgkmcnt(9)
	v_mfma_f32_32x32x16_bf16 v[84:99], v[232:235], v[116:119], v[84:99]
	ds_read_b128 v[232:235], v174 offset:57472
	s_waitcnt lgkmcnt(9)
	v_mfma_f32_32x32x16_bf16 v[68:83], v[236:239], v[124:127], v[68:83]
	s_waitcnt lgkmcnt(8)
	v_mfma_f32_32x32x16_bf16 v[84:99], v[240:243], v[124:127], v[84:99]
	s_waitcnt lgkmcnt(7)
	v_mfma_f32_32x32x16_bf16 v[68:83], v[244:247], v[104:107], v[68:83]
	s_waitcnt lgkmcnt(6)
	v_mfma_f32_32x32x16_bf16 v[84:99], v[248:251], v[104:107], v[84:99]
	s_waitcnt lgkmcnt(5)
	v_mfma_f32_32x32x16_bf16 v[68:83], v[212:215], v[112:115], v[68:83]
	s_waitcnt lgkmcnt(4)
	v_mfma_f32_32x32x16_bf16 v[84:99], v[216:219], v[112:115], v[84:99]
	s_waitcnt lgkmcnt(3)
	v_mfma_f32_32x32x16_bf16 v[68:83], v[220:223], v[120:123], v[68:83]
	s_waitcnt lgkmcnt(2)
	v_mfma_f32_32x32x16_bf16 v[84:99], v[224:227], v[120:123], v[84:99]
	s_waitcnt lgkmcnt(1)
	v_mfma_f32_32x32x16_bf16 v[68:83], v[228:231], v[128:131], v[68:83]
	s_waitcnt lgkmcnt(0)
	s_nop 0
	v_mfma_f32_32x32x16_bf16 v[84:99], v[232:235], v[128:131], v[84:99]
	s_cbranch_scc1 .LBB0_1787
	v_sub_u32_e32 v1, v1, v137
	v_cmp_lt_i32_e32 vcc, 0, v1
	s_nop 5
	v_cndmask_b32_e32 v68, v168, v68, vcc
	v_cmp_lt_i32_e32 vcc, 32, v1
	s_nop 1
	v_cndmask_b32_e32 v84, v168, v84, vcc
	v_cmp_lt_i32_e32 vcc, 1, v1
	s_nop 1
	v_cndmask_b32_e32 v69, v168, v69, vcc
	v_cmp_lt_i32_e32 vcc, 33, v1
	s_nop 1
	v_cndmask_b32_e32 v85, v168, v85, vcc
	v_cmp_lt_i32_e32 vcc, 2, v1
	s_nop 1
	v_cndmask_b32_e32 v70, v168, v70, vcc
	v_cmp_lt_i32_e32 vcc, 34, v1
	s_nop 1
	v_cndmask_b32_e32 v86, v168, v86, vcc
	v_cmp_lt_i32_e32 vcc, 3, v1
	s_nop 1
	v_cndmask_b32_e32 v71, v168, v71, vcc
	v_cmp_lt_i32_e32 vcc, 35, v1
	s_nop 1
	v_cndmask_b32_e32 v87, v168, v87, vcc
	v_cmp_lt_i32_e32 vcc, 8, v1
	s_nop 1
	v_cndmask_b32_e32 v72, v168, v72, vcc
	v_cmp_lt_i32_e32 vcc, 40, v1
	s_nop 1
	v_cndmask_b32_e32 v88, v168, v88, vcc
	v_cmp_lt_i32_e32 vcc, 9, v1
	s_nop 1
	v_cndmask_b32_e32 v73, v168, v73, vcc
	v_cmp_lt_i32_e32 vcc, 41, v1
	s_nop 1
	v_cndmask_b32_e32 v89, v168, v89, vcc
	v_cmp_lt_i32_e32 vcc, 10, v1
	s_nop 1
	v_cndmask_b32_e32 v74, v168, v74, vcc
	v_cmp_lt_i32_e32 vcc, 42, v1
	s_nop 1
	v_cndmask_b32_e32 v90, v168, v90, vcc
	v_cmp_lt_i32_e32 vcc, 11, v1
	s_nop 1
	v_cndmask_b32_e32 v75, v168, v75, vcc
	v_cmp_lt_i32_e32 vcc, 43, v1
	s_nop 1
	v_cndmask_b32_e32 v91, v168, v91, vcc
	v_cmp_lt_i32_e32 vcc, 16, v1
	s_nop 1
	v_cndmask_b32_e32 v76, v168, v76, vcc
	v_cmp_lt_i32_e32 vcc, 48, v1
	s_nop 1
	v_cndmask_b32_e32 v92, v168, v92, vcc
	v_cmp_lt_i32_e32 vcc, 17, v1
	s_nop 1
	v_cndmask_b32_e32 v77, v168, v77, vcc
	v_cmp_lt_i32_e32 vcc, 49, v1
	s_nop 1
	v_cndmask_b32_e32 v93, v168, v93, vcc
	v_cmp_lt_i32_e32 vcc, 18, v1
	s_nop 1
	v_cndmask_b32_e32 v78, v168, v78, vcc
	v_cmp_lt_i32_e32 vcc, 50, v1
	s_nop 1
	v_cndmask_b32_e32 v94, v168, v94, vcc
	v_cmp_lt_i32_e32 vcc, 19, v1
	s_nop 1
	v_cndmask_b32_e32 v79, v168, v79, vcc
	v_cmp_lt_i32_e32 vcc, 51, v1
	s_nop 1
	v_cndmask_b32_e32 v95, v168, v95, vcc
	v_cmp_lt_i32_e32 vcc, 24, v1
	s_nop 1
	v_cndmask_b32_e32 v80, v168, v80, vcc
	v_cmp_lt_i32_e32 vcc, 56, v1
	s_nop 1
	v_cndmask_b32_e32 v96, v168, v96, vcc
	v_cmp_lt_i32_e32 vcc, 25, v1
	s_nop 1
	v_cndmask_b32_e32 v81, v168, v81, vcc
	v_cmp_lt_i32_e32 vcc, 57, v1
	s_nop 1
	v_cndmask_b32_e32 v97, v168, v97, vcc
	v_cmp_lt_i32_e32 vcc, 26, v1
	s_nop 1
	v_cndmask_b32_e32 v82, v168, v82, vcc
	v_cmp_lt_i32_e32 vcc, 58, v1
	s_nop 1
	v_cndmask_b32_e32 v98, v168, v98, vcc
	v_cmp_lt_i32_e32 vcc, 27, v1
	s_nop 1
	v_cndmask_b32_e32 v83, v168, v83, vcc
	v_cmp_lt_i32_e32 vcc, 59, v1
	s_nop 1
	v_cndmask_b32_e32 v99, v168, v99, vcc

.LBB0_1808:
	s_and_b64 vcc, exec, s[12:13]
	s_cbranch_vccz .LBB0_1904
	v_and_b32_e32 v0, 16, v170
	v_cmp_ne_u32_e32 vcc, 0, v155
	v_add3_u32 v0, 0, v142, v0
	s_cmp_lg_u64 vcc, 0
	s_cselect_b64 s[10:11], -1, 0
	v_add_u32_e32 v142, v0, v143
	v_add_u32_e32 v143, v0, v152
	v_add_u32_e32 v152, v0, v153
	v_add_u32_e32 v153, v0, v154
	s_cbranch_vccz .LBB0_1815
	ds_read_b128 v[212:215], v142 offset:32768
	ds_read_b128 v[216:219], v143 offset:32768
	ds_read_b128 v[220:223], v142 offset:40960
	ds_read_b128 v[224:227], v143 offset:40960
	ds_read_b128 v[228:231], v152 offset:32768
	ds_read_b128 v[232:235], v152 offset:40960
	ds_read_b128 v[236:239], v153 offset:32768
	ds_read_b128 v[240:243], v153 offset:40960
	ds_read_b128 v[244:247], v142 offset:32896
	ds_read_b128 v[248:251], v142 offset:41088
	v_cndmask_b32_e64 v0, 64, v163, s[8:9]
	v_cndmask_b32_e32 v0, 0, v0, vcc
	v_cmp_lt_u32_e32 vcc, 63, v0
	s_cmp_eq_u64 vcc, exec
	s_waitcnt lgkmcnt(9)
	v_mfma_f32_32x32x16_bf16 v[20:35], v[212:215], v[100:103], 0
	ds_read_b128 v[212:215], v143 offset:32896
	s_waitcnt lgkmcnt(9)
	v_mfma_f32_32x32x16_bf16 v[20:35], v[216:219], v[108:111], v[20:35]
	ds_read_b128 v[216:219], v143 offset:41088
	s_waitcnt lgkmcnt(9)
	v_mfma_f32_32x32x16_bf16 v[4:19], v[220:223], v[100:103], 0
	ds_read_b128 v[220:223], v152 offset:32896
	s_waitcnt lgkmcnt(9)
	v_mfma_f32_32x32x16_bf16 v[4:19], v[224:227], v[108:111], v[4:19]
	ds_read_b128 v[224:227], v152 offset:41088
	s_waitcnt lgkmcnt(9)
	v_mfma_f32_32x32x16_bf16 v[20:35], v[228:231], v[116:119], v[20:35]
	ds_read_b128 v[228:231], v153 offset:32896
	s_waitcnt lgkmcnt(9)
	v_mfma_f32_32x32x16_bf16 v[4:19], v[232:235], v[116:119], v[4:19]
	ds_read_b128 v[232:235], v153 offset:41088
	s_waitcnt lgkmcnt(9)
	v_mfma_f32_32x32x16_bf16 v[20:35], v[236:239], v[124:127], v[20:35]
	s_waitcnt lgkmcnt(8)
	v_mfma_f32_32x32x16_bf16 v[4:19], v[240:243], v[124:127], v[4:19]
	s_waitcnt lgkmcnt(7)
	v_mfma_f32_32x32x16_bf16 v[20:35], v[244:247], v[104:107], v[20:35]
	s_waitcnt lgkmcnt(6)
	v_mfma_f32_32x32x16_bf16 v[4:19], v[248:251], v[104:107], v[4:19]
	s_waitcnt lgkmcnt(5)
	v_mfma_f32_32x32x16_bf16 v[20:35], v[212:215], v[112:115], v[20:35]
	s_waitcnt lgkmcnt(4)
	v_mfma_f32_32x32x16_bf16 v[4:19], v[216:219], v[112:115], v[4:19]
	s_waitcnt lgkmcnt(3)
	v_mfma_f32_32x32x16_bf16 v[20:35], v[220:223], v[120:123], v[20:35]
	s_waitcnt lgkmcnt(2)
	v_mfma_f32_32x32x16_bf16 v[4:19], v[224:227], v[120:123], v[4:19]
	s_waitcnt lgkmcnt(1)
	v_mfma_f32_32x32x16_bf16 v[20:35], v[228:231], v[128:131], v[20:35]
	s_waitcnt lgkmcnt(0)
	s_nop 0
	v_mfma_f32_32x32x16_bf16 v[4:19], v[232:235], v[128:131], v[4:19]
	s_cbranch_scc1 .LBB0_1812
	v_sub_u32_e32 v0, v0, v137
	v_cmp_lt_i32_e32 vcc, 0, v0
	s_nop 5
	v_cndmask_b32_e32 v20, v168, v20, vcc
	v_cmp_lt_i32_e32 vcc, 32, v0
	s_nop 1
	v_cndmask_b32_e32 v4, v168, v4, vcc
	v_cmp_lt_i32_e32 vcc, 1, v0
	s_nop 1
	v_cndmask_b32_e32 v21, v168, v21, vcc
	v_cmp_lt_i32_e32 vcc, 33, v0
	s_nop 1
	v_cndmask_b32_e32 v5, v168, v5, vcc
	v_cmp_lt_i32_e32 vcc, 2, v0
	s_nop 1
	v_cndmask_b32_e32 v22, v168, v22, vcc
	v_cmp_lt_i32_e32 vcc, 34, v0
	s_nop 1
	v_cndmask_b32_e32 v6, v168, v6, vcc
	v_cmp_lt_i32_e32 vcc, 3, v0
	s_nop 1
	v_cndmask_b32_e32 v23, v168, v23, vcc
	v_cmp_lt_i32_e32 vcc, 35, v0
	s_nop 1
	v_cndmask_b32_e32 v7, v168, v7, vcc
	v_cmp_lt_i32_e32 vcc, 8, v0
	s_nop 1
	v_cndmask_b32_e32 v24, v168, v24, vcc
	v_cmp_lt_i32_e32 vcc, 40, v0
	s_nop 1
	v_cndmask_b32_e32 v8, v168, v8, vcc
	v_cmp_lt_i32_e32 vcc, 9, v0
	s_nop 1
	v_cndmask_b32_e32 v25, v168, v25, vcc
	v_cmp_lt_i32_e32 vcc, 41, v0
	s_nop 1
	v_cndmask_b32_e32 v9, v168, v9, vcc
	v_cmp_lt_i32_e32 vcc, 10, v0
	s_nop 1
	v_cndmask_b32_e32 v26, v168, v26, vcc
	v_cmp_lt_i32_e32 vcc, 42, v0
	s_nop 1
	v_cndmask_b32_e32 v10, v168, v10, vcc
	v_cmp_lt_i32_e32 vcc, 11, v0
	s_nop 1
	v_cndmask_b32_e32 v27, v168, v27, vcc
	v_cmp_lt_i32_e32 vcc, 43, v0
	s_nop 1
	v_cndmask_b32_e32 v11, v168, v11, vcc
	v_cmp_lt_i32_e32 vcc, 16, v0
	s_nop 1
	v_cndmask_b32_e32 v28, v168, v28, vcc
	v_cmp_lt_i32_e32 vcc, 48, v0
	s_nop 1
	v_cndmask_b32_e32 v12, v168, v12, vcc
	v_cmp_lt_i32_e32 vcc, 17, v0
	s_nop 1
	v_cndmask_b32_e32 v29, v168, v29, vcc
	v_cmp_lt_i32_e32 vcc, 49, v0
	s_nop 1
	v_cndmask_b32_e32 v13, v168, v13, vcc
	v_cmp_lt_i32_e32 vcc, 18, v0
	s_nop 1
	v_cndmask_b32_e32 v30, v168, v30, vcc
	v_cmp_lt_i32_e32 vcc, 50, v0
	s_nop 1
	v_cndmask_b32_e32 v14, v168, v14, vcc
	v_cmp_lt_i32_e32 vcc, 19, v0
	s_nop 1
	v_cndmask_b32_e32 v31, v168, v31, vcc
	v_cmp_lt_i32_e32 vcc, 51, v0
	s_nop 1
	v_cndmask_b32_e32 v15, v168, v15, vcc
	v_cmp_lt_i32_e32 vcc, 24, v0
	s_nop 1
	v_cndmask_b32_e32 v32, v168, v32, vcc
	v_cmp_lt_i32_e32 vcc, 56, v0
	s_nop 1
	v_cndmask_b32_e32 v16, v168, v16, vcc
	v_cmp_lt_i32_e32 vcc, 25, v0
	s_nop 1
	v_cndmask_b32_e32 v33, v168, v33, vcc
	v_cmp_lt_i32_e32 vcc, 57, v0
	s_nop 1
	v_cndmask_b32_e32 v17, v168, v17, vcc
	v_cmp_lt_i32_e32 vcc, 26, v0
	s_nop 1
	v_cndmask_b32_e32 v34, v168, v34, vcc
	v_cmp_lt_i32_e32 vcc, 58, v0
	s_nop 1
	v_cndmask_b32_e32 v18, v168, v18, vcc
	v_cmp_lt_i32_e32 vcc, 27, v0
	s_nop 1
	v_cndmask_b32_e32 v35, v168, v35, vcc
	v_cmp_lt_i32_e32 vcc, 59, v0
	s_nop 1
	v_cndmask_b32_e32 v19, v168, v19, vcc

.LBB0_1827:
	v_bfe_u32 v1, v150, 1, 1
	v_cmp_ne_u32_e32 vcc, 0, v1
	s_cmp_lg_u64 vcc, 0
	s_cselect_b64 s[12:13], -1, 0
	s_cbranch_vccz .LBB0_1832
	ds_read_b128 v[212:215], v142 offset:49152
	ds_read_b128 v[216:219], v143 offset:49152
	ds_read_b128 v[220:223], v142 offset:57344
	ds_read_b128 v[224:227], v143 offset:57344
	ds_read_b128 v[228:231], v152 offset:49152
	ds_read_b128 v[232:235], v152 offset:57344
	ds_read_b128 v[236:239], v153 offset:49152
	ds_read_b128 v[240:243], v153 offset:57344
	ds_read_b128 v[244:247], v142 offset:49280
	ds_read_b128 v[248:251], v142 offset:57472
	v_cndmask_b32_e64 v1, 64, v163, s[10:11]
	v_cndmask_b32_e32 v1, 0, v1, vcc
	v_cmp_lt_u32_e32 vcc, 63, v1
	s_cmp_eq_u64 vcc, exec
	s_waitcnt lgkmcnt(9)
	v_mfma_f32_32x32x16_bf16 v[68:83], v[212:215], v[100:103], 0
	ds_read_b128 v[212:215], v143 offset:49280
	s_waitcnt lgkmcnt(9)
	v_mfma_f32_32x32x16_bf16 v[68:83], v[216:219], v[108:111], v[68:83]
	ds_read_b128 v[216:219], v143 offset:57472
	s_waitcnt lgkmcnt(9)
	v_mfma_f32_32x32x16_bf16 v[84:99], v[220:223], v[100:103], 0
	ds_read_b128 v[220:223], v152 offset:49280
	s_waitcnt lgkmcnt(9)
	v_mfma_f32_32x32x16_bf16 v[84:99], v[224:227], v[108:111], v[84:99]
	ds_read_b128 v[224:227], v152 offset:57472
	s_waitcnt lgkmcnt(9)
	v_mfma_f32_32x32x16_bf16 v[68:83], v[228:231], v[116:119], v[68:83]
	ds_read_b128 v[228:231], v153 offset:49280
	s_waitcnt lgkmcnt(9)
	v_mfma_f32_32x32x16_bf16 v[84:99], v[232:235], v[116:119], v[84:99]
	ds_read_b128 v[232:235], v153 offset:57472
	s_waitcnt lgkmcnt(9)
	v_mfma_f32_32x32x16_bf16 v[68:83], v[236:239], v[124:127], v[68:83]
	s_waitcnt lgkmcnt(8)
	v_mfma_f32_32x32x16_bf16 v[84:99], v[240:243], v[124:127], v[84:99]
	s_waitcnt lgkmcnt(7)
	v_mfma_f32_32x32x16_bf16 v[68:83], v[244:247], v[104:107], v[68:83]
	s_waitcnt lgkmcnt(6)
	v_mfma_f32_32x32x16_bf16 v[84:99], v[248:251], v[104:107], v[84:99]
	s_waitcnt lgkmcnt(5)
	v_mfma_f32_32x32x16_bf16 v[68:83], v[212:215], v[112:115], v[68:83]
	s_waitcnt lgkmcnt(4)
	v_mfma_f32_32x32x16_bf16 v[84:99], v[216:219], v[112:115], v[84:99]
	s_waitcnt lgkmcnt(3)
	v_mfma_f32_32x32x16_bf16 v[68:83], v[220:223], v[120:123], v[68:83]
	s_waitcnt lgkmcnt(2)
	v_mfma_f32_32x32x16_bf16 v[84:99], v[224:227], v[120:123], v[84:99]
	s_waitcnt lgkmcnt(1)
	v_mfma_f32_32x32x16_bf16 v[68:83], v[228:231], v[128:131], v[68:83]
	s_waitcnt lgkmcnt(0)
	s_nop 0
	v_mfma_f32_32x32x16_bf16 v[84:99], v[232:235], v[128:131], v[84:99]
	s_cbranch_scc1 .LBB0_1830
	v_sub_u32_e32 v1, v1, v137
	v_cmp_lt_i32_e32 vcc, 0, v1
	s_nop 5
	v_cndmask_b32_e32 v68, v168, v68, vcc
	v_cmp_lt_i32_e32 vcc, 32, v1
	s_nop 1
	v_cndmask_b32_e32 v84, v168, v84, vcc
	v_cmp_lt_i32_e32 vcc, 1, v1
	s_nop 1
	v_cndmask_b32_e32 v69, v168, v69, vcc
	v_cmp_lt_i32_e32 vcc, 33, v1
	s_nop 1
	v_cndmask_b32_e32 v85, v168, v85, vcc
	v_cmp_lt_i32_e32 vcc, 2, v1
	s_nop 1
	v_cndmask_b32_e32 v70, v168, v70, vcc
	v_cmp_lt_i32_e32 vcc, 34, v1
	s_nop 1
	v_cndmask_b32_e32 v86, v168, v86, vcc
	v_cmp_lt_i32_e32 vcc, 3, v1
	s_nop 1
	v_cndmask_b32_e32 v71, v168, v71, vcc
	v_cmp_lt_i32_e32 vcc, 35, v1
	s_nop 1
	v_cndmask_b32_e32 v87, v168, v87, vcc
	v_cmp_lt_i32_e32 vcc, 8, v1
	s_nop 1
	v_cndmask_b32_e32 v72, v168, v72, vcc
	v_cmp_lt_i32_e32 vcc, 40, v1
	s_nop 1
	v_cndmask_b32_e32 v88, v168, v88, vcc
	v_cmp_lt_i32_e32 vcc, 9, v1
	s_nop 1
	v_cndmask_b32_e32 v73, v168, v73, vcc
	v_cmp_lt_i32_e32 vcc, 41, v1
	s_nop 1
	v_cndmask_b32_e32 v89, v168, v89, vcc
	v_cmp_lt_i32_e32 vcc, 10, v1
	s_nop 1
	v_cndmask_b32_e32 v74, v168, v74, vcc
	v_cmp_lt_i32_e32 vcc, 42, v1
	s_nop 1
	v_cndmask_b32_e32 v90, v168, v90, vcc
	v_cmp_lt_i32_e32 vcc, 11, v1
	s_nop 1
	v_cndmask_b32_e32 v75, v168, v75, vcc
	v_cmp_lt_i32_e32 vcc, 43, v1
	s_nop 1
	v_cndmask_b32_e32 v91, v168, v91, vcc
	v_cmp_lt_i32_e32 vcc, 16, v1
	s_nop 1
	v_cndmask_b32_e32 v76, v168, v76, vcc
	v_cmp_lt_i32_e32 vcc, 48, v1
	s_nop 1
	v_cndmask_b32_e32 v92, v168, v92, vcc
	v_cmp_lt_i32_e32 vcc, 17, v1
	s_nop 1
	v_cndmask_b32_e32 v77, v168, v77, vcc
	v_cmp_lt_i32_e32 vcc, 49, v1
	s_nop 1
	v_cndmask_b32_e32 v93, v168, v93, vcc
	v_cmp_lt_i32_e32 vcc, 18, v1
	s_nop 1
	v_cndmask_b32_e32 v78, v168, v78, vcc
	v_cmp_lt_i32_e32 vcc, 50, v1
	s_nop 1
	v_cndmask_b32_e32 v94, v168, v94, vcc
	v_cmp_lt_i32_e32 vcc, 19, v1
	s_nop 1
	v_cndmask_b32_e32 v79, v168, v79, vcc
	v_cmp_lt_i32_e32 vcc, 51, v1
	s_nop 1
	v_cndmask_b32_e32 v95, v168, v95, vcc
	v_cmp_lt_i32_e32 vcc, 24, v1
	s_nop 1
	v_cndmask_b32_e32 v80, v168, v80, vcc
	v_cmp_lt_i32_e32 vcc, 56, v1
	s_nop 1
	v_cndmask_b32_e32 v96, v168, v96, vcc
	v_cmp_lt_i32_e32 vcc, 25, v1
	s_nop 1
	v_cndmask_b32_e32 v81, v168, v81, vcc
	v_cmp_lt_i32_e32 vcc, 57, v1
	s_nop 1
	v_cndmask_b32_e32 v97, v168, v97, vcc
	v_cmp_lt_i32_e32 vcc, 26, v1
	s_nop 1
	v_cndmask_b32_e32 v82, v168, v82, vcc
	v_cmp_lt_i32_e32 vcc, 58, v1
	s_nop 1
	v_cndmask_b32_e32 v98, v168, v98, vcc
	v_cmp_lt_i32_e32 vcc, 27, v1
	s_nop 1
	v_cndmask_b32_e32 v83, v168, v83, vcc
	v_cmp_lt_i32_e32 vcc, 59, v1
	s_nop 1
	v_cndmask_b32_e32 v99, v168, v99, vcc

.LBB0_1853:
	s_add_i32 s3, s1, s28
	s_cmp_lt_u32 s4, 32
	v_lshrrev_b32_e32 v1, s4, v150
	s_cselect_b64 s[10:11], -1, 0
	s_sub_i32 s4, s28, 34
	v_lshrrev_b32_e32 v2, s4, v151
	v_cndmask_b32_e64 v1, v2, v1, s[10:11]
	v_and_b32_e32 v1, 1, v1
	v_cmp_ne_u32_e32 vcc, 0, v1
	s_cmp_lg_u64 vcc, 0
	s_cselect_b64 s[18:19], -1, 0
	s_cbranch_vccz .LBB0_1858
	ds_read_b128 v[212:215], v142 offset:32768
	ds_read_b128 v[216:219], v143 offset:32768
	ds_read_b128 v[220:223], v142 offset:40960
	ds_read_b128 v[224:227], v143 offset:40960
	ds_read_b128 v[228:231], v152 offset:32768
	ds_read_b128 v[232:235], v152 offset:40960
	ds_read_b128 v[236:239], v153 offset:32768
	ds_read_b128 v[240:243], v153 offset:40960
	ds_read_b128 v[244:247], v142 offset:32896
	ds_read_b128 v[248:251], v142 offset:41088
	s_cmp_eq_u32 s3, 2
	s_cselect_b64 s[12:13], -1, 0
	v_cndmask_b32_e64 v1, 64, v163, s[12:13]
	v_cndmask_b32_e32 v1, 0, v1, vcc
	v_cmp_lt_u32_e32 vcc, 63, v1
	s_cmp_eq_u64 vcc, exec
	s_waitcnt lgkmcnt(9)
	v_mfma_f32_32x32x16_bf16 v[68:83], v[212:215], v[100:103], 0
	ds_read_b128 v[212:215], v143 offset:32896
	s_waitcnt lgkmcnt(9)
	v_mfma_f32_32x32x16_bf16 v[68:83], v[216:219], v[108:111], v[68:83]
	ds_read_b128 v[216:219], v143 offset:41088
	s_waitcnt lgkmcnt(9)
	v_mfma_f32_32x32x16_bf16 v[84:99], v[220:223], v[100:103], 0
	ds_read_b128 v[220:223], v152 offset:32896
	s_waitcnt lgkmcnt(9)
	v_mfma_f32_32x32x16_bf16 v[84:99], v[224:227], v[108:111], v[84:99]
	ds_read_b128 v[224:227], v152 offset:41088
	s_waitcnt lgkmcnt(9)
	v_mfma_f32_32x32x16_bf16 v[68:83], v[228:231], v[116:119], v[68:83]
	ds_read_b128 v[228:231], v153 offset:32896
	s_waitcnt lgkmcnt(9)
	v_mfma_f32_32x32x16_bf16 v[84:99], v[232:235], v[116:119], v[84:99]
	ds_read_b128 v[232:235], v153 offset:41088
	s_waitcnt lgkmcnt(9)
	v_mfma_f32_32x32x16_bf16 v[68:83], v[236:239], v[124:127], v[68:83]
	s_waitcnt lgkmcnt(8)
	v_mfma_f32_32x32x16_bf16 v[84:99], v[240:243], v[124:127], v[84:99]
	s_waitcnt lgkmcnt(7)
	v_mfma_f32_32x32x16_bf16 v[68:83], v[244:247], v[104:107], v[68:83]
	s_waitcnt lgkmcnt(6)
	v_mfma_f32_32x32x16_bf16 v[84:99], v[248:251], v[104:107], v[84:99]
	s_waitcnt lgkmcnt(5)
	v_mfma_f32_32x32x16_bf16 v[68:83], v[212:215], v[112:115], v[68:83]
	s_waitcnt lgkmcnt(4)
	v_mfma_f32_32x32x16_bf16 v[84:99], v[216:219], v[112:115], v[84:99]
	s_waitcnt lgkmcnt(3)
	v_mfma_f32_32x32x16_bf16 v[68:83], v[220:223], v[120:123], v[68:83]
	s_waitcnt lgkmcnt(2)
	v_mfma_f32_32x32x16_bf16 v[84:99], v[224:227], v[120:123], v[84:99]
	s_waitcnt lgkmcnt(1)
	v_mfma_f32_32x32x16_bf16 v[68:83], v[228:231], v[128:131], v[68:83]
	s_waitcnt lgkmcnt(0)
	s_nop 0
	v_mfma_f32_32x32x16_bf16 v[84:99], v[232:235], v[128:131], v[84:99]
	s_cbranch_scc1 .LBB0_1856
	v_sub_u32_e32 v1, v1, v137
	v_cmp_lt_i32_e32 vcc, 0, v1
	s_nop 5
	v_cndmask_b32_e32 v68, v168, v68, vcc
	v_cmp_lt_i32_e32 vcc, 32, v1
	s_nop 1
	v_cndmask_b32_e32 v84, v168, v84, vcc
	v_cmp_lt_i32_e32 vcc, 1, v1
	s_nop 1
	v_cndmask_b32_e32 v69, v168, v69, vcc
	v_cmp_lt_i32_e32 vcc, 33, v1
	s_nop 1
	v_cndmask_b32_e32 v85, v168, v85, vcc
	v_cmp_lt_i32_e32 vcc, 2, v1
	s_nop 1
	v_cndmask_b32_e32 v70, v168, v70, vcc
	v_cmp_lt_i32_e32 vcc, 34, v1
	s_nop 1
	v_cndmask_b32_e32 v86, v168, v86, vcc
	v_cmp_lt_i32_e32 vcc, 3, v1
	s_nop 1
	v_cndmask_b32_e32 v71, v168, v71, vcc
	v_cmp_lt_i32_e32 vcc, 35, v1
	s_nop 1
	v_cndmask_b32_e32 v87, v168, v87, vcc
	v_cmp_lt_i32_e32 vcc, 8, v1
	s_nop 1
	v_cndmask_b32_e32 v72, v168, v72, vcc
	v_cmp_lt_i32_e32 vcc, 40, v1
	s_nop 1
	v_cndmask_b32_e32 v88, v168, v88, vcc
	v_cmp_lt_i32_e32 vcc, 9, v1
	s_nop 1
	v_cndmask_b32_e32 v73, v168, v73, vcc
	v_cmp_lt_i32_e32 vcc, 41, v1
	s_nop 1
	v_cndmask_b32_e32 v89, v168, v89, vcc
	v_cmp_lt_i32_e32 vcc, 10, v1
	s_nop 1
	v_cndmask_b32_e32 v74, v168, v74, vcc
	v_cmp_lt_i32_e32 vcc, 42, v1
	s_nop 1
	v_cndmask_b32_e32 v90, v168, v90, vcc
	v_cmp_lt_i32_e32 vcc, 11, v1
	s_nop 1
	v_cndmask_b32_e32 v75, v168, v75, vcc
	v_cmp_lt_i32_e32 vcc, 43, v1
	s_nop 1
	v_cndmask_b32_e32 v91, v168, v91, vcc
	v_cmp_lt_i32_e32 vcc, 16, v1
	s_nop 1
	v_cndmask_b32_e32 v76, v168, v76, vcc
	v_cmp_lt_i32_e32 vcc, 48, v1
	s_nop 1
	v_cndmask_b32_e32 v92, v168, v92, vcc
	v_cmp_lt_i32_e32 vcc, 17, v1
	s_nop 1
	v_cndmask_b32_e32 v77, v168, v77, vcc
	v_cmp_lt_i32_e32 vcc, 49, v1
	s_nop 1
	v_cndmask_b32_e32 v93, v168, v93, vcc
	v_cmp_lt_i32_e32 vcc, 18, v1
	s_nop 1
	v_cndmask_b32_e32 v78, v168, v78, vcc
	v_cmp_lt_i32_e32 vcc, 50, v1
	s_nop 1
	v_cndmask_b32_e32 v94, v168, v94, vcc
	v_cmp_lt_i32_e32 vcc, 19, v1
	s_nop 1
	v_cndmask_b32_e32 v79, v168, v79, vcc
	v_cmp_lt_i32_e32 vcc, 51, v1
	s_nop 1
	v_cndmask_b32_e32 v95, v168, v95, vcc
	v_cmp_lt_i32_e32 vcc, 24, v1
	s_nop 1
	v_cndmask_b32_e32 v80, v168, v80, vcc
	v_cmp_lt_i32_e32 vcc, 56, v1
	s_nop 1
	v_cndmask_b32_e32 v96, v168, v96, vcc
	v_cmp_lt_i32_e32 vcc, 25, v1
	s_nop 1
	v_cndmask_b32_e32 v81, v168, v81, vcc
	v_cmp_lt_i32_e32 vcc, 57, v1
	s_nop 1
	v_cndmask_b32_e32 v97, v168, v97, vcc
	v_cmp_lt_i32_e32 vcc, 26, v1
	s_nop 1
	v_cndmask_b32_e32 v82, v168, v82, vcc
	v_cmp_lt_i32_e32 vcc, 58, v1
	s_nop 1
	v_cndmask_b32_e32 v98, v168, v98, vcc
	v_cmp_lt_i32_e32 vcc, 27, v1
	s_nop 1
	v_cndmask_b32_e32 v83, v168, v83, vcc
	v_cmp_lt_i32_e32 vcc, 59, v1
	s_nop 1
	v_cndmask_b32_e32 v99, v168, v99, vcc

.LBB0_1877:
	s_add_i32 s4, s28, -1
	v_lshrrev_b32_e32 v1, s4, v150
	s_sub_i32 s4, s28, 33
	v_lshrrev_b32_e32 v2, s4, v151
	v_cndmask_b32_e64 v1, v2, v1, s[10:11]
	v_and_b32_e32 v1, 1, v1
	v_cmp_ne_u32_e32 vcc, 0, v1
	s_cmp_lg_u64 vcc, 0
	s_cselect_b64 s[12:13], -1, 0
	s_cbranch_vccz .LBB0_1882
	ds_read_b128 v[212:215], v142 offset:49152
	ds_read_b128 v[216:219], v143 offset:49152
	ds_read_b128 v[220:223], v142 offset:57344
	ds_read_b128 v[224:227], v143 offset:57344
	ds_read_b128 v[228:231], v152 offset:49152
	ds_read_b128 v[232:235], v152 offset:57344
	ds_read_b128 v[236:239], v153 offset:49152
	ds_read_b128 v[240:243], v153 offset:57344
	ds_read_b128 v[244:247], v142 offset:49280
	ds_read_b128 v[248:251], v142 offset:57472
	s_cmp_eq_u32 s3, 1
	s_cselect_b64 s[10:11], -1, 0
	v_cndmask_b32_e64 v1, 64, v163, s[10:11]
	v_cndmask_b32_e32 v1, 0, v1, vcc
	v_cmp_lt_u32_e32 vcc, 63, v1
	s_cmp_eq_u64 vcc, exec
	s_waitcnt lgkmcnt(9)
	v_mfma_f32_32x32x16_bf16 v[68:83], v[212:215], v[100:103], 0
	ds_read_b128 v[212:215], v143 offset:49280
	s_waitcnt lgkmcnt(9)
	v_mfma_f32_32x32x16_bf16 v[68:83], v[216:219], v[108:111], v[68:83]
	ds_read_b128 v[216:219], v143 offset:57472
	s_waitcnt lgkmcnt(9)
	v_mfma_f32_32x32x16_bf16 v[84:99], v[220:223], v[100:103], 0
	ds_read_b128 v[220:223], v152 offset:49280
	s_waitcnt lgkmcnt(9)
	v_mfma_f32_32x32x16_bf16 v[84:99], v[224:227], v[108:111], v[84:99]
	ds_read_b128 v[224:227], v152 offset:57472
	s_waitcnt lgkmcnt(9)
	v_mfma_f32_32x32x16_bf16 v[68:83], v[228:231], v[116:119], v[68:83]
	ds_read_b128 v[228:231], v153 offset:49280
	s_waitcnt lgkmcnt(9)
	v_mfma_f32_32x32x16_bf16 v[84:99], v[232:235], v[116:119], v[84:99]
	ds_read_b128 v[232:235], v153 offset:57472
	s_waitcnt lgkmcnt(9)
	v_mfma_f32_32x32x16_bf16 v[68:83], v[236:239], v[124:127], v[68:83]
	s_waitcnt lgkmcnt(8)
	v_mfma_f32_32x32x16_bf16 v[84:99], v[240:243], v[124:127], v[84:99]
	s_waitcnt lgkmcnt(7)
	v_mfma_f32_32x32x16_bf16 v[68:83], v[244:247], v[104:107], v[68:83]
	s_waitcnt lgkmcnt(6)
	v_mfma_f32_32x32x16_bf16 v[84:99], v[248:251], v[104:107], v[84:99]
	s_waitcnt lgkmcnt(5)
	v_mfma_f32_32x32x16_bf16 v[68:83], v[212:215], v[112:115], v[68:83]
	s_waitcnt lgkmcnt(4)
	v_mfma_f32_32x32x16_bf16 v[84:99], v[216:219], v[112:115], v[84:99]
	s_waitcnt lgkmcnt(3)
	v_mfma_f32_32x32x16_bf16 v[68:83], v[220:223], v[120:123], v[68:83]
	s_waitcnt lgkmcnt(2)
	v_mfma_f32_32x32x16_bf16 v[84:99], v[224:227], v[120:123], v[84:99]
	s_waitcnt lgkmcnt(1)
	v_mfma_f32_32x32x16_bf16 v[68:83], v[228:231], v[128:131], v[68:83]
	s_waitcnt lgkmcnt(0)
	s_nop 0
	v_mfma_f32_32x32x16_bf16 v[84:99], v[232:235], v[128:131], v[84:99]
	s_cbranch_scc1 .LBB0_1880
	v_sub_u32_e32 v1, v1, v137
	v_cmp_lt_i32_e32 vcc, 0, v1
	s_nop 5
	v_cndmask_b32_e32 v68, v168, v68, vcc
	v_cmp_lt_i32_e32 vcc, 32, v1
	s_nop 1
	v_cndmask_b32_e32 v84, v168, v84, vcc
	v_cmp_lt_i32_e32 vcc, 1, v1
	s_nop 1
	v_cndmask_b32_e32 v69, v168, v69, vcc
	v_cmp_lt_i32_e32 vcc, 33, v1
	s_nop 1
	v_cndmask_b32_e32 v85, v168, v85, vcc
	v_cmp_lt_i32_e32 vcc, 2, v1
	s_nop 1
	v_cndmask_b32_e32 v70, v168, v70, vcc
	v_cmp_lt_i32_e32 vcc, 34, v1
	s_nop 1
	v_cndmask_b32_e32 v86, v168, v86, vcc
	v_cmp_lt_i32_e32 vcc, 3, v1
	s_nop 1
	v_cndmask_b32_e32 v71, v168, v71, vcc
	v_cmp_lt_i32_e32 vcc, 35, v1
	s_nop 1
	v_cndmask_b32_e32 v87, v168, v87, vcc
	v_cmp_lt_i32_e32 vcc, 8, v1
	s_nop 1
	v_cndmask_b32_e32 v72, v168, v72, vcc
	v_cmp_lt_i32_e32 vcc, 40, v1
	s_nop 1
	v_cndmask_b32_e32 v88, v168, v88, vcc
	v_cmp_lt_i32_e32 vcc, 9, v1
	s_nop 1
	v_cndmask_b32_e32 v73, v168, v73, vcc
	v_cmp_lt_i32_e32 vcc, 41, v1
	s_nop 1
	v_cndmask_b32_e32 v89, v168, v89, vcc
	v_cmp_lt_i32_e32 vcc, 10, v1
	s_nop 1
	v_cndmask_b32_e32 v74, v168, v74, vcc
	v_cmp_lt_i32_e32 vcc, 42, v1
	s_nop 1
	v_cndmask_b32_e32 v90, v168, v90, vcc
	v_cmp_lt_i32_e32 vcc, 11, v1
	s_nop 1
	v_cndmask_b32_e32 v75, v168, v75, vcc
	v_cmp_lt_i32_e32 vcc, 43, v1
	s_nop 1
	v_cndmask_b32_e32 v91, v168, v91, vcc
	v_cmp_lt_i32_e32 vcc, 16, v1
	s_nop 1
	v_cndmask_b32_e32 v76, v168, v76, vcc
	v_cmp_lt_i32_e32 vcc, 48, v1
	s_nop 1
	v_cndmask_b32_e32 v92, v168, v92, vcc
	v_cmp_lt_i32_e32 vcc, 17, v1
	s_nop 1
	v_cndmask_b32_e32 v77, v168, v77, vcc
	v_cmp_lt_i32_e32 vcc, 49, v1
	s_nop 1
	v_cndmask_b32_e32 v93, v168, v93, vcc
	v_cmp_lt_i32_e32 vcc, 18, v1
	s_nop 1
	v_cndmask_b32_e32 v78, v168, v78, vcc
	v_cmp_lt_i32_e32 vcc, 50, v1
	s_nop 1
	v_cndmask_b32_e32 v94, v168, v94, vcc
	v_cmp_lt_i32_e32 vcc, 19, v1
	s_nop 1
	v_cndmask_b32_e32 v79, v168, v79, vcc
	v_cmp_lt_i32_e32 vcc, 51, v1
	s_nop 1
	v_cndmask_b32_e32 v95, v168, v95, vcc
	v_cmp_lt_i32_e32 vcc, 24, v1
	s_nop 1
	v_cndmask_b32_e32 v80, v168, v80, vcc
	v_cmp_lt_i32_e32 vcc, 56, v1
	s_nop 1
	v_cndmask_b32_e32 v96, v168, v96, vcc
	v_cmp_lt_i32_e32 vcc, 25, v1
	s_nop 1
	v_cndmask_b32_e32 v81, v168, v81, vcc
	v_cmp_lt_i32_e32 vcc, 57, v1
	s_nop 1
	v_cndmask_b32_e32 v97, v168, v97, vcc
	v_cmp_lt_i32_e32 vcc, 26, v1
	s_nop 1
	v_cndmask_b32_e32 v82, v168, v82, vcc
	v_cmp_lt_i32_e32 vcc, 58, v1
	s_nop 1
	v_cndmask_b32_e32 v98, v168, v98, vcc
	v_cmp_lt_i32_e32 vcc, 27, v1
	s_nop 1
	v_cndmask_b32_e32 v83, v168, v83, vcc
	v_cmp_lt_i32_e32 vcc, 59, v1
	s_nop 1
	v_cndmask_b32_e32 v99, v168, v99, vcc

.LBB0_1912:
	s_or_b64 exec, exec, s[8:9]
	v_mov_b32_e32 v1, v156
	s_nop 0
	v_bfe_u32 v69, v1, 5, 1
	v_and_b32_e32 v68, 31, v1
	v_cmp_eq_u32_e32 vcc, 0, v69
	s_and_saveexec_b64 s[4:5], vcc
	v_lshl_add_u32 v1, v68, 2, s45
	ds_write_b32 v1, v0
	s_or_b64 exec, exec, s[4:5]
	v_lshlrev_b32_e32 v1, 2, v69
	v_lshl_add_u32 v0, v68, 1, s72
	v_or_b32_e32 v73, s48, v1
	s_waitcnt lgkmcnt(0)
	v_lshl_add_u32 v72, v69, 4, s45
	v_mad_u64_u32 v[74:75], s[4:5], v73, s71, v[0:1]
	ds_read_b128 v[68:71], v72
	ds_read_u16 v73, v74
	v_writelane_b32 v255, s52, 16
	s_sub_i32 s91, s89, s79
	s_mov_b64 s[8:9], -1
	v_writelane_b32 v255, s53, 17
	s_waitcnt lgkmcnt(0)
	v_lshlrev_b32_e32 v73, 16, v73
	v_fmac_f32_e32 v73, v20, v68
	v_bfe_u32 v20, v73, 16, 1
	v_add3_u32 v20, v73, v20, s96
	ds_write_b16_d16_hi v74, v20
	ds_read_u16 v20, v74 offset:64
	v_writelane_b32 v255, s54, 18
	v_writelane_b32 v255, s55, 19
	s_and_b64 vcc, exec, s[50:51]
	v_writelane_b32 v255, s72, 20
	s_waitcnt lgkmcnt(0)
	v_lshlrev_b32_e32 v20, 16, v20
	v_fmac_f32_e32 v20, v36, v68
	v_bfe_u32 v36, v20, 16, 1
	v_add3_u32 v20, v20, v36, s96
	ds_write_b16_d16_hi v74, v20 offset:64
	ds_read_u16 v20, v74 offset:128
	s_waitcnt lgkmcnt(0)
	v_lshlrev_b32_e32 v20, 16, v20
	v_fmac_f32_e32 v20, v52, v68
	v_bfe_u32 v36, v20, 16, 1
	v_add3_u32 v20, v20, v36, s96
	ds_write_b16_d16_hi v74, v20 offset:128
	ds_read_u16 v20, v74 offset:192
	s_waitcnt lgkmcnt(0)
	v_lshlrev_b32_e32 v20, 16, v20
	v_fmac_f32_e32 v20, v4, v68
	v_bfe_u32 v4, v20, 16, 1
	v_add3_u32 v4, v20, v4, s96
	ds_write_b16_d16_hi v74, v4 offset:192
	v_or_b32_e32 v4, s49, v1
	v_mad_u64_u32 v[74:75], s[4:5], v4, s71, v[0:1]
	ds_read_u16 v4, v74
	s_waitcnt lgkmcnt(0)
	v_lshlrev_b32_e32 v4, 16, v4
	v_fmac_f32_e32 v4, v21, v69
	v_bfe_u32 v20, v4, 16, 1
	v_add3_u32 v4, v4, v20, s96
	ds_write_b16_d16_hi v74, v4
	ds_read_u16 v4, v74 offset:64
	s_waitcnt lgkmcnt(0)
	v_lshlrev_b32_e32 v4, 16, v4
	v_fmac_f32_e32 v4, v37, v69
	v_bfe_u32 v20, v4, 16, 1
	v_add3_u32 v4, v4, v20, s96
	ds_write_b16_d16_hi v74, v4 offset:64
	ds_read_u16 v4, v74 offset:128
	s_waitcnt lgkmcnt(0)
	v_lshlrev_b32_e32 v4, 16, v4
	v_fmac_f32_e32 v4, v53, v69
	v_bfe_u32 v20, v4, 16, 1
	v_add3_u32 v4, v4, v20, s96
	ds_write_b16_d16_hi v74, v4 offset:128
	ds_read_u16 v4, v74 offset:192
	s_waitcnt lgkmcnt(0)
	v_lshlrev_b32_e32 v4, 16, v4
	v_fmac_f32_e32 v4, v5, v69
	v_bfe_u32 v5, v4, 16, 1
	v_add3_u32 v4, v4, v5, s96
	ds_write_b16_d16_hi v74, v4 offset:192
	v_or_b32_e32 v4, s56, v1
	v_mad_u64_u32 v[4:5], s[4:5], v4, s71, v[0:1]
	ds_read_u16 v5, v4
	s_waitcnt lgkmcnt(0)
	v_lshlrev_b32_e32 v5, 16, v5
	v_fmac_f32_e32 v5, v22, v70
	v_bfe_u32 v20, v5, 16, 1
	v_add3_u32 v5, v5, v20, s96
	ds_write_b16_d16_hi v4, v5
	ds_read_u16 v5, v4 offset:64
	s_waitcnt lgkmcnt(0)
	v_lshlrev_b32_e32 v5, 16, v5
	v_fmac_f32_e32 v5, v38, v70
	v_bfe_u32 v20, v5, 16, 1
	v_add3_u32 v5, v5, v20, s96
	ds_write_b16_d16_hi v4, v5 offset:64
	ds_read_u16 v5, v4 offset:128
	s_waitcnt lgkmcnt(0)
	v_lshlrev_b32_e32 v5, 16, v5
	v_fmac_f32_e32 v5, v54, v70
	v_bfe_u32 v20, v5, 16, 1
	v_add3_u32 v5, v5, v20, s96
	ds_write_b16_d16_hi v4, v5 offset:128
	ds_read_u16 v5, v4 offset:192
	v_or_b32_e32 v20, s58, v1
	v_mad_u64_u32 v[20:21], s[4:5], v20, s71, v[0:1]
	ds_read_u16 v21, v20
	s_waitcnt lgkmcnt(1)
	v_lshlrev_b32_e32 v5, 16, v5
	v_fmac_f32_e32 v5, v6, v70
	v_bfe_u32 v6, v5, 16, 1
	v_add3_u32 v5, v5, v6, s96
	ds_write_b16_d16_hi v4, v5 offset:192
	v_or_b32_e32 v4, s57, v1
	v_mad_u64_u32 v[4:5], s[4:5], v4, s71, v[0:1]
	ds_read_u16 v5, v4
	s_waitcnt lgkmcnt(2)
	v_lshlrev_b32_e32 v21, 16, v21
	s_waitcnt lgkmcnt(0)
	v_lshlrev_b32_e32 v5, 16, v5
	v_fmac_f32_e32 v5, v23, v71
	v_bfe_u32 v6, v5, 16, 1
	v_add3_u32 v5, v5, v6, s96
	ds_write_b16_d16_hi v4, v5
	ds_read_u16 v5, v4 offset:64
	s_waitcnt lgkmcnt(0)
	v_lshlrev_b32_e32 v5, 16, v5
	v_fmac_f32_e32 v5, v39, v71
	v_bfe_u32 v6, v5, 16, 1
	v_add3_u32 v5, v5, v6, s96
	ds_write_b16_d16_hi v4, v5 offset:64
	ds_read_u16 v5, v4 offset:128
	s_waitcnt lgkmcnt(0)
	v_lshlrev_b32_e32 v5, 16, v5
	v_fmac_f32_e32 v5, v55, v71
	v_bfe_u32 v6, v5, 16, 1
	v_add3_u32 v5, v5, v6, s96
	ds_write_b16_d16_hi v4, v5 offset:128
	ds_read_u16 v5, v4 offset:192
	s_waitcnt lgkmcnt(0)
	v_lshlrev_b32_e32 v5, 16, v5
	v_fmac_f32_e32 v5, v7, v71
	v_bfe_u32 v6, v5, 16, 1
	v_add3_u32 v5, v5, v6, s96
	ds_write_b16_d16_hi v4, v5 offset:192
	ds_read_b128 v[4:7], v72 offset:32
	s_waitcnt lgkmcnt(0)
	v_fmac_f32_e32 v21, v24, v4
	v_bfe_u32 v22, v21, 16, 1
	v_add3_u32 v21, v21, v22, s96
	ds_write_b16_d16_hi v20, v21
	ds_read_u16 v21, v20 offset:64
	s_waitcnt lgkmcnt(0)
	v_lshlrev_b32_e32 v21, 16, v21
	v_fmac_f32_e32 v21, v40, v4
	v_bfe_u32 v22, v21, 16, 1
	v_add3_u32 v21, v21, v22, s96
	ds_write_b16_d16_hi v20, v21 offset:64
	ds_read_u16 v21, v20 offset:128
	s_waitcnt lgkmcnt(0)
	v_lshlrev_b32_e32 v21, 16, v21
	v_fmac_f32_e32 v21, v56, v4
	v_bfe_u32 v22, v21, 16, 1
	v_add3_u32 v21, v21, v22, s96
	ds_write_b16_d16_hi v20, v21 offset:128
	ds_read_u16 v21, v20 offset:192
	s_waitcnt lgkmcnt(0)
	v_lshlrev_b32_e32 v21, 16, v21
	v_fmac_f32_e32 v21, v8, v4
	v_bfe_u32 v4, v21, 16, 1
	v_add3_u32 v4, v21, v4, s96
	ds_write_b16_d16_hi v20, v4 offset:192
	v_or_b32_e32 v4, s59, v1
	v_mad_u64_u32 v[20:21], s[4:5], v4, s71, v[0:1]
	ds_read_u16 v4, v20
	s_waitcnt lgkmcnt(0)
	v_lshlrev_b32_e32 v4, 16, v4
	v_fmac_f32_e32 v4, v25, v5
	v_bfe_u32 v8, v4, 16, 1
	v_add3_u32 v4, v4, v8, s96
	ds_write_b16_d16_hi v20, v4
	ds_read_u16 v4, v20 offset:64
	s_waitcnt lgkmcnt(0)
	v_lshlrev_b32_e32 v4, 16, v4
	v_fmac_f32_e32 v4, v41, v5
	v_bfe_u32 v8, v4, 16, 1
	v_add3_u32 v4, v4, v8, s96
	ds_write_b16_d16_hi v20, v4 offset:64
	ds_read_u16 v4, v20 offset:128
	s_waitcnt lgkmcnt(0)
	v_lshlrev_b32_e32 v4, 16, v4
	v_fmac_f32_e32 v4, v57, v5
	v_bfe_u32 v8, v4, 16, 1
	v_add3_u32 v4, v4, v8, s96
	ds_write_b16_d16_hi v20, v4 offset:128
	ds_read_u16 v4, v20 offset:192
	s_waitcnt lgkmcnt(0)
	v_lshlrev_b32_e32 v4, 16, v4
	v_fmac_f32_e32 v4, v9, v5
	v_bfe_u32 v5, v4, 16, 1
	v_add3_u32 v4, v4, v5, s96
	ds_write_b16_d16_hi v20, v4 offset:192
	v_or_b32_e32 v4, s60, v1
	v_mad_u64_u32 v[4:5], s[4:5], v4, s71, v[0:1]
	ds_read_u16 v5, v4
	s_waitcnt lgkmcnt(0)
	v_lshlrev_b32_e32 v5, 16, v5
	v_fmac_f32_e32 v5, v26, v6
	v_bfe_u32 v8, v5, 16, 1
	v_add3_u32 v5, v5, v8, s96
	ds_write_b16_d16_hi v4, v5
	ds_read_u16 v5, v4 offset:64
	s_waitcnt lgkmcnt(0)
	v_lshlrev_b32_e32 v5, 16, v5
	v_fmac_f32_e32 v5, v42, v6
	v_bfe_u32 v8, v5, 16, 1
	v_add3_u32 v5, v5, v8, s96
	ds_write_b16_d16_hi v4, v5 offset:64
	ds_read_u16 v5, v4 offset:128
	s_waitcnt lgkmcnt(0)
	v_lshlrev_b32_e32 v5, 16, v5
	v_fmac_f32_e32 v5, v58, v6
	v_bfe_u32 v8, v5, 16, 1
	v_add3_u32 v5, v5, v8, s96
	ds_write_b16_d16_hi v4, v5 offset:128
	ds_read_u16 v5, v4 offset:192
	v_or_b32_e32 v8, s62, v1
	v_mad_u64_u32 v[8:9], s[4:5], v8, s71, v[0:1]
	ds_read_u16 v9, v8
	s_waitcnt lgkmcnt(1)
	v_lshlrev_b32_e32 v5, 16, v5
	v_fmac_f32_e32 v5, v10, v6
	v_bfe_u32 v6, v5, 16, 1
	v_add3_u32 v5, v5, v6, s96
	ds_write_b16_d16_hi v4, v5 offset:192
	v_or_b32_e32 v4, s61, v1
	v_mad_u64_u32 v[4:5], s[4:5], v4, s71, v[0:1]
	ds_read_u16 v5, v4
	s_waitcnt lgkmcnt(2)
	v_lshlrev_b32_e32 v9, 16, v9
	s_waitcnt lgkmcnt(0)
	v_lshlrev_b32_e32 v5, 16, v5
	v_fmac_f32_e32 v5, v27, v7
	v_bfe_u32 v6, v5, 16, 1
	v_add3_u32 v5, v5, v6, s96
	ds_write_b16_d16_hi v4, v5
	ds_read_u16 v5, v4 offset:64
	s_waitcnt lgkmcnt(0)
	v_lshlrev_b32_e32 v5, 16, v5
	v_fmac_f32_e32 v5, v43, v7
	v_bfe_u32 v6, v5, 16, 1
	v_add3_u32 v5, v5, v6, s96
	ds_write_b16_d16_hi v4, v5 offset:64
	ds_read_u16 v5, v4 offset:128
	s_waitcnt lgkmcnt(0)
	v_lshlrev_b32_e32 v5, 16, v5
	v_fmac_f32_e32 v5, v59, v7
	v_bfe_u32 v6, v5, 16, 1
	v_add3_u32 v5, v5, v6, s96
	ds_write_b16_d16_hi v4, v5 offset:128
	ds_read_u16 v5, v4 offset:192
	s_waitcnt lgkmcnt(0)
	v_lshlrev_b32_e32 v5, 16, v5
	v_fmac_f32_e32 v5, v11, v7
	v_bfe_u32 v6, v5, 16, 1
	v_add3_u32 v5, v5, v6, s96
	ds_write_b16_d16_hi v4, v5 offset:192
	ds_read_b128 v[4:7], v72 offset:64
	s_waitcnt lgkmcnt(0)
	v_fmac_f32_e32 v9, v28, v4
	v_bfe_u32 v10, v9, 16, 1
	v_add3_u32 v9, v9, v10, s96
	ds_write_b16_d16_hi v8, v9
	ds_read_u16 v9, v8 offset:64
	s_waitcnt lgkmcnt(0)
	v_lshlrev_b32_e32 v9, 16, v9
	v_fmac_f32_e32 v9, v44, v4
	v_bfe_u32 v10, v9, 16, 1
	v_add3_u32 v9, v9, v10, s96
	ds_write_b16_d16_hi v8, v9 offset:64
	ds_read_u16 v9, v8 offset:128
	s_waitcnt lgkmcnt(0)
	v_lshlrev_b32_e32 v9, 16, v9
	v_fmac_f32_e32 v9, v60, v4
	v_bfe_u32 v10, v9, 16, 1
	v_add3_u32 v9, v9, v10, s96
	ds_write_b16_d16_hi v8, v9 offset:128
	ds_read_u16 v9, v8 offset:192
	s_waitcnt lgkmcnt(0)
	v_lshlrev_b32_e32 v9, 16, v9
	v_fmac_f32_e32 v9, v12, v4
	v_bfe_u32 v4, v9, 16, 1
	v_add3_u32 v4, v9, v4, s96
	ds_write_b16_d16_hi v8, v4 offset:192
	v_or_b32_e32 v4, s63, v1
	v_mad_u64_u32 v[8:9], s[4:5], v4, s71, v[0:1]
	ds_read_u16 v4, v8
	s_waitcnt lgkmcnt(0)
	v_lshlrev_b32_e32 v4, 16, v4
	v_fmac_f32_e32 v4, v29, v5
	v_bfe_u32 v9, v4, 16, 1
	v_add3_u32 v4, v4, v9, s96
	ds_write_b16_d16_hi v8, v4
	ds_read_u16 v4, v8 offset:64
	s_waitcnt lgkmcnt(0)
	v_lshlrev_b32_e32 v4, 16, v4
	v_fmac_f32_e32 v4, v45, v5
	v_bfe_u32 v9, v4, 16, 1
	v_add3_u32 v4, v4, v9, s96
	ds_write_b16_d16_hi v8, v4 offset:64
	ds_read_u16 v4, v8 offset:128
	s_waitcnt lgkmcnt(0)
	v_lshlrev_b32_e32 v4, 16, v4
	v_fmac_f32_e32 v4, v61, v5
	v_bfe_u32 v9, v4, 16, 1
	v_add3_u32 v4, v4, v9, s96
	ds_write_b16_d16_hi v8, v4 offset:128
	ds_read_u16 v4, v8 offset:192
	s_waitcnt lgkmcnt(0)
	v_lshlrev_b32_e32 v4, 16, v4
	v_fmac_f32_e32 v4, v13, v5
	v_bfe_u32 v5, v4, 16, 1
	v_add3_u32 v4, v4, v5, s96
	ds_write_b16_d16_hi v8, v4 offset:192
	v_or_b32_e32 v4, s64, v1
	v_mad_u64_u32 v[4:5], s[4:5], v4, s71, v[0:1]
	ds_read_u16 v5, v4
	s_waitcnt lgkmcnt(0)
	v_lshlrev_b32_e32 v5, 16, v5
	v_fmac_f32_e32 v5, v30, v6
	v_bfe_u32 v8, v5, 16, 1
	v_add3_u32 v5, v5, v8, s96
	ds_write_b16_d16_hi v4, v5
	ds_read_u16 v5, v4 offset:64
	s_waitcnt lgkmcnt(0)
	v_lshlrev_b32_e32 v5, 16, v5
	v_fmac_f32_e32 v5, v46, v6
	v_bfe_u32 v8, v5, 16, 1
	v_add3_u32 v5, v5, v8, s96
	ds_write_b16_d16_hi v4, v5 offset:64
	ds_read_u16 v5, v4 offset:128
	s_waitcnt lgkmcnt(0)
	v_lshlrev_b32_e32 v5, 16, v5
	v_fmac_f32_e32 v5, v62, v6
	v_bfe_u32 v8, v5, 16, 1
	v_add3_u32 v5, v5, v8, s96
	ds_write_b16_d16_hi v4, v5 offset:128
	ds_read_u16 v5, v4 offset:192
	v_or_b32_e32 v8, s66, v1
	v_mad_u64_u32 v[8:9], s[4:5], v8, s71, v[0:1]
	ds_read_u16 v9, v8
	s_waitcnt lgkmcnt(1)
	v_lshlrev_b32_e32 v5, 16, v5
	v_fmac_f32_e32 v5, v14, v6
	v_bfe_u32 v6, v5, 16, 1
	v_add3_u32 v5, v5, v6, s96
	ds_write_b16_d16_hi v4, v5 offset:192
	v_or_b32_e32 v4, s65, v1
	v_mad_u64_u32 v[4:5], s[4:5], v4, s71, v[0:1]
	ds_read_u16 v5, v4
	s_waitcnt lgkmcnt(2)
	v_lshlrev_b32_e32 v9, 16, v9
	s_waitcnt lgkmcnt(0)
	v_lshlrev_b32_e32 v5, 16, v5
	v_fmac_f32_e32 v5, v31, v7
	v_bfe_u32 v6, v5, 16, 1
	v_add3_u32 v5, v5, v6, s96
	ds_write_b16_d16_hi v4, v5
	ds_read_u16 v5, v4 offset:64
	s_waitcnt lgkmcnt(0)
	v_lshlrev_b32_e32 v5, 16, v5
	v_fmac_f32_e32 v5, v47, v7
	v_bfe_u32 v6, v5, 16, 1
	v_add3_u32 v5, v5, v6, s96
	ds_write_b16_d16_hi v4, v5 offset:64
	ds_read_u16 v5, v4 offset:128
	s_waitcnt lgkmcnt(0)
	v_lshlrev_b32_e32 v5, 16, v5
	v_fmac_f32_e32 v5, v63, v7
	v_bfe_u32 v6, v5, 16, 1
	v_add3_u32 v5, v5, v6, s96
	ds_write_b16_d16_hi v4, v5 offset:128
	ds_read_u16 v5, v4 offset:192
	s_waitcnt lgkmcnt(0)
	v_lshlrev_b32_e32 v5, 16, v5
	v_fmac_f32_e32 v5, v15, v7
	v_bfe_u32 v6, v5, 16, 1
	v_add3_u32 v5, v5, v6, s96
	ds_write_b16_d16_hi v4, v5 offset:192
	ds_read_b128 v[4:7], v72 offset:96
	s_waitcnt lgkmcnt(0)
	v_fmac_f32_e32 v9, v32, v4
	v_bfe_u32 v10, v9, 16, 1
	v_add3_u32 v9, v9, v10, s96
	ds_write_b16_d16_hi v8, v9
	ds_read_u16 v9, v8 offset:64
	s_waitcnt lgkmcnt(0)
	v_lshlrev_b32_e32 v9, 16, v9
	v_fmac_f32_e32 v9, v48, v4
	v_bfe_u32 v10, v9, 16, 1
	v_add3_u32 v9, v9, v10, s96
	ds_write_b16_d16_hi v8, v9 offset:64
	ds_read_u16 v9, v8 offset:128
	s_waitcnt lgkmcnt(0)
	v_lshlrev_b32_e32 v9, 16, v9
	v_fmac_f32_e32 v9, v64, v4
	v_bfe_u32 v10, v9, 16, 1
	v_add3_u32 v9, v9, v10, s96
	ds_write_b16_d16_hi v8, v9 offset:128
	ds_read_u16 v9, v8 offset:192
	s_waitcnt lgkmcnt(0)
	v_lshlrev_b32_e32 v9, 16, v9
	v_fmac_f32_e32 v9, v16, v4
	v_bfe_u32 v4, v9, 16, 1
	v_add3_u32 v4, v9, v4, s96
	ds_write_b16_d16_hi v8, v4 offset:192
	v_or_b32_e32 v4, s67, v1
	v_mad_u64_u32 v[8:9], s[4:5], v4, s71, v[0:1]
	ds_read_u16 v4, v8
	s_waitcnt lgkmcnt(0)
	v_lshlrev_b32_e32 v4, 16, v4
	v_fmac_f32_e32 v4, v33, v5
	v_bfe_u32 v9, v4, 16, 1
	v_add3_u32 v4, v4, v9, s96
	ds_write_b16_d16_hi v8, v4
	ds_read_u16 v4, v8 offset:64
	s_waitcnt lgkmcnt(0)
	v_lshlrev_b32_e32 v4, 16, v4
	v_fmac_f32_e32 v4, v49, v5
	v_bfe_u32 v9, v4, 16, 1
	v_add3_u32 v4, v4, v9, s96
	ds_write_b16_d16_hi v8, v4 offset:64
	ds_read_u16 v4, v8 offset:128
	s_waitcnt lgkmcnt(0)
	v_lshlrev_b32_e32 v4, 16, v4
	v_fmac_f32_e32 v4, v65, v5
	v_bfe_u32 v9, v4, 16, 1
	v_add3_u32 v4, v4, v9, s96
	ds_write_b16_d16_hi v8, v4 offset:128
	ds_read_u16 v4, v8 offset:192
	s_waitcnt lgkmcnt(0)
	v_lshlrev_b32_e32 v4, 16, v4
	v_fmac_f32_e32 v4, v17, v5
	v_bfe_u32 v5, v4, 16, 1
	v_add3_u32 v4, v4, v5, s96
	ds_write_b16_d16_hi v8, v4 offset:192
	v_or_b32_e32 v4, s68, v1
	v_mad_u64_u32 v[4:5], s[4:5], v4, s71, v[0:1]
	ds_read_u16 v5, v4
	v_or_b32_e32 v1, s69, v1
	v_mad_u64_u32 v[0:1], s[4:5], v1, s71, v[0:1]
	ds_read_u16 v1, v0
	s_waitcnt lgkmcnt(1)
	v_lshlrev_b32_e32 v5, 16, v5
	v_fmac_f32_e32 v5, v34, v6
	v_bfe_u32 v8, v5, 16, 1
	v_add3_u32 v5, v5, v8, s96
	ds_write_b16_d16_hi v4, v5
	ds_read_u16 v5, v4 offset:64
	s_waitcnt lgkmcnt(2)
	v_lshlrev_b32_e32 v1, 16, v1
	v_fmac_f32_e32 v1, v35, v7
	s_waitcnt lgkmcnt(0)
	v_lshlrev_b32_e32 v5, 16, v5
	v_fmac_f32_e32 v5, v50, v6
	v_bfe_u32 v8, v5, 16, 1
	v_add3_u32 v5, v5, v8, s96
	ds_write_b16_d16_hi v4, v5 offset:64
	ds_read_u16 v5, v4 offset:128
	s_waitcnt lgkmcnt(0)
	v_lshlrev_b32_e32 v5, 16, v5
	v_fmac_f32_e32 v5, v66, v6
	v_bfe_u32 v8, v5, 16, 1
	v_add3_u32 v5, v5, v8, s96
	ds_write_b16_d16_hi v4, v5 offset:128
	ds_read_u16 v5, v4 offset:192
	s_waitcnt lgkmcnt(0)
	v_lshlrev_b32_e32 v5, 16, v5
	v_fmac_f32_e32 v5, v18, v6
	v_bfe_u32 v6, v5, 16, 1
	v_add3_u32 v5, v5, v6, s96
	ds_write_b16_d16_hi v4, v5 offset:192
	v_bfe_u32 v4, v1, 16, 1
	v_add3_u32 v1, v1, v4, s96
	ds_write_b16_d16_hi v0, v1
	ds_read_u16 v1, v0 offset:64
	s_waitcnt lgkmcnt(0)
	v_lshlrev_b32_e32 v1, 16, v1
	v_fmac_f32_e32 v1, v51, v7
	v_bfe_u32 v4, v1, 16, 1
	v_add3_u32 v1, v1, v4, s96
	ds_write_b16_d16_hi v0, v1 offset:64
	ds_read_u16 v1, v0 offset:128
	s_waitcnt lgkmcnt(0)
	v_lshlrev_b32_e32 v1, 16, v1
	v_fmac_f32_e32 v1, v67, v7
	v_bfe_u32 v4, v1, 16, 1
	v_add3_u32 v1, v1, v4, s96
	ds_write_b16_d16_hi v0, v1 offset:128
	ds_read_u16 v1, v0 offset:192
	s_waitcnt lgkmcnt(0)
	v_lshlrev_b32_e32 v1, 16, v1
	v_fmac_f32_e32 v1, v19, v7
	v_bfe_u32 v4, v1, 16, 1
	v_add3_u32 v1, v1, v4, s96
	ds_write_b16_d16_hi v0, v1 offset:192
	s_waitcnt lgkmcnt(0)
	v_mbcnt_lo_u32_b32 v0, -1, 0
	v_mbcnt_hi_u32_b32 v0, -1, v0
	s_waitcnt vmcnt(0) lgkmcnt(0)
	s_barrier
	v_lshlrev_b32_e32 v5, 4, v0
	v_lshlrev_b32_e32 v4, 3, v0
	v_and_b32_e32 v6, 0xc0, v5
	v_lshlrev_b32_e32 v7, 1, v0
	v_and_or_b32 v6, v4, 24, v6
	v_and_b32_e32 v8, 32, v7
	v_and_b32_e32 v4, 0x100, v4
	v_or3_b32 v137, v6, v8, v4
	v_add_u32_e32 v4, s40, v5
	v_bfe_u32 v8, v0, 2, 2
	v_lshrrev_b32_e32 v9, 1, v0
	v_and_b32_e32 v6, 15, v0
	v_and_or_b32 v8, v9, 8, v8
	v_ashrrev_i32_e32 v9, 8, v4
	v_bitop3_b32 v10, v9, v6, 7 bitop3:0x6c
	v_lshlrev_b32_e32 v11, 10, v9
	v_lshl_or_b32 v132, v10, 4, v11
	v_and_b32_e32 v10, 0xfffff0, v9
	v_lshrrev_b32_e32 v9, 1, v9
	v_and_b32_e32 v9, 4, v9
	v_or3_b32 v9, v10, v9, v8
	v_and_b32_e32 v5, 48, v5
	v_and_b32_e32 v7, 0xc0, v7
	v_mul_i32_i24_e32 v9, 0x6a00, v9
	v_add_u32_e32 v4, 0x400, v4
	v_or3_b32 v133, v9, v7, v5
	v_ashrrev_i32_e32 v7, 8, v4
	v_bitop3_b32 v6, v7, v6, 7 bitop3:0x6c
	v_lshlrev_b32_e32 v9, 10, v7
	v_lshl_or_b32 v134, v6, 4, v9
	v_and_b32_e32 v6, 0xfffff0, v7
	v_lshrrev_b32_e32 v7, 1, v7
	v_and_b32_e32 v7, 4, v7
	v_or3_b32 v6, v6, v7, v8
	v_lshrrev_b32_e32 v4, 3, v4
	v_and_b32_e32 v138, 31, v0
	v_lshrrev_b32_e32 v1, 5, v0
	v_bfe_u32 v139, v0, 5, 1
	v_and_b32_e32 v4, 0xc0, v4
	v_mul_i32_i24_e32 v6, 0x6a00, v6
	v_or3_b32 v135, v6, v4, v5
	v_xor_b32_e32 v0, v1, v0
	v_lshlrev_b32_e32 v1, 4, v138
	v_lshlrev_b32_e32 v141, 2, v139
	v_cndmask_b32_e64 v4, 0, 1, s[10:11]
	v_add_u32_e32 v136, 0, v137
	v_lshlrev_b32_e32 v152, 8, v138
	v_lshlrev_b32_e32 v154, 4, v0
	v_and_b32_e32 v153, 0x60, v1
	v_bitop3_b32 v151, v1, 32, v166 bitop3:0x6c
	v_bitop3_b32 v150, v1, 64, v166 bitop3:0x6c
	v_bitop3_b32 v143, v1, s70, v1 bitop3:0xc
	v_sub_u32_e32 v142, v163, v141
	v_cmp_ne_u32_e64 s[10:11], 1, v4
	s_cbranch_vccz .LBB0_2005
	v_and_b32_e32 v0, 16, v154
	v_add3_u32 v0, 0, v152, v0
	s_waitcnt vmcnt(0) lgkmcnt(0)
	s_barrier
	v_add_u32_e32 v155, v0, v153
	ds_read_b128 v[212:215], v155 offset:32768
	ds_read_b128 v[216:219], v155 offset:40960
	v_add_u32_e32 v170, v0, v151
	ds_read_b128 v[220:223], v170 offset:32768
	ds_read_b128 v[224:227], v170 offset:40960
	v_add_u32_e32 v171, v0, v150
	ds_read_b128 v[228:231], v171 offset:32768
	ds_read_b128 v[232:235], v171 offset:40960
	v_add_u32_e32 v172, v0, v143
	ds_read_b128 v[236:239], v172 offset:32768
	ds_read_b128 v[240:243], v172 offset:40960
	ds_read_b128 v[244:247], v155 offset:32896
	ds_read_b128 v[248:251], v155 offset:41088
	v_cmp_lt_i32_e64 s[12:13], 0, v142
	v_cmp_lt_i32_e64 s[14:15], 32, v142
	s_waitcnt lgkmcnt(9)
	v_mfma_f32_32x32x16_bf16 v[20:35], v[212:215], v[100:103], 0
	ds_read_b128 v[212:215], v170 offset:32896
	v_cmp_lt_i32_e64 s[16:17], 1, v142
	v_cmp_lt_i32_e64 s[18:19], 33, v142
	v_cmp_lt_i32_e64 s[20:21], 2, v142
	v_cmp_lt_i32_e64 s[22:23], 34, v142
	v_cmp_lt_i32_e64 s[24:25], 3, v142
	v_cmp_lt_i32_e64 s[26:27], 35, v142
	s_waitcnt lgkmcnt(9)
	v_mfma_f32_32x32x16_bf16 v[36:51], v[216:219], v[100:103], 0
	ds_read_b128 v[216:219], v170 offset:41088
	v_cmp_lt_i32_e64 s[28:29], 8, v142
	v_cmp_lt_i32_e64 s[30:31], 40, v142
	v_cmp_lt_i32_e64 s[34:35], 9, v142
	v_cmp_lt_i32_e64 s[36:37], 41, v142
	v_cmp_lt_i32_e64 s[38:39], 10, v142
	v_cmp_lt_i32_e64 s[40:41], 42, v142
	s_waitcnt lgkmcnt(9)
	v_mfma_f32_32x32x16_bf16 v[20:35], v[220:223], v[108:111], v[20:35]
	ds_read_b128 v[220:223], v171 offset:32896
	v_cmp_lt_i32_e64 s[42:43], 11, v142
	v_cmp_lt_i32_e64 s[44:45], 43, v142
	v_cmp_lt_i32_e64 s[46:47], 16, v142
	v_cmp_lt_i32_e64 s[48:49], 48, v142
	v_cmp_lt_i32_e64 s[50:51], 17, v142
	v_cmp_lt_i32_e64 s[52:53], 49, v142
	s_waitcnt lgkmcnt(9)
	v_mfma_f32_32x32x16_bf16 v[36:51], v[224:227], v[108:111], v[36:51]
	ds_read_b128 v[224:227], v171 offset:41088
	v_cmp_lt_i32_e64 s[54:55], 18, v142
	v_cmp_lt_i32_e64 s[56:57], 50, v142
	v_cmp_lt_i32_e64 s[58:59], 19, v142
	v_cmp_lt_i32_e64 s[60:61], 51, v142
	v_cmp_lt_i32_e64 s[62:63], 24, v142
	v_cmp_lt_i32_e64 s[64:65], 56, v142
	s_waitcnt lgkmcnt(9)
	v_mfma_f32_32x32x16_bf16 v[20:35], v[228:231], v[116:119], v[20:35]
	ds_read_b128 v[228:231], v172 offset:32896
	v_cmp_lt_i32_e64 s[66:67], 25, v142
	v_cmp_lt_i32_e64 s[68:69], 57, v142
	v_cmp_lt_i32_e64 s[70:71], 26, v142
	v_cmp_lt_i32_e64 s[72:73], 58, v142
	v_cmp_lt_i32_e64 s[74:75], 27, v142
	v_cmp_lt_i32_e64 s[76:77], 59, v142
	s_waitcnt lgkmcnt(9)
	v_mfma_f32_32x32x16_bf16 v[36:51], v[232:235], v[116:119], v[36:51]
	ds_read_b128 v[232:235], v172 offset:41088
	s_and_b64 vcc, exec, s[10:11]
	s_waitcnt lgkmcnt(9)
	v_mfma_f32_32x32x16_bf16 v[20:35], v[236:239], v[124:127], v[20:35]
	s_waitcnt lgkmcnt(8)
	v_mfma_f32_32x32x16_bf16 v[36:51], v[240:243], v[124:127], v[36:51]
	s_waitcnt lgkmcnt(7)
	v_mfma_f32_32x32x16_bf16 v[20:35], v[244:247], v[104:107], v[20:35]
	s_waitcnt lgkmcnt(6)
	v_mfma_f32_32x32x16_bf16 v[36:51], v[248:251], v[104:107], v[36:51]
	s_waitcnt lgkmcnt(5)
	v_mfma_f32_32x32x16_bf16 v[20:35], v[212:215], v[112:115], v[20:35]
	s_waitcnt lgkmcnt(4)
	v_mfma_f32_32x32x16_bf16 v[36:51], v[216:219], v[112:115], v[36:51]
	s_waitcnt lgkmcnt(3)
	v_mfma_f32_32x32x16_bf16 v[20:35], v[220:223], v[120:123], v[20:35]
	s_waitcnt lgkmcnt(2)
	v_mfma_f32_32x32x16_bf16 v[36:51], v[224:227], v[120:123], v[36:51]
	s_waitcnt lgkmcnt(1)
	v_mfma_f32_32x32x16_bf16 v[20:35], v[228:231], v[128:131], v[20:35]
	s_waitcnt lgkmcnt(0)
	v_mfma_f32_32x32x16_bf16 v[36:51], v[232:235], v[128:131], v[36:51]
	s_cbranch_vccnz .LBB0_1917
	s_nop 9
	v_cndmask_b32_e64 v20, v168, v20, s[12:13]
	v_cndmask_b32_e64 v36, v168, v36, s[14:15]
	v_cndmask_b32_e64 v21, v168, v21, s[16:17]
	v_cndmask_b32_e64 v37, v168, v37, s[18:19]
	v_cndmask_b32_e64 v22, v168, v22, s[20:21]
	v_cndmask_b32_e64 v38, v168, v38, s[22:23]
	v_cndmask_b32_e64 v23, v168, v23, s[24:25]
	v_cndmask_b32_e64 v39, v168, v39, s[26:27]
	v_cndmask_b32_e64 v24, v168, v24, s[28:29]
	v_cndmask_b32_e64 v40, v168, v40, s[30:31]
	v_cndmask_b32_e64 v25, v168, v25, s[34:35]
	v_cndmask_b32_e64 v41, v168, v41, s[36:37]
	v_cndmask_b32_e64 v26, v168, v26, s[38:39]
	v_cndmask_b32_e64 v42, v168, v42, s[40:41]
	v_cndmask_b32_e64 v27, v168, v27, s[42:43]
	v_cndmask_b32_e64 v43, v168, v43, s[44:45]
	v_cndmask_b32_e64 v28, v168, v28, s[46:47]
	v_cndmask_b32_e64 v44, v168, v44, s[48:49]
	v_cndmask_b32_e64 v29, v168, v29, s[50:51]
	v_cndmask_b32_e64 v45, v168, v45, s[52:53]
	v_cndmask_b32_e64 v30, v168, v30, s[54:55]
	v_cndmask_b32_e64 v46, v168, v46, s[56:57]
	v_cndmask_b32_e64 v31, v168, v31, s[58:59]
	v_cndmask_b32_e64 v47, v168, v47, s[60:61]
	v_cndmask_b32_e64 v32, v168, v32, s[62:63]
	v_cndmask_b32_e64 v48, v168, v48, s[64:65]
	v_cndmask_b32_e64 v33, v168, v33, s[66:67]
	v_cndmask_b32_e64 v49, v168, v49, s[68:69]
	v_cndmask_b32_e64 v34, v168, v34, s[70:71]
	v_cndmask_b32_e64 v50, v168, v50, s[72:73]
	v_cndmask_b32_e64 v35, v168, v35, s[74:75]
	v_cndmask_b32_e64 v51, v168, v51, s[76:77]

.LBB0_1939:
	ds_read_b128 v[212:215], v155 offset:49152
	ds_read_b128 v[216:219], v170 offset:49152
	ds_read_b128 v[220:223], v155 offset:57344
	ds_read_b128 v[224:227], v170 offset:57344
	ds_read_b128 v[228:231], v171 offset:49152
	ds_read_b128 v[232:235], v171 offset:57344
	ds_read_b128 v[236:239], v172 offset:49152
	ds_read_b128 v[240:243], v172 offset:57344
	ds_read_b128 v[244:247], v155 offset:49280
	ds_read_b128 v[248:251], v155 offset:57472
	v_readlane_b32 s1, v255, 21
	s_add_i32 s1, s1, 1
	s_cmp_lg_u32 s1, s89
	s_waitcnt lgkmcnt(9)
	v_mfma_f32_32x32x16_bf16 v[68:83], v[212:215], v[100:103], 0
	ds_read_b128 v[212:215], v170 offset:49280
	s_waitcnt lgkmcnt(9)
	v_mfma_f32_32x32x16_bf16 v[68:83], v[216:219], v[108:111], v[68:83]
	ds_read_b128 v[216:219], v170 offset:57472
	s_waitcnt lgkmcnt(9)
	v_mfma_f32_32x32x16_bf16 v[84:99], v[220:223], v[100:103], 0
	ds_read_b128 v[220:223], v171 offset:49280
	s_waitcnt lgkmcnt(9)
	v_mfma_f32_32x32x16_bf16 v[84:99], v[224:227], v[108:111], v[84:99]
	ds_read_b128 v[224:227], v171 offset:57472
	s_waitcnt lgkmcnt(9)
	v_mfma_f32_32x32x16_bf16 v[68:83], v[228:231], v[116:119], v[68:83]
	ds_read_b128 v[228:231], v172 offset:49280
	s_waitcnt lgkmcnt(9)
	v_mfma_f32_32x32x16_bf16 v[84:99], v[232:235], v[116:119], v[84:99]
	ds_read_b128 v[232:235], v172 offset:57472
	s_waitcnt lgkmcnt(9)
	v_mfma_f32_32x32x16_bf16 v[68:83], v[236:239], v[124:127], v[68:83]
	s_waitcnt lgkmcnt(8)
	v_mfma_f32_32x32x16_bf16 v[84:99], v[240:243], v[124:127], v[84:99]
	s_waitcnt lgkmcnt(7)
	v_mfma_f32_32x32x16_bf16 v[68:83], v[244:247], v[104:107], v[68:83]
	s_waitcnt lgkmcnt(6)
	v_mfma_f32_32x32x16_bf16 v[84:99], v[248:251], v[104:107], v[84:99]
	s_waitcnt lgkmcnt(5)
	v_mfma_f32_32x32x16_bf16 v[68:83], v[212:215], v[112:115], v[68:83]
	s_waitcnt lgkmcnt(4)
	v_mfma_f32_32x32x16_bf16 v[84:99], v[216:219], v[112:115], v[84:99]
	s_waitcnt lgkmcnt(3)
	v_mfma_f32_32x32x16_bf16 v[68:83], v[220:223], v[120:123], v[68:83]
	s_waitcnt lgkmcnt(2)
	v_mfma_f32_32x32x16_bf16 v[84:99], v[224:227], v[120:123], v[84:99]
	s_waitcnt lgkmcnt(1)
	v_mfma_f32_32x32x16_bf16 v[68:83], v[228:231], v[128:131], v[68:83]
	s_waitcnt lgkmcnt(0)
	s_nop 0
	v_mfma_f32_32x32x16_bf16 v[84:99], v[232:235], v[128:131], v[84:99]
	s_cbranch_scc1 .LBB0_1941
	s_nop 7
	v_cndmask_b32_e64 v68, v168, v68, s[12:13]
	s_nop 1
	v_cndmask_b32_e64 v84, v168, v84, s[14:15]
	v_cndmask_b32_e64 v69, v168, v69, s[16:17]
	v_cndmask_b32_e64 v85, v168, v85, s[18:19]
	v_cndmask_b32_e64 v70, v168, v70, s[20:21]
	v_cndmask_b32_e64 v86, v168, v86, s[22:23]
	v_cndmask_b32_e64 v71, v168, v71, s[24:25]
	v_cndmask_b32_e64 v87, v168, v87, s[26:27]
	v_cndmask_b32_e64 v72, v168, v72, s[28:29]
	v_cndmask_b32_e64 v88, v168, v88, s[30:31]
	v_cndmask_b32_e64 v73, v168, v73, s[34:35]
	v_cndmask_b32_e64 v89, v168, v89, s[36:37]
	v_cndmask_b32_e64 v74, v168, v74, s[38:39]
	v_cndmask_b32_e64 v90, v168, v90, s[40:41]
	v_cndmask_b32_e64 v75, v168, v75, s[42:43]
	v_cndmask_b32_e64 v91, v168, v91, s[44:45]
	v_cndmask_b32_e64 v76, v168, v76, s[46:47]
	v_cndmask_b32_e64 v92, v168, v92, s[48:49]
	v_cndmask_b32_e64 v77, v168, v77, s[50:51]
	v_cndmask_b32_e64 v93, v168, v93, s[52:53]
	v_cndmask_b32_e64 v78, v168, v78, s[54:55]
	v_cndmask_b32_e64 v94, v168, v94, s[56:57]
	v_cndmask_b32_e64 v79, v168, v79, s[58:59]
	v_cndmask_b32_e64 v95, v168, v95, s[60:61]
	v_cndmask_b32_e64 v80, v168, v80, s[62:63]
	v_cndmask_b32_e64 v96, v168, v96, s[64:65]
	v_cndmask_b32_e64 v81, v168, v81, s[66:67]
	v_cndmask_b32_e64 v97, v168, v97, s[68:69]
	v_cndmask_b32_e64 v82, v168, v82, s[70:71]
	v_cndmask_b32_e64 v98, v168, v98, s[72:73]
	v_cndmask_b32_e64 v83, v168, v83, s[74:75]
	v_cndmask_b32_e64 v99, v168, v99, s[76:77]

.LBB0_1963:
	ds_read_b128 v[212:215], v155 offset:32768
	ds_read_b128 v[216:219], v170 offset:32768
	ds_read_b128 v[220:223], v155 offset:40960
	ds_read_b128 v[224:227], v170 offset:40960
	ds_read_b128 v[228:231], v171 offset:32768
	ds_read_b128 v[232:235], v171 offset:40960
	ds_read_b128 v[236:239], v172 offset:32768
	ds_read_b128 v[240:243], v172 offset:40960
	ds_read_b128 v[244:247], v155 offset:32896
	ds_read_b128 v[248:251], v155 offset:41088
	s_add_i32 s4, s3, s6
	s_cmp_lg_u32 s4, 3
	s_waitcnt lgkmcnt(9)
	v_mfma_f32_32x32x16_bf16 v[68:83], v[212:215], v[100:103], 0
	ds_read_b128 v[212:215], v170 offset:32896
	s_waitcnt lgkmcnt(9)
	v_mfma_f32_32x32x16_bf16 v[68:83], v[216:219], v[108:111], v[68:83]
	ds_read_b128 v[216:219], v170 offset:41088
	s_waitcnt lgkmcnt(9)
	v_mfma_f32_32x32x16_bf16 v[84:99], v[220:223], v[100:103], 0
	ds_read_b128 v[220:223], v171 offset:32896
	s_waitcnt lgkmcnt(9)
	v_mfma_f32_32x32x16_bf16 v[84:99], v[224:227], v[108:111], v[84:99]
	ds_read_b128 v[224:227], v171 offset:41088
	s_waitcnt lgkmcnt(9)
	v_mfma_f32_32x32x16_bf16 v[68:83], v[228:231], v[116:119], v[68:83]
	ds_read_b128 v[228:231], v172 offset:32896
	s_waitcnt lgkmcnt(9)
	v_mfma_f32_32x32x16_bf16 v[84:99], v[232:235], v[116:119], v[84:99]
	ds_read_b128 v[232:235], v172 offset:41088
	s_waitcnt lgkmcnt(9)
	v_mfma_f32_32x32x16_bf16 v[68:83], v[236:239], v[124:127], v[68:83]
	s_waitcnt lgkmcnt(8)
	v_mfma_f32_32x32x16_bf16 v[84:99], v[240:243], v[124:127], v[84:99]
	s_waitcnt lgkmcnt(7)
	v_mfma_f32_32x32x16_bf16 v[68:83], v[244:247], v[104:107], v[68:83]
	s_waitcnt lgkmcnt(6)
	v_mfma_f32_32x32x16_bf16 v[84:99], v[248:251], v[104:107], v[84:99]
	s_waitcnt lgkmcnt(5)
	v_mfma_f32_32x32x16_bf16 v[68:83], v[212:215], v[112:115], v[68:83]
	s_waitcnt lgkmcnt(4)
	v_mfma_f32_32x32x16_bf16 v[84:99], v[216:219], v[112:115], v[84:99]
	s_waitcnt lgkmcnt(3)
	v_mfma_f32_32x32x16_bf16 v[68:83], v[220:223], v[120:123], v[68:83]
	s_waitcnt lgkmcnt(2)
	v_mfma_f32_32x32x16_bf16 v[84:99], v[224:227], v[120:123], v[84:99]
	s_waitcnt lgkmcnt(1)
	v_mfma_f32_32x32x16_bf16 v[68:83], v[228:231], v[128:131], v[68:83]
	s_waitcnt lgkmcnt(0)
	s_nop 0
	v_mfma_f32_32x32x16_bf16 v[84:99], v[232:235], v[128:131], v[84:99]
	s_cbranch_scc1 .LBB0_1965
	s_nop 7
	v_cndmask_b32_e64 v68, v168, v68, s[12:13]
	s_nop 1
	v_cndmask_b32_e64 v84, v168, v84, s[14:15]
	v_cndmask_b32_e64 v69, v168, v69, s[16:17]
	v_cndmask_b32_e64 v85, v168, v85, s[18:19]
	v_cndmask_b32_e64 v70, v168, v70, s[20:21]
	v_cndmask_b32_e64 v86, v168, v86, s[22:23]
	v_cndmask_b32_e64 v71, v168, v71, s[24:25]
	v_cndmask_b32_e64 v87, v168, v87, s[26:27]
	v_cndmask_b32_e64 v72, v168, v72, s[28:29]
	v_cndmask_b32_e64 v88, v168, v88, s[30:31]
	v_cndmask_b32_e64 v73, v168, v73, s[34:35]
	v_cndmask_b32_e64 v89, v168, v89, s[36:37]
	v_cndmask_b32_e64 v74, v168, v74, s[38:39]
	v_cndmask_b32_e64 v90, v168, v90, s[40:41]
	v_cndmask_b32_e64 v75, v168, v75, s[42:43]
	v_cndmask_b32_e64 v91, v168, v91, s[44:45]
	v_cndmask_b32_e64 v76, v168, v76, s[46:47]
	v_cndmask_b32_e64 v92, v168, v92, s[48:49]
	v_cndmask_b32_e64 v77, v168, v77, s[50:51]
	v_cndmask_b32_e64 v93, v168, v93, s[52:53]
	v_cndmask_b32_e64 v78, v168, v78, s[54:55]
	v_cndmask_b32_e64 v94, v168, v94, s[56:57]
	v_cndmask_b32_e64 v79, v168, v79, s[58:59]
	v_cndmask_b32_e64 v95, v168, v95, s[60:61]
	v_cndmask_b32_e64 v80, v168, v80, s[62:63]
	v_cndmask_b32_e64 v96, v168, v96, s[64:65]
	v_cndmask_b32_e64 v81, v168, v81, s[66:67]
	v_cndmask_b32_e64 v97, v168, v97, s[68:69]
	v_cndmask_b32_e64 v82, v168, v82, s[70:71]
	v_cndmask_b32_e64 v98, v168, v98, s[72:73]
	v_cndmask_b32_e64 v83, v168, v83, s[74:75]
	v_cndmask_b32_e64 v99, v168, v99, s[76:77]

.LBB0_1982:
	ds_read_b128 v[212:215], v155 offset:49152
	ds_read_b128 v[216:219], v170 offset:49152
	ds_read_b128 v[220:223], v155 offset:57344
	ds_read_b128 v[224:227], v170 offset:57344
	ds_read_b128 v[228:231], v171 offset:49152
	ds_read_b128 v[232:235], v171 offset:57344
	ds_read_b128 v[236:239], v172 offset:49152
	ds_read_b128 v[240:243], v172 offset:57344
	ds_read_b128 v[244:247], v155 offset:49280
	ds_read_b128 v[248:251], v155 offset:57472
	s_add_i32 s4, s1, s6
	s_cmp_lg_u32 s4, 5
	s_waitcnt lgkmcnt(9)
	v_mfma_f32_32x32x16_bf16 v[68:83], v[212:215], v[100:103], 0
	ds_read_b128 v[212:215], v170 offset:49280
	s_waitcnt lgkmcnt(9)
	v_mfma_f32_32x32x16_bf16 v[68:83], v[216:219], v[108:111], v[68:83]
	ds_read_b128 v[216:219], v170 offset:57472
	s_waitcnt lgkmcnt(9)
	v_mfma_f32_32x32x16_bf16 v[84:99], v[220:223], v[100:103], 0
	ds_read_b128 v[220:223], v171 offset:49280
	s_waitcnt lgkmcnt(9)
	v_mfma_f32_32x32x16_bf16 v[84:99], v[224:227], v[108:111], v[84:99]
	ds_read_b128 v[224:227], v171 offset:57472
	s_waitcnt lgkmcnt(9)
	v_mfma_f32_32x32x16_bf16 v[68:83], v[228:231], v[116:119], v[68:83]
	ds_read_b128 v[228:231], v172 offset:49280
	s_waitcnt lgkmcnt(9)
	v_mfma_f32_32x32x16_bf16 v[84:99], v[232:235], v[116:119], v[84:99]
	ds_read_b128 v[232:235], v172 offset:57472
	s_waitcnt lgkmcnt(9)
	v_mfma_f32_32x32x16_bf16 v[68:83], v[236:239], v[124:127], v[68:83]
	s_waitcnt lgkmcnt(8)
	v_mfma_f32_32x32x16_bf16 v[84:99], v[240:243], v[124:127], v[84:99]
	s_waitcnt lgkmcnt(7)
	v_mfma_f32_32x32x16_bf16 v[68:83], v[244:247], v[104:107], v[68:83]
	s_waitcnt lgkmcnt(6)
	v_mfma_f32_32x32x16_bf16 v[84:99], v[248:251], v[104:107], v[84:99]
	s_waitcnt lgkmcnt(5)
	v_mfma_f32_32x32x16_bf16 v[68:83], v[212:215], v[112:115], v[68:83]
	s_waitcnt lgkmcnt(4)
	v_mfma_f32_32x32x16_bf16 v[84:99], v[216:219], v[112:115], v[84:99]
	s_waitcnt lgkmcnt(3)
	v_mfma_f32_32x32x16_bf16 v[68:83], v[220:223], v[120:123], v[68:83]
	s_waitcnt lgkmcnt(2)
	v_mfma_f32_32x32x16_bf16 v[84:99], v[224:227], v[120:123], v[84:99]
	s_waitcnt lgkmcnt(1)
	v_mfma_f32_32x32x16_bf16 v[68:83], v[228:231], v[128:131], v[68:83]
	s_waitcnt lgkmcnt(0)
	s_nop 0
	v_mfma_f32_32x32x16_bf16 v[84:99], v[232:235], v[128:131], v[84:99]
	s_cbranch_scc1 .LBB0_1984
	s_nop 7
	v_cndmask_b32_e64 v68, v168, v68, s[12:13]
	s_nop 1
	v_cndmask_b32_e64 v84, v168, v84, s[14:15]
	v_cndmask_b32_e64 v69, v168, v69, s[16:17]
	v_cndmask_b32_e64 v85, v168, v85, s[18:19]
	v_cndmask_b32_e64 v70, v168, v70, s[20:21]
	v_cndmask_b32_e64 v86, v168, v86, s[22:23]
	v_cndmask_b32_e64 v71, v168, v71, s[24:25]
	v_cndmask_b32_e64 v87, v168, v87, s[26:27]
	v_cndmask_b32_e64 v72, v168, v72, s[28:29]
	v_cndmask_b32_e64 v88, v168, v88, s[30:31]
	v_cndmask_b32_e64 v73, v168, v73, s[34:35]
	v_cndmask_b32_e64 v89, v168, v89, s[36:37]
	v_cndmask_b32_e64 v74, v168, v74, s[38:39]
	v_cndmask_b32_e64 v90, v168, v90, s[40:41]
	v_cndmask_b32_e64 v75, v168, v75, s[42:43]
	v_cndmask_b32_e64 v91, v168, v91, s[44:45]
	v_cndmask_b32_e64 v76, v168, v76, s[46:47]
	v_cndmask_b32_e64 v92, v168, v92, s[48:49]
	v_cndmask_b32_e64 v77, v168, v77, s[50:51]
	v_cndmask_b32_e64 v93, v168, v93, s[52:53]
	v_cndmask_b32_e64 v78, v168, v78, s[54:55]
	v_cndmask_b32_e64 v94, v168, v94, s[56:57]
	v_cndmask_b32_e64 v79, v168, v79, s[58:59]
	v_cndmask_b32_e64 v95, v168, v95, s[60:61]
	v_cndmask_b32_e64 v80, v168, v80, s[62:63]
	v_cndmask_b32_e64 v96, v168, v96, s[64:65]
	v_cndmask_b32_e64 v81, v168, v81, s[66:67]
	v_cndmask_b32_e64 v97, v168, v97, s[68:69]
	v_cndmask_b32_e64 v82, v168, v82, s[70:71]
	v_cndmask_b32_e64 v98, v168, v98, s[72:73]
	v_cndmask_b32_e64 v83, v168, v83, s[74:75]
	v_cndmask_b32_e64 v99, v168, v99, s[76:77]

.LBB0_2005:
	s_and_b64 vcc, exec, s[8:9]
	s_cbranch_vccz .LBB0_2092
	v_and_b32_e32 v0, 16, v154
	v_add3_u32 v0, 0, v152, v0
	v_add_u32_e32 v152, v0, v153
	ds_read_b128 v[212:215], v152 offset:32768
	ds_read_b128 v[216:219], v152 offset:40960
	v_add_u32_e32 v151, v0, v151
	ds_read_b128 v[220:223], v151 offset:32768
	ds_read_b128 v[224:227], v151 offset:40960
	v_add_u32_e32 v150, v0, v150
	ds_read_b128 v[228:231], v150 offset:32768
	ds_read_b128 v[232:235], v150 offset:40960
	v_add_u32_e32 v143, v0, v143
	ds_read_b128 v[236:239], v143 offset:32768
	ds_read_b128 v[240:243], v143 offset:40960
	ds_read_b128 v[244:247], v152 offset:32896
	ds_read_b128 v[248:251], v152 offset:41088
	v_cmp_lt_i32_e64 s[12:13], 0, v142
	v_cmp_lt_i32_e64 s[14:15], 32, v142
	v_cmp_lt_i32_e64 s[16:17], 1, v142
	v_cmp_lt_i32_e64 s[18:19], 33, v142
	v_cmp_lt_i32_e64 s[20:21], 2, v142
	s_waitcnt lgkmcnt(9)
	v_mfma_f32_32x32x16_bf16 v[36:51], v[212:215], v[100:103], 0
	ds_read_b128 v[212:215], v151 offset:32896
	v_cmp_lt_i32_e64 s[22:23], 34, v142
	v_cmp_lt_i32_e64 s[24:25], 3, v142
	v_cmp_lt_i32_e64 s[26:27], 35, v142
	v_cmp_lt_i32_e64 s[28:29], 8, v142
	v_cmp_lt_i32_e64 s[30:31], 40, v142
	v_cmp_lt_i32_e64 s[34:35], 9, v142
	v_cmp_lt_i32_e64 s[36:37], 41, v142
	s_waitcnt lgkmcnt(9)
	v_mfma_f32_32x32x16_bf16 v[20:35], v[216:219], v[100:103], 0
	ds_read_b128 v[216:219], v151 offset:41088
	v_cmp_lt_i32_e64 s[38:39], 10, v142
	v_cmp_lt_i32_e64 s[40:41], 42, v142
	v_cmp_lt_i32_e64 s[42:43], 11, v142
	v_cmp_lt_i32_e64 s[44:45], 43, v142
	v_cmp_lt_i32_e64 s[46:47], 16, v142
	v_cmp_lt_i32_e64 s[48:49], 48, v142
	s_waitcnt lgkmcnt(9)
	v_mfma_f32_32x32x16_bf16 v[36:51], v[220:223], v[108:111], v[36:51]
	ds_read_b128 v[220:223], v150 offset:32896
	v_cmp_lt_i32_e64 s[50:51], 17, v142
	v_cmp_lt_i32_e64 s[52:53], 49, v142
	v_cmp_lt_i32_e64 s[54:55], 18, v142
	v_cmp_lt_i32_e64 s[56:57], 50, v142
	v_cmp_lt_i32_e64 s[58:59], 19, v142
	v_cmp_lt_i32_e64 s[60:61], 51, v142
	s_waitcnt lgkmcnt(9)
	v_mfma_f32_32x32x16_bf16 v[20:35], v[224:227], v[108:111], v[20:35]
	ds_read_b128 v[224:227], v150 offset:41088
	v_cmp_lt_i32_e64 s[62:63], 24, v142
	v_cmp_lt_i32_e64 s[64:65], 56, v142
	v_cmp_lt_i32_e64 s[66:67], 25, v142
	v_cmp_lt_i32_e64 s[68:69], 57, v142
	v_cmp_lt_i32_e64 s[70:71], 26, v142
	v_cmp_lt_i32_e64 s[72:73], 58, v142
	s_waitcnt lgkmcnt(9)
	v_mfma_f32_32x32x16_bf16 v[36:51], v[228:231], v[116:119], v[36:51]
	ds_read_b128 v[228:231], v143 offset:32896
	v_cmp_lt_i32_e64 s[74:75], 27, v142
	v_cmp_lt_i32_e64 s[76:77], 59, v142
	s_and_b64 vcc, exec, s[10:11]
	s_waitcnt lgkmcnt(9)
	v_mfma_f32_32x32x16_bf16 v[20:35], v[232:235], v[116:119], v[20:35]
	ds_read_b128 v[232:235], v143 offset:41088
	s_waitcnt lgkmcnt(9)
	v_mfma_f32_32x32x16_bf16 v[36:51], v[236:239], v[124:127], v[36:51]
	s_waitcnt lgkmcnt(8)
	v_mfma_f32_32x32x16_bf16 v[20:35], v[240:243], v[124:127], v[20:35]
	s_waitcnt lgkmcnt(7)
	v_mfma_f32_32x32x16_bf16 v[36:51], v[244:247], v[104:107], v[36:51]
	s_waitcnt lgkmcnt(6)
	v_mfma_f32_32x32x16_bf16 v[20:35], v[248:251], v[104:107], v[20:35]
	s_waitcnt lgkmcnt(5)
	v_mfma_f32_32x32x16_bf16 v[36:51], v[212:215], v[112:115], v[36:51]
	s_waitcnt lgkmcnt(4)
	v_mfma_f32_32x32x16_bf16 v[20:35], v[216:219], v[112:115], v[20:35]
	s_waitcnt lgkmcnt(3)
	v_mfma_f32_32x32x16_bf16 v[36:51], v[220:223], v[120:123], v[36:51]
	s_waitcnt lgkmcnt(2)
	v_mfma_f32_32x32x16_bf16 v[20:35], v[224:227], v[120:123], v[20:35]
	s_waitcnt lgkmcnt(1)
	v_mfma_f32_32x32x16_bf16 v[36:51], v[228:231], v[128:131], v[36:51]
	s_waitcnt lgkmcnt(0)
	v_mfma_f32_32x32x16_bf16 v[20:35], v[232:235], v[128:131], v[20:35]
	s_cbranch_vccnz .LBB0_2008
	s_nop 9
	v_cndmask_b32_e64 v36, v168, v36, s[12:13]
	v_cndmask_b32_e64 v20, v168, v20, s[14:15]
	v_cndmask_b32_e64 v37, v168, v37, s[16:17]
	v_cndmask_b32_e64 v21, v168, v21, s[18:19]
	v_cndmask_b32_e64 v38, v168, v38, s[20:21]
	v_cndmask_b32_e64 v22, v168, v22, s[22:23]
	v_cndmask_b32_e64 v39, v168, v39, s[24:25]
	v_cndmask_b32_e64 v23, v168, v23, s[26:27]
	v_cndmask_b32_e64 v40, v168, v40, s[28:29]
	v_cndmask_b32_e64 v24, v168, v24, s[30:31]
	v_cndmask_b32_e64 v41, v168, v41, s[34:35]
	v_cndmask_b32_e64 v25, v168, v25, s[36:37]
	v_cndmask_b32_e64 v42, v168, v42, s[38:39]
	v_cndmask_b32_e64 v26, v168, v26, s[40:41]
	v_cndmask_b32_e64 v43, v168, v43, s[42:43]
	v_cndmask_b32_e64 v27, v168, v27, s[44:45]
	v_cndmask_b32_e64 v44, v168, v44, s[46:47]
	v_cndmask_b32_e64 v28, v168, v28, s[48:49]
	v_cndmask_b32_e64 v45, v168, v45, s[50:51]
	v_cndmask_b32_e64 v29, v168, v29, s[52:53]
	v_cndmask_b32_e64 v46, v168, v46, s[54:55]
	v_cndmask_b32_e64 v30, v168, v30, s[56:57]
	v_cndmask_b32_e64 v47, v168, v47, s[58:59]
	v_cndmask_b32_e64 v31, v168, v31, s[60:61]
	v_cndmask_b32_e64 v48, v168, v48, s[62:63]
	v_cndmask_b32_e64 v32, v168, v32, s[64:65]
	v_cndmask_b32_e64 v49, v168, v49, s[66:67]
	v_cndmask_b32_e64 v33, v168, v33, s[68:69]
	v_cndmask_b32_e64 v50, v168, v50, s[70:71]
	v_cndmask_b32_e64 v34, v168, v34, s[72:73]
	v_cndmask_b32_e64 v51, v168, v51, s[74:75]
	v_cndmask_b32_e64 v35, v168, v35, s[76:77]

.LBB0_2020:
	ds_read_b128 v[212:215], v152 offset:49152
	ds_read_b128 v[216:219], v151 offset:49152
	ds_read_b128 v[220:223], v152 offset:57344
	ds_read_b128 v[224:227], v151 offset:57344
	ds_read_b128 v[228:231], v150 offset:49152
	ds_read_b128 v[232:235], v150 offset:57344
	ds_read_b128 v[236:239], v143 offset:49152
	ds_read_b128 v[240:243], v143 offset:57344
	ds_read_b128 v[244:247], v152 offset:49280
	ds_read_b128 v[248:251], v152 offset:57472
	s_add_i32 s1, s4, 1
	s_cmp_lg_u32 s1, s89
	s_waitcnt lgkmcnt(9)
	v_mfma_f32_32x32x16_bf16 v[68:83], v[212:215], v[100:103], 0
	ds_read_b128 v[212:215], v151 offset:49280
	s_waitcnt lgkmcnt(9)
	v_mfma_f32_32x32x16_bf16 v[68:83], v[216:219], v[108:111], v[68:83]
	ds_read_b128 v[216:219], v151 offset:57472
	s_waitcnt lgkmcnt(9)
	v_mfma_f32_32x32x16_bf16 v[84:99], v[220:223], v[100:103], 0
	ds_read_b128 v[220:223], v150 offset:49280
	s_waitcnt lgkmcnt(9)
	v_mfma_f32_32x32x16_bf16 v[84:99], v[224:227], v[108:111], v[84:99]
	ds_read_b128 v[224:227], v150 offset:57472
	s_waitcnt lgkmcnt(9)
	v_mfma_f32_32x32x16_bf16 v[68:83], v[228:231], v[116:119], v[68:83]
	ds_read_b128 v[228:231], v143 offset:49280
	s_waitcnt lgkmcnt(9)
	v_mfma_f32_32x32x16_bf16 v[84:99], v[232:235], v[116:119], v[84:99]
	ds_read_b128 v[232:235], v143 offset:57472
	s_waitcnt lgkmcnt(9)
	v_mfma_f32_32x32x16_bf16 v[68:83], v[236:239], v[124:127], v[68:83]
	s_waitcnt lgkmcnt(8)
	v_mfma_f32_32x32x16_bf16 v[84:99], v[240:243], v[124:127], v[84:99]
	s_waitcnt lgkmcnt(7)
	v_mfma_f32_32x32x16_bf16 v[68:83], v[244:247], v[104:107], v[68:83]
	s_waitcnt lgkmcnt(6)
	v_mfma_f32_32x32x16_bf16 v[84:99], v[248:251], v[104:107], v[84:99]
	s_waitcnt lgkmcnt(5)
	v_mfma_f32_32x32x16_bf16 v[68:83], v[212:215], v[112:115], v[68:83]
	s_waitcnt lgkmcnt(4)
	v_mfma_f32_32x32x16_bf16 v[84:99], v[216:219], v[112:115], v[84:99]
	s_waitcnt lgkmcnt(3)
	v_mfma_f32_32x32x16_bf16 v[68:83], v[220:223], v[120:123], v[68:83]
	s_waitcnt lgkmcnt(2)
	v_mfma_f32_32x32x16_bf16 v[84:99], v[224:227], v[120:123], v[84:99]
	s_waitcnt lgkmcnt(1)
	v_mfma_f32_32x32x16_bf16 v[68:83], v[228:231], v[128:131], v[68:83]
	s_waitcnt lgkmcnt(0)
	s_nop 0
	v_mfma_f32_32x32x16_bf16 v[84:99], v[232:235], v[128:131], v[84:99]
	s_cbranch_scc1 .LBB0_2022
	s_nop 7
	v_cndmask_b32_e64 v68, v168, v68, s[12:13]
	s_nop 1
	v_cndmask_b32_e64 v84, v168, v84, s[14:15]
	v_cndmask_b32_e64 v69, v168, v69, s[16:17]
	v_cndmask_b32_e64 v85, v168, v85, s[18:19]
	v_cndmask_b32_e64 v70, v168, v70, s[20:21]
	v_cndmask_b32_e64 v86, v168, v86, s[22:23]
	v_cndmask_b32_e64 v71, v168, v71, s[24:25]
	v_cndmask_b32_e64 v87, v168, v87, s[26:27]
	v_cndmask_b32_e64 v72, v168, v72, s[28:29]
	v_cndmask_b32_e64 v88, v168, v88, s[30:31]
	v_cndmask_b32_e64 v73, v168, v73, s[34:35]
	v_cndmask_b32_e64 v89, v168, v89, s[36:37]
	v_cndmask_b32_e64 v74, v168, v74, s[38:39]
	v_cndmask_b32_e64 v90, v168, v90, s[40:41]
	v_cndmask_b32_e64 v75, v168, v75, s[42:43]
	v_cndmask_b32_e64 v91, v168, v91, s[44:45]
	v_cndmask_b32_e64 v76, v168, v76, s[46:47]
	v_cndmask_b32_e64 v92, v168, v92, s[48:49]
	v_cndmask_b32_e64 v77, v168, v77, s[50:51]
	v_cndmask_b32_e64 v93, v168, v93, s[52:53]
	v_cndmask_b32_e64 v78, v168, v78, s[54:55]
	v_cndmask_b32_e64 v94, v168, v94, s[56:57]
	v_cndmask_b32_e64 v79, v168, v79, s[58:59]
	v_cndmask_b32_e64 v95, v168, v95, s[60:61]
	v_cndmask_b32_e64 v80, v168, v80, s[62:63]
	v_cndmask_b32_e64 v96, v168, v96, s[64:65]
	v_cndmask_b32_e64 v81, v168, v81, s[66:67]
	v_cndmask_b32_e64 v97, v168, v97, s[68:69]
	v_cndmask_b32_e64 v82, v168, v82, s[70:71]
	v_cndmask_b32_e64 v98, v168, v98, s[72:73]
	v_cndmask_b32_e64 v83, v168, v83, s[74:75]
	v_cndmask_b32_e64 v99, v168, v99, s[76:77]

.LBB0_2047:
	ds_read_b128 v[212:215], v152 offset:32768
	ds_read_b128 v[216:219], v151 offset:32768
	ds_read_b128 v[220:223], v152 offset:40960
	ds_read_b128 v[224:227], v151 offset:40960
	ds_read_b128 v[228:231], v150 offset:32768
	ds_read_b128 v[232:235], v150 offset:40960
	ds_read_b128 v[236:239], v143 offset:32768
	ds_read_b128 v[240:243], v143 offset:40960
	ds_read_b128 v[244:247], v152 offset:32896
	ds_read_b128 v[248:251], v152 offset:41088
	s_add_i32 s4, s6, s7
	s_cmp_lg_u32 s4, 4
	s_waitcnt lgkmcnt(9)
	v_mfma_f32_32x32x16_bf16 v[68:83], v[212:215], v[100:103], 0
	ds_read_b128 v[212:215], v151 offset:32896
	s_waitcnt lgkmcnt(9)
	v_mfma_f32_32x32x16_bf16 v[68:83], v[216:219], v[108:111], v[68:83]
	ds_read_b128 v[216:219], v151 offset:41088
	s_waitcnt lgkmcnt(9)
	v_mfma_f32_32x32x16_bf16 v[84:99], v[220:223], v[100:103], 0
	ds_read_b128 v[220:223], v150 offset:32896
	s_waitcnt lgkmcnt(9)
	v_mfma_f32_32x32x16_bf16 v[84:99], v[224:227], v[108:111], v[84:99]
	ds_read_b128 v[224:227], v150 offset:41088
	s_waitcnt lgkmcnt(9)
	v_mfma_f32_32x32x16_bf16 v[68:83], v[228:231], v[116:119], v[68:83]
	ds_read_b128 v[228:231], v143 offset:32896
	s_waitcnt lgkmcnt(9)
	v_mfma_f32_32x32x16_bf16 v[84:99], v[232:235], v[116:119], v[84:99]
	ds_read_b128 v[232:235], v143 offset:41088
	s_waitcnt lgkmcnt(9)
	v_mfma_f32_32x32x16_bf16 v[68:83], v[236:239], v[124:127], v[68:83]
	s_waitcnt lgkmcnt(8)
	v_mfma_f32_32x32x16_bf16 v[84:99], v[240:243], v[124:127], v[84:99]
	s_waitcnt lgkmcnt(7)
	v_mfma_f32_32x32x16_bf16 v[68:83], v[244:247], v[104:107], v[68:83]
	s_waitcnt lgkmcnt(6)
	v_mfma_f32_32x32x16_bf16 v[84:99], v[248:251], v[104:107], v[84:99]
	s_waitcnt lgkmcnt(5)
	v_mfma_f32_32x32x16_bf16 v[68:83], v[212:215], v[112:115], v[68:83]
	s_waitcnt lgkmcnt(4)
	v_mfma_f32_32x32x16_bf16 v[84:99], v[216:219], v[112:115], v[84:99]
	s_waitcnt lgkmcnt(3)
	v_mfma_f32_32x32x16_bf16 v[68:83], v[220:223], v[120:123], v[68:83]
	s_waitcnt lgkmcnt(2)
	v_mfma_f32_32x32x16_bf16 v[84:99], v[224:227], v[120:123], v[84:99]
	s_waitcnt lgkmcnt(1)
	v_mfma_f32_32x32x16_bf16 v[68:83], v[228:231], v[128:131], v[68:83]
	s_waitcnt lgkmcnt(0)
	s_nop 0
	v_mfma_f32_32x32x16_bf16 v[84:99], v[232:235], v[128:131], v[84:99]
	s_cbranch_scc1 .LBB0_2049
	s_nop 7
	v_cndmask_b32_e64 v68, v168, v68, s[12:13]
	s_nop 1
	v_cndmask_b32_e64 v84, v168, v84, s[14:15]
	v_cndmask_b32_e64 v69, v168, v69, s[16:17]
	v_cndmask_b32_e64 v85, v168, v85, s[18:19]
	v_cndmask_b32_e64 v70, v168, v70, s[20:21]
	v_cndmask_b32_e64 v86, v168, v86, s[22:23]
	v_cndmask_b32_e64 v71, v168, v71, s[24:25]
	v_cndmask_b32_e64 v87, v168, v87, s[26:27]
	v_cndmask_b32_e64 v72, v168, v72, s[28:29]
	v_cndmask_b32_e64 v88, v168, v88, s[30:31]
	v_cndmask_b32_e64 v73, v168, v73, s[34:35]
	v_cndmask_b32_e64 v89, v168, v89, s[36:37]
	v_cndmask_b32_e64 v74, v168, v74, s[38:39]
	v_cndmask_b32_e64 v90, v168, v90, s[40:41]
	v_cndmask_b32_e64 v75, v168, v75, s[42:43]
	v_cndmask_b32_e64 v91, v168, v91, s[44:45]
	v_cndmask_b32_e64 v76, v168, v76, s[46:47]
	v_cndmask_b32_e64 v92, v168, v92, s[48:49]
	v_cndmask_b32_e64 v77, v168, v77, s[50:51]
	v_cndmask_b32_e64 v93, v168, v93, s[52:53]
	v_cndmask_b32_e64 v78, v168, v78, s[54:55]
	v_cndmask_b32_e64 v94, v168, v94, s[56:57]
	v_cndmask_b32_e64 v79, v168, v79, s[58:59]
	v_cndmask_b32_e64 v95, v168, v95, s[60:61]
	v_cndmask_b32_e64 v80, v168, v80, s[62:63]
	v_cndmask_b32_e64 v96, v168, v96, s[64:65]
	v_cndmask_b32_e64 v81, v168, v81, s[66:67]
	v_cndmask_b32_e64 v97, v168, v97, s[68:69]
	v_cndmask_b32_e64 v82, v168, v82, s[70:71]
	v_cndmask_b32_e64 v98, v168, v98, s[72:73]
	v_cndmask_b32_e64 v83, v168, v83, s[74:75]
	v_cndmask_b32_e64 v99, v168, v99, s[76:77]

.LBB0_2066:
	ds_read_b128 v[212:215], v152 offset:49152
	ds_read_b128 v[216:219], v151 offset:49152
	ds_read_b128 v[220:223], v152 offset:57344
	ds_read_b128 v[224:227], v151 offset:57344
	ds_read_b128 v[228:231], v150 offset:49152
	ds_read_b128 v[232:235], v150 offset:57344
	ds_read_b128 v[236:239], v143 offset:49152
	ds_read_b128 v[240:243], v143 offset:57344
	ds_read_b128 v[244:247], v152 offset:49280
	ds_read_b128 v[248:251], v152 offset:57472
	s_add_i32 s4, s89, s7
	s_cmp_lg_u32 s4, 1
	s_waitcnt lgkmcnt(9)
	v_mfma_f32_32x32x16_bf16 v[68:83], v[212:215], v[100:103], 0
	ds_read_b128 v[212:215], v151 offset:49280
	s_waitcnt lgkmcnt(9)
	v_mfma_f32_32x32x16_bf16 v[68:83], v[216:219], v[108:111], v[68:83]
	ds_read_b128 v[216:219], v151 offset:57472
	s_waitcnt lgkmcnt(9)
	v_mfma_f32_32x32x16_bf16 v[84:99], v[220:223], v[100:103], 0
	ds_read_b128 v[220:223], v150 offset:49280
	s_waitcnt lgkmcnt(9)
	v_mfma_f32_32x32x16_bf16 v[84:99], v[224:227], v[108:111], v[84:99]
	ds_read_b128 v[224:227], v150 offset:57472
	s_waitcnt lgkmcnt(9)
	v_mfma_f32_32x32x16_bf16 v[68:83], v[228:231], v[116:119], v[68:83]
	ds_read_b128 v[228:231], v143 offset:49280
	s_waitcnt lgkmcnt(9)
	v_mfma_f32_32x32x16_bf16 v[84:99], v[232:235], v[116:119], v[84:99]
	ds_read_b128 v[232:235], v143 offset:57472
	s_waitcnt lgkmcnt(9)
	v_mfma_f32_32x32x16_bf16 v[68:83], v[236:239], v[124:127], v[68:83]
	s_waitcnt lgkmcnt(8)
	v_mfma_f32_32x32x16_bf16 v[84:99], v[240:243], v[124:127], v[84:99]
	s_waitcnt lgkmcnt(7)
	v_mfma_f32_32x32x16_bf16 v[68:83], v[244:247], v[104:107], v[68:83]
	s_waitcnt lgkmcnt(6)
	v_mfma_f32_32x32x16_bf16 v[84:99], v[248:251], v[104:107], v[84:99]
	s_waitcnt lgkmcnt(5)
	v_mfma_f32_32x32x16_bf16 v[68:83], v[212:215], v[112:115], v[68:83]
	s_waitcnt lgkmcnt(4)
	v_mfma_f32_32x32x16_bf16 v[84:99], v[216:219], v[112:115], v[84:99]
	s_waitcnt lgkmcnt(3)
	v_mfma_f32_32x32x16_bf16 v[68:83], v[220:223], v[120:123], v[68:83]
	s_waitcnt lgkmcnt(2)
	v_mfma_f32_32x32x16_bf16 v[84:99], v[224:227], v[120:123], v[84:99]
	s_waitcnt lgkmcnt(1)
	v_mfma_f32_32x32x16_bf16 v[68:83], v[228:231], v[128:131], v[68:83]
	s_waitcnt lgkmcnt(0)
	s_nop 0
	v_mfma_f32_32x32x16_bf16 v[84:99], v[232:235], v[128:131], v[84:99]
	s_cbranch_scc1 .LBB0_2068
	s_nop 7
	v_cndmask_b32_e64 v68, v168, v68, s[12:13]
	s_nop 1
	v_cndmask_b32_e64 v84, v168, v84, s[14:15]
	v_cndmask_b32_e64 v69, v168, v69, s[16:17]
	v_cndmask_b32_e64 v85, v168, v85, s[18:19]
	v_cndmask_b32_e64 v70, v168, v70, s[20:21]
	v_cndmask_b32_e64 v86, v168, v86, s[22:23]
	v_cndmask_b32_e64 v71, v168, v71, s[24:25]
	v_cndmask_b32_e64 v87, v168, v87, s[26:27]
	v_cndmask_b32_e64 v72, v168, v72, s[28:29]
	v_cndmask_b32_e64 v88, v168, v88, s[30:31]
	v_cndmask_b32_e64 v73, v168, v73, s[34:35]
	v_cndmask_b32_e64 v89, v168, v89, s[36:37]
	v_cndmask_b32_e64 v74, v168, v74, s[38:39]
	v_cndmask_b32_e64 v90, v168, v90, s[40:41]
	v_cndmask_b32_e64 v75, v168, v75, s[42:43]
	v_cndmask_b32_e64 v91, v168, v91, s[44:45]
	v_cndmask_b32_e64 v76, v168, v76, s[46:47]
	v_cndmask_b32_e64 v92, v168, v92, s[48:49]
	v_cndmask_b32_e64 v77, v168, v77, s[50:51]
	v_cndmask_b32_e64 v93, v168, v93, s[52:53]
	v_cndmask_b32_e64 v78, v168, v78, s[54:55]
	v_cndmask_b32_e64 v94, v168, v94, s[56:57]
	v_cndmask_b32_e64 v79, v168, v79, s[58:59]
	v_cndmask_b32_e64 v95, v168, v95, s[60:61]
	v_cndmask_b32_e64 v80, v168, v80, s[62:63]
	v_cndmask_b32_e64 v96, v168, v96, s[64:65]
	v_cndmask_b32_e64 v81, v168, v81, s[66:67]
	v_cndmask_b32_e64 v97, v168, v97, s[68:69]
	v_cndmask_b32_e64 v82, v168, v82, s[70:71]
	v_cndmask_b32_e64 v98, v168, v98, s[72:73]
	v_cndmask_b32_e64 v83, v168, v83, s[74:75]
	v_cndmask_b32_e64 v99, v168, v99, s[76:77]
